# removed the empty s_setprio 0/1 flip pair between the two 8-MFMA groups of every GEMM compute segment (44 sites)
# speedup vs baseline: 1.0067x; 1.0067x over previous
; #define PG8_STAGE(bufoff, gbase, voff) do { _Pragma("unroll") for (int _i = 0; _i < 2; ++_i) { unsigned vo_ = (voff)[_i]; asm volatile("" : "+v"(vo_));   \
;         __builtin_amdgcn_global_load_lds((const unsigned*)((const char*)(gbase) + vo_), (LAS unsigned*)(lds + (bufoff) + ldsw + _i * 8192), 16, 0, 0); } } while (0)
; #define PG8_LDA(dst, b, h) do { _Pragma("unroll") for (int m = 0; m < 4; ++m) _Pragma("unroll") for (int k = 0; k < 2; ++k) dst[m][k] = *(const LAS bf16x8*)(lds + PG8_SA(b, h) + aoff + m * 2048 + k * 1024); } while (0)
; #define PG8_LDB(dst, b, h) do { _Pragma("unroll") for (int n = 0; n < 2; ++n) _Pragma("unroll") for (int k = 0; k < 2; ++k) dst[n][k] = *(const LAS bf16x8*)(lds + PG8_SB(b, h) + boff + n * 2048 + k * 1024); } while (0)
; #define PG8_WAIT_V(n) asm volatile("s_waitcnt vmcnt(" #n ")" ::: "memory")
; #define PG8_WAIT_L(n) asm volatile("s_waitcnt lgkmcnt(" #n ")" ::: "memory")
; #define PG8_BAR __builtin_amdgcn_s_barrier()
; #define PG8_SCHED __builtin_amdgcn_sched_barrier(0)
; #define PG8_AOFFS(dst, un) do { _Pragma("unroll") for (int _h = 0; _h < 2; ++_h) _Pragma("unroll") for (int _i = 0; _i < 2; ++_i) dst[_h][_i] = S.Aoff(un, _h * HALF + Rr[_i]) + (unsigned)Cc[_i] * 2u; } while (0)
;     ...
;             PG8_LDB(B0, 0, 0); PG8_LDB(B1, 0, 1); PG8_SCHED; PG8_LDA(At, 0, 0); PG8_STAGE(PG8_SA(1, 1), a1, va[1]);
;             PG8_WAIT_V(8); PG8_WAIT_L(0); PG8_BAR; PG8_MMA(0, 0, At, B0); PG8_MMA(0, 1, At, B1); PG8_BAR; PG8_SCHED;
;             if (last && has_next) { PG8_AOFFS(va, nxt); }
;             PG8_LDA(At, 0, 1); PG8_STAGE(PG8_SB(0, 0), b2, voffB); PG8_STAGE(PG8_SB(0, 1), b2 + hstepB, voffB); PG8_STAGE(PG8_SA(0, 0), a2, va[0]);
;             PG8_WAIT_V(8); PG8_WAIT_L(0); PG8_BAR; PG8_MMA(1, 0, At, B0); PG8_MMA(1, 1, At, B1); PG8_BAR; PG8_SCHED;
;             PG8_LDB(B0, 1, 0); PG8_LDB(B1, 1, 1); PG8_SCHED; PG8_LDA(At, 1, 0); PG8_STAGE(PG8_SA(0, 1), a2, va[1]);
;             PG8_WAIT_V(8); PG8_WAIT_L(0); PG8_BAR; PG8_MMA(0, 0, At, B0); PG8_MMA(0, 1, At, B1); PG8_BAR; PG8_SCHED;
.LBB0_571:
	ds_read_b128 v[146:149], v182
	ds_read_b128 v[150:153], v182 offset:1024
	ds_read_b128 v[154:157], v182 offset:2048
	ds_read_b128 v[158:161], v182 offset:3072
	ds_read_b128 v[130:133], v183
	ds_read_b128 v[134:137], v183 offset:1024
	ds_read_b128 v[138:141], v183 offset:2048
	ds_read_b128 v[142:145], v183 offset:3072
	s_cmp_eq_u32 s84, 12
	s_cselect_b64 s[58:59], -1, 0
	s_add_i32 m0, s61, 0xc000
	v_mov_b32_e32 v162, v177
	s_add_u32 s54, s22, s52
	ds_read_b128 v[188:191], v184
	ds_read_b128 v[192:195], v184 offset:1024
	ds_read_b128 v[196:199], v184 offset:2048
	ds_read_b128 v[200:203], v184 offset:3072
	ds_read_b128 v[204:207], v184 offset:4096
	ds_read_b128 v[208:211], v184 offset:5120
	ds_read_b128 v[212:215], v184 offset:6144
	ds_read_b128 v[216:219], v184 offset:7168
	s_addc_u32 s55, s23, s53
	global_load_lds_dwordx4 v162, s[54:55]
	v_mov_b32_e32 v162, v178
	s_add_i32 m0, s61, 0xe000
	s_nop 0
	global_load_lds_dwordx4 v162, s[54:55]
	s_waitcnt vmcnt(8)
	s_waitcnt lgkmcnt(0)
	s_barrier
	s_setprio 1
	s_waitcnt lgkmcnt(0)
	v_mfma_i32_16x16x64_i8 v[126:129], v[146:149], v[188:191], v[126:129]
	v_mfma_i32_16x16x64_i8 v[122:125], v[154:157], v[188:191], v[122:125]
	v_mfma_i32_16x16x64_i8 v[118:121], v[146:149], v[196:199], v[118:121]
	v_mfma_i32_16x16x64_i8 v[114:117], v[154:157], v[196:199], v[114:117]
	v_mfma_i32_16x16x64_i8 v[102:105], v[146:149], v[204:207], v[102:105]
	v_mfma_i32_16x16x64_i8 v[98:101], v[154:157], v[204:207], v[98:101]
	v_mfma_i32_16x16x64_i8 v[86:89], v[146:149], v[212:215], v[86:89]
	v_mfma_i32_16x16x64_i8 v[82:85], v[154:157], v[212:215], v[82:85]
	v_mfma_i32_16x16x64_i8 v[126:129], v[150:153], v[192:195], v[126:129]
	v_mfma_i32_16x16x64_i8 v[122:125], v[158:161], v[192:195], v[122:125]
	v_mfma_i32_16x16x64_i8 v[118:121], v[150:153], v[200:203], v[118:121]
	v_mfma_i32_16x16x64_i8 v[114:117], v[158:161], v[200:203], v[114:117]
	v_mfma_i32_16x16x64_i8 v[102:105], v[150:153], v[208:211], v[102:105]
	v_mfma_i32_16x16x64_i8 v[98:101], v[158:161], v[208:211], v[98:101]
	v_mfma_i32_16x16x64_i8 v[86:89], v[150:153], v[216:219], v[86:89]
	v_mfma_i32_16x16x64_i8 v[82:85], v[158:161], v[216:219], v[82:85]
	v_mfma_i32_16x16x64_i8 v[110:113], v[130:133], v[188:191], v[110:113]
	v_mfma_i32_16x16x64_i8 v[106:109], v[138:141], v[188:191], v[106:109]
	v_mfma_i32_16x16x64_i8 v[94:97], v[130:133], v[196:199], v[94:97]
	v_mfma_i32_16x16x64_i8 v[90:93], v[138:141], v[196:199], v[90:93]
	v_mfma_i32_16x16x64_i8 v[78:81], v[130:133], v[204:207], v[78:81]
	v_mfma_i32_16x16x64_i8 v[74:77], v[138:141], v[204:207], v[74:77]
	v_mfma_i32_16x16x64_i8 v[70:73], v[130:133], v[212:215], v[70:73]
	v_mfma_i32_16x16x64_i8 v[66:69], v[138:141], v[212:215], v[66:69]
	v_mfma_i32_16x16x64_i8 v[110:113], v[134:137], v[192:195], v[110:113]
	v_mfma_i32_16x16x64_i8 v[106:109], v[142:145], v[192:195], v[106:109]
	v_mfma_i32_16x16x64_i8 v[94:97], v[134:137], v[200:203], v[94:97]
	v_mfma_i32_16x16x64_i8 v[90:93], v[142:145], v[200:203], v[90:93]
	v_mfma_i32_16x16x64_i8 v[78:81], v[134:137], v[208:211], v[78:81]
	v_mfma_i32_16x16x64_i8 v[74:77], v[142:145], v[208:211], v[74:77]
	v_mfma_i32_16x16x64_i8 v[70:73], v[134:137], v[216:219], v[70:73]
	v_mfma_i32_16x16x64_i8 v[66:69], v[142:145], v[216:219], v[66:69]
	s_setprio 0
	s_barrier
	s_and_b64 s[54:55], s[48:49], s[58:59]
	s_andn2_b64 vcc, exec, s[54:55]
	s_cbranch_vccnz .LBB0_573
	v_mov_b32_e32 v178, v187
	v_mov_b32_e32 v177, v186
	v_mov_b32_e32 v176, v185
	v_mov_b32_e32 v175, v167
.LBB0_573:
	s_add_u32 s54, s52, 0x100
	s_addc_u32 s55, s53, 0
	s_and_b64 s[56:57], s[58:59], exec
	s_cselect_b32 s56, 0, s54
	s_cselect_b32 s57, 0, s55
	s_add_u32 s56, s2, s56
	s_addc_u32 s57, s3, s57
	s_add_u32 s85, s47, s52
	s_addc_u32 s86, s83, s53
	s_and_b64 s[52:53], s[58:59], exec
	v_mov_b32_e32 v162, v172
	s_mov_b32 m0, s62
	s_cselect_b32 s53, s51, s86
	s_cselect_b32 s52, s50, s85
	ds_read_b128 v[188:191], v184 offset:16384
	ds_read_b128 v[192:195], v184 offset:17408
	ds_read_b128 v[196:199], v184 offset:18432
	ds_read_b128 v[200:203], v184 offset:19456
	ds_read_b128 v[204:207], v184 offset:20480
	ds_read_b128 v[208:211], v184 offset:21504
	ds_read_b128 v[212:215], v184 offset:22528
	ds_read_b128 v[216:219], v184 offset:23552
	s_add_u32 s58, s52, 0x40000
	global_load_lds_dwordx4 v162, s[52:53]
	v_mov_b32_e32 v162, v174
	s_mov_b32 m0, s63
	s_addc_u32 s59, s53, 0
	global_load_lds_dwordx4 v162, s[52:53]
	v_mov_b32_e32 v162, v172
	s_mov_b32 m0, s64
	s_nop 0
	global_load_lds_dwordx4 v162, s[58:59]
	v_mov_b32_e32 v162, v174
	s_mov_b32 m0, s65
	s_nop 0
	global_load_lds_dwordx4 v162, s[58:59]
	v_mov_b32_e32 v162, v175
	s_mov_b32 m0, s61
	s_nop 0
	global_load_lds_dwordx4 v162, s[56:57]
	v_mov_b32_e32 v162, v176
	s_mov_b32 m0, s66
	s_nop 0
	global_load_lds_dwordx4 v162, s[56:57]
	s_waitcnt vmcnt(8)
	s_waitcnt lgkmcnt(0)
	s_barrier
; #define PG8_STAGE(bufoff, gbase, voff) do { _Pragma("unroll") for (int _i = 0; _i < 2; ++_i) { unsigned vo_ = (voff)[_i]; asm volatile("" : "+v"(vo_));   \
;         __builtin_amdgcn_global_load_lds((const unsigned*)((const char*)(gbase) + vo_), (LAS unsigned*)(lds + (bufoff) + ldsw + _i * 8192), 16, 0, 0); } } while (0)
; #define PG8_LDA(dst, b, h) do { _Pragma("unroll") for (int m = 0; m < 4; ++m) _Pragma("unroll") for (int k = 0; k < 2; ++k) dst[m][k] = *(const LAS bf16x8*)(lds + PG8_SA(b, h) + aoff + m * 2048 + k * 1024); } while (0)
; #define PG8_LDB(dst, b, h) do { _Pragma("unroll") for (int n = 0; n < 2; ++n) _Pragma("unroll") for (int k = 0; k < 2; ++k) dst[n][k] = *(const LAS bf16x8*)(lds + PG8_SB(b, h) + boff + n * 2048 + k * 1024); } while (0)
; #define PG8_WAIT_V(n) asm volatile("s_waitcnt vmcnt(" #n ")" ::: "memory")
; #define PG8_WAIT_L(n) asm volatile("s_waitcnt lgkmcnt(" #n ")" ::: "memory")
; #define PG8_BAR __builtin_amdgcn_s_barrier()
; #define PG8_SCHED __builtin_amdgcn_sched_barrier(0)
;     ...
;             PG8_WAIT_V(8); PG8_WAIT_L(0); PG8_BAR; PG8_MMA(1, 0, At, B0); PG8_MMA(1, 1, At, B1); PG8_BAR; PG8_SCHED;
;             PG8_LDB(B0, 1, 0); PG8_LDB(B1, 1, 1); PG8_SCHED; PG8_LDA(At, 1, 0); PG8_STAGE(PG8_SA(0, 1), a2, va[1]);
;             PG8_WAIT_V(8); PG8_WAIT_L(0); PG8_BAR; PG8_MMA(0, 0, At, B0); PG8_MMA(0, 1, At, B1); PG8_BAR; PG8_SCHED;
;             PG8_LDA(At, 1, 1); PG8_STAGE(PG8_SB(1, 0), b3, voffB); PG8_STAGE(PG8_SB(1, 1), b3 + hstepB, voffB); PG8_STAGE(PG8_SA(1, 0), a3, va[0]);
;             PG8_WAIT_V(8); PG8_WAIT_L(0); PG8_BAR; PG8_MMA(1, 0, At, B0); PG8_MMA(1, 1, At, B1); PG8_BAR; PG8_SCHED;
	s_setprio 1
	s_waitcnt lgkmcnt(0)
	v_mfma_i32_16x16x64_i8 v[62:65], v[146:149], v[188:191], v[62:65]
	v_mfma_i32_16x16x64_i8 v[58:61], v[154:157], v[188:191], v[58:61]
	v_mfma_i32_16x16x64_i8 v[46:49], v[146:149], v[196:199], v[46:49]
	v_mfma_i32_16x16x64_i8 v[42:45], v[154:157], v[196:199], v[42:45]
	v_mfma_i32_16x16x64_i8 v[30:33], v[146:149], v[204:207], v[30:33]
	v_mfma_i32_16x16x64_i8 v[26:29], v[154:157], v[204:207], v[26:29]
	v_mfma_i32_16x16x64_i8 v[14:17], v[146:149], v[212:215], v[14:17]
	v_mfma_i32_16x16x64_i8 v[10:13], v[154:157], v[212:215], v[10:13]
	v_mfma_i32_16x16x64_i8 v[62:65], v[150:153], v[192:195], v[62:65]
	v_mfma_i32_16x16x64_i8 v[58:61], v[158:161], v[192:195], v[58:61]
	v_mfma_i32_16x16x64_i8 v[46:49], v[150:153], v[200:203], v[46:49]
	v_mfma_i32_16x16x64_i8 v[42:45], v[158:161], v[200:203], v[42:45]
	v_mfma_i32_16x16x64_i8 v[30:33], v[150:153], v[208:211], v[30:33]
	v_mfma_i32_16x16x64_i8 v[26:29], v[158:161], v[208:211], v[26:29]
	v_mfma_i32_16x16x64_i8 v[14:17], v[150:153], v[216:219], v[14:17]
	v_mfma_i32_16x16x64_i8 v[10:13], v[158:161], v[216:219], v[10:13]
	v_mfma_i32_16x16x64_i8 v[54:57], v[130:133], v[188:191], v[54:57]
	v_mfma_i32_16x16x64_i8 v[50:53], v[138:141], v[188:191], v[50:53]
	v_mfma_i32_16x16x64_i8 v[38:41], v[130:133], v[196:199], v[38:41]
	v_mfma_i32_16x16x64_i8 v[34:37], v[138:141], v[196:199], v[34:37]
	v_mfma_i32_16x16x64_i8 v[22:25], v[130:133], v[204:207], v[22:25]
	v_mfma_i32_16x16x64_i8 v[18:21], v[138:141], v[204:207], v[18:21]
	v_mfma_i32_16x16x64_i8 v[6:9], v[130:133], v[212:215], v[6:9]
	v_mfma_i32_16x16x64_i8 v[2:5], v[138:141], v[212:215], v[2:5]
	v_mfma_i32_16x16x64_i8 v[54:57], v[134:137], v[192:195], v[54:57]
	v_mfma_i32_16x16x64_i8 v[50:53], v[142:145], v[192:195], v[50:53]
	v_mfma_i32_16x16x64_i8 v[38:41], v[134:137], v[200:203], v[38:41]
	v_mfma_i32_16x16x64_i8 v[34:37], v[142:145], v[200:203], v[34:37]
	v_mfma_i32_16x16x64_i8 v[22:25], v[134:137], v[208:211], v[22:25]
	v_mfma_i32_16x16x64_i8 v[18:21], v[142:145], v[208:211], v[18:21]
	v_mfma_i32_16x16x64_i8 v[6:9], v[134:137], v[216:219], v[6:9]
	v_mfma_i32_16x16x64_i8 v[2:5], v[142:145], v[216:219], v[2:5]
	s_setprio 0
	s_barrier
	s_add_i32 s58, 0, 0x18000
	s_add_i32 s59, 0, 0x1c000
	v_add_u32_e32 v142, s58, v180
	v_add_u32_e32 v158, s59, v180
	ds_read_b128 v[130:133], v142
	ds_read_b128 v[134:137], v142 offset:1024
	ds_read_b128 v[138:141], v142 offset:2048
	ds_read_b128 v[142:145], v142 offset:3072
	ds_read_b128 v[146:149], v158
	ds_read_b128 v[150:153], v158 offset:1024
	ds_read_b128 v[154:157], v158 offset:2048
	ds_read_b128 v[158:161], v158 offset:3072
	v_mov_b32_e32 v162, v177
	s_mov_b32 m0, s67
	ds_read_b128 v[188:191], v184 offset:32768
	ds_read_b128 v[192:195], v184 offset:33792
	ds_read_b128 v[196:199], v184 offset:34816
	ds_read_b128 v[200:203], v184 offset:35840
	ds_read_b128 v[204:207], v184 offset:36864
	ds_read_b128 v[208:211], v184 offset:37888
	ds_read_b128 v[212:215], v184 offset:38912
	ds_read_b128 v[216:219], v184 offset:39936
	s_nop 0
	global_load_lds_dwordx4 v162, s[56:57]
	v_mov_b32_e32 v162, v178
	s_mov_b32 m0, s68
	s_nop 0
	global_load_lds_dwordx4 v162, s[56:57]
	s_waitcnt vmcnt(8)
	s_waitcnt lgkmcnt(0)
	s_barrier
	s_setprio 1
	s_waitcnt lgkmcnt(0)
	v_mfma_i32_16x16x64_i8 v[126:129], v[130:133], v[188:191], v[126:129]
	v_mfma_i32_16x16x64_i8 v[122:125], v[138:141], v[188:191], v[122:125]
	v_mfma_i32_16x16x64_i8 v[118:121], v[130:133], v[196:199], v[118:121]
	v_mfma_i32_16x16x64_i8 v[114:117], v[138:141], v[196:199], v[114:117]
	v_mfma_i32_16x16x64_i8 v[102:105], v[130:133], v[204:207], v[102:105]
	v_mfma_i32_16x16x64_i8 v[98:101], v[138:141], v[204:207], v[98:101]
	v_mfma_i32_16x16x64_i8 v[86:89], v[130:133], v[212:215], v[86:89]
	v_mfma_i32_16x16x64_i8 v[82:85], v[138:141], v[212:215], v[82:85]
	v_mfma_i32_16x16x64_i8 v[126:129], v[134:137], v[192:195], v[126:129]
	v_mfma_i32_16x16x64_i8 v[122:125], v[142:145], v[192:195], v[122:125]
	v_mfma_i32_16x16x64_i8 v[118:121], v[134:137], v[200:203], v[118:121]
	v_mfma_i32_16x16x64_i8 v[114:117], v[142:145], v[200:203], v[114:117]
	v_mfma_i32_16x16x64_i8 v[102:105], v[134:137], v[208:211], v[102:105]
	v_mfma_i32_16x16x64_i8 v[98:101], v[142:145], v[208:211], v[98:101]
	v_mfma_i32_16x16x64_i8 v[86:89], v[134:137], v[216:219], v[86:89]
	v_mfma_i32_16x16x64_i8 v[82:85], v[142:145], v[216:219], v[82:85]
	v_mfma_i32_16x16x64_i8 v[110:113], v[146:149], v[188:191], v[110:113]
	v_mfma_i32_16x16x64_i8 v[106:109], v[154:157], v[188:191], v[106:109]
	v_mfma_i32_16x16x64_i8 v[94:97], v[146:149], v[196:199], v[94:97]
	v_mfma_i32_16x16x64_i8 v[90:93], v[154:157], v[196:199], v[90:93]
	v_mfma_i32_16x16x64_i8 v[78:81], v[146:149], v[204:207], v[78:81]
	v_mfma_i32_16x16x64_i8 v[74:77], v[154:157], v[204:207], v[74:77]
	v_mfma_i32_16x16x64_i8 v[70:73], v[146:149], v[212:215], v[70:73]
	v_mfma_i32_16x16x64_i8 v[66:69], v[154:157], v[212:215], v[66:69]
	v_mfma_i32_16x16x64_i8 v[110:113], v[150:153], v[192:195], v[110:113]
	v_mfma_i32_16x16x64_i8 v[106:109], v[158:161], v[192:195], v[106:109]
	v_mfma_i32_16x16x64_i8 v[94:97], v[150:153], v[200:203], v[94:97]
	v_mfma_i32_16x16x64_i8 v[90:93], v[158:161], v[200:203], v[90:93]
	v_mfma_i32_16x16x64_i8 v[78:81], v[150:153], v[208:211], v[78:81]
	v_mfma_i32_16x16x64_i8 v[74:77], v[158:161], v[208:211], v[74:77]
	v_mfma_i32_16x16x64_i8 v[70:73], v[150:153], v[216:219], v[70:73]
	v_mfma_i32_16x16x64_i8 v[66:69], v[158:161], v[216:219], v[66:69]
	s_setprio 0
	s_barrier
; #define PG8_STAGE(bufoff, gbase, voff) do { _Pragma("unroll") for (int _i = 0; _i < 2; ++_i) { unsigned vo_ = (voff)[_i]; asm volatile("" : "+v"(vo_));   \
;         __builtin_amdgcn_global_load_lds((const unsigned*)((const char*)(gbase) + vo_), (LAS unsigned*)(lds + (bufoff) + ldsw + _i * 8192), 16, 0, 0); } } while (0)
; #define PG8_LDA(dst, b, h) do { _Pragma("unroll") for (int m = 0; m < 4; ++m) _Pragma("unroll") for (int k = 0; k < 2; ++k) dst[m][k] = *(const LAS bf16x8*)(lds + PG8_SA(b, h) + aoff + m * 2048 + k * 1024); } while (0)
; #define PG8_WAIT_V(n) asm volatile("s_waitcnt vmcnt(" #n ")" ::: "memory")
; #define PG8_WAIT_L(n) asm volatile("s_waitcnt lgkmcnt(" #n ")" ::: "memory")
; #define PG8_BAR __builtin_amdgcn_s_barrier()
; #define PG8_SCHED __builtin_amdgcn_sched_barrier(0)
;     ...
;             PG8_LDA(At, 1, 1); PG8_STAGE(PG8_SB(1, 0), b3, voffB); PG8_STAGE(PG8_SB(1, 1), b3 + hstepB, voffB); PG8_STAGE(PG8_SA(1, 0), a3, va[0]);
;             PG8_WAIT_V(8); PG8_WAIT_L(0); PG8_BAR; PG8_MMA(1, 0, At, B0); PG8_MMA(1, 1, At, B1); PG8_BAR; PG8_SCHED;
;         }
	v_mov_b32_e32 v162, v172
	ds_read_b128 v[188:191], v184 offset:49152
	ds_read_b128 v[192:195], v184 offset:50176
	ds_read_b128 v[196:199], v184 offset:51200
	ds_read_b128 v[200:203], v184 offset:52224
	ds_read_b128 v[204:207], v184 offset:53248
	ds_read_b128 v[208:211], v184 offset:54272
	ds_read_b128 v[212:215], v184 offset:55296
	ds_read_b128 v[216:219], v184 offset:56320
	s_add_i32 s58, s58, s38
	v_lshl_add_u64 v[220:221], s[52:53], 0, v[162:163]
	v_lshl_add_u64 v[220:221], v[220:221], 0, s[20:21]
	s_mov_b32 m0, s58
	v_mov_b32_e32 v162, v174
	global_load_lds_dwordx4 v[220:221], off
	s_add_i32 m0, s58, 0x2000
	s_nop 0
	v_lshl_add_u64 v[220:221], s[52:53], 0, v[162:163]
	s_add_u32 s52, s52, 0x40080
	v_lshl_add_u64 v[220:221], v[220:221], 0, s[20:21]
	s_addc_u32 s53, s53, 0
	v_mov_b32_e32 v162, v172
	s_add_i32 s58, s59, s38
	global_load_lds_dwordx4 v[220:221], off
	s_mov_b32 m0, s58
	s_nop 0
	global_load_lds_dwordx4 v162, s[52:53]
	v_mov_b32_e32 v162, v174
	s_add_i32 m0, s58, 0x2000
	s_nop 0
	global_load_lds_dwordx4 v162, s[52:53]
	v_mov_b32_e32 v162, v175
	s_mov_b32 m0, s71
	v_lshl_add_u64 v[220:221], s[56:57], 0, v[162:163]
	v_lshl_add_u64 v[220:221], v[220:221], 0, s[20:21]
	v_mov_b32_e32 v162, v176
	global_load_lds_dwordx4 v[220:221], off
	s_mov_b32 m0, s72
	v_lshl_add_u64 v[220:221], s[56:57], 0, v[162:163]
	v_lshl_add_u64 v[220:221], v[220:221], 0, s[20:21]
	global_load_lds_dwordx4 v[220:221], off
	s_waitcnt vmcnt(8)
	s_waitcnt lgkmcnt(0)
	s_barrier
	s_setprio 1
	s_waitcnt lgkmcnt(0)
	v_mfma_i32_16x16x64_i8 v[62:65], v[130:133], v[188:191], v[62:65]
	v_mfma_i32_16x16x64_i8 v[58:61], v[138:141], v[188:191], v[58:61]
	v_mfma_i32_16x16x64_i8 v[46:49], v[130:133], v[196:199], v[46:49]
	v_mfma_i32_16x16x64_i8 v[42:45], v[138:141], v[196:199], v[42:45]
	v_mfma_i32_16x16x64_i8 v[30:33], v[130:133], v[204:207], v[30:33]
	v_mfma_i32_16x16x64_i8 v[26:29], v[138:141], v[204:207], v[26:29]
	v_mfma_i32_16x16x64_i8 v[14:17], v[130:133], v[212:215], v[14:17]
	v_mfma_i32_16x16x64_i8 v[10:13], v[138:141], v[212:215], v[10:13]
	v_mfma_i32_16x16x64_i8 v[62:65], v[134:137], v[192:195], v[62:65]
	v_mfma_i32_16x16x64_i8 v[58:61], v[142:145], v[192:195], v[58:61]
	v_mfma_i32_16x16x64_i8 v[46:49], v[134:137], v[200:203], v[46:49]
	v_mfma_i32_16x16x64_i8 v[42:45], v[142:145], v[200:203], v[42:45]
	v_mfma_i32_16x16x64_i8 v[30:33], v[134:137], v[208:211], v[30:33]
	v_mfma_i32_16x16x64_i8 v[26:29], v[142:145], v[208:211], v[26:29]
	v_mfma_i32_16x16x64_i8 v[14:17], v[134:137], v[216:219], v[14:17]
	v_mfma_i32_16x16x64_i8 v[10:13], v[142:145], v[216:219], v[10:13]
	v_mfma_i32_16x16x64_i8 v[54:57], v[146:149], v[188:191], v[54:57]
	v_mfma_i32_16x16x64_i8 v[50:53], v[154:157], v[188:191], v[50:53]
	v_mfma_i32_16x16x64_i8 v[38:41], v[146:149], v[196:199], v[38:41]
	v_mfma_i32_16x16x64_i8 v[34:37], v[154:157], v[196:199], v[34:37]
	v_mfma_i32_16x16x64_i8 v[22:25], v[146:149], v[204:207], v[22:25]
	v_mfma_i32_16x16x64_i8 v[18:21], v[154:157], v[204:207], v[18:21]
	v_mfma_i32_16x16x64_i8 v[6:9], v[146:149], v[212:215], v[6:9]
	v_mfma_i32_16x16x64_i8 v[2:5], v[154:157], v[212:215], v[2:5]
	v_mfma_i32_16x16x64_i8 v[54:57], v[150:153], v[192:195], v[54:57]
	v_mfma_i32_16x16x64_i8 v[50:53], v[158:161], v[192:195], v[50:53]
	v_mfma_i32_16x16x64_i8 v[38:41], v[150:153], v[200:203], v[38:41]
	v_mfma_i32_16x16x64_i8 v[34:37], v[158:161], v[200:203], v[34:37]
	v_mfma_i32_16x16x64_i8 v[22:25], v[150:153], v[208:211], v[22:25]
	v_mfma_i32_16x16x64_i8 v[18:21], v[158:161], v[208:211], v[18:21]
	v_mfma_i32_16x16x64_i8 v[6:9], v[150:153], v[216:219], v[6:9]
	v_mfma_i32_16x16x64_i8 v[2:5], v[158:161], v[216:219], v[2:5]
	s_setprio 0
	s_barrier
	s_add_i32 s84, s84, 2
	s_cmp_gt_u32 s84, 13
	s_cbranch_scc1 .LBB0_575
	s_mov_b64 s[52:53], s[54:55]
	s_branch .LBB0_571

; #define PG8_STAGE(bufoff, gbase, voff) do { _Pragma("unroll") for (int _i = 0; _i < 2; ++_i) { unsigned vo_ = (voff)[_i]; asm volatile("" : "+v"(vo_));   \
;         __builtin_amdgcn_global_load_lds((const unsigned*)((const char*)(gbase) + vo_), (LAS unsigned*)(lds + (bufoff) + ldsw + _i * 8192), 16, 0, 0); } } while (0)
; #define PG8_LDA(dst, b, h) do { _Pragma("unroll") for (int m = 0; m < 4; ++m) _Pragma("unroll") for (int k = 0; k < 2; ++k) dst[m][k] = *(const LAS bf16x8*)(lds + PG8_SA(b, h) + aoff + m * 2048 + k * 1024); } while (0)
; #define PG8_LDB(dst, b, h) do { _Pragma("unroll") for (int n = 0; n < 2; ++n) _Pragma("unroll") for (int k = 0; k < 2; ++k) dst[n][k] = *(const LAS bf16x8*)(lds + PG8_SB(b, h) + boff + n * 2048 + k * 1024); } while (0)
; #define PG8_WAIT_V(n) asm volatile("s_waitcnt vmcnt(" #n ")" ::: "memory")
; #define PG8_WAIT_L(n) asm volatile("s_waitcnt lgkmcnt(" #n ")" ::: "memory")
; #define PG8_BAR __builtin_amdgcn_s_barrier()
; #define PG8_SCHED __builtin_amdgcn_sched_barrier(0)
; #define PG8_AOFFS(dst, un) do { _Pragma("unroll") for (int _h = 0; _h < 2; ++_h) _Pragma("unroll") for (int _i = 0; _i < 2; ++_i) dst[_h][_i] = S.Aoff(un, _h * HALF + Rr[_i]) + (unsigned)Cc[_i] * 2u; } while (0)
;     ...
;             PG8_LDB(B0, 0, 0); PG8_LDB(B1, 0, 1); PG8_SCHED; PG8_LDA(At, 0, 0); PG8_STAGE(PG8_SA(1, 1), a1, va[1]);
;             PG8_WAIT_V(8); PG8_WAIT_L(0); PG8_BAR; PG8_MMA(0, 0, At, B0); PG8_MMA(0, 1, At, B1); PG8_BAR; PG8_SCHED;
;             if (last && has_next) { PG8_AOFFS(va, nxt); }
;             PG8_LDA(At, 0, 1); PG8_STAGE(PG8_SB(0, 0), b2, voffB); PG8_STAGE(PG8_SB(0, 1), b2 + hstepB, voffB); PG8_STAGE(PG8_SA(0, 0), a2, va[0]);
;             PG8_WAIT_V(8); PG8_WAIT_L(0); PG8_BAR; PG8_MMA(1, 0, At, B0); PG8_MMA(1, 1, At, B1); PG8_BAR; PG8_SCHED;
;             PG8_LDB(B0, 1, 0); PG8_LDB(B1, 1, 1); PG8_SCHED; PG8_LDA(At, 1, 0); PG8_STAGE(PG8_SA(0, 1), a2, va[1]);
;             PG8_WAIT_V(8); PG8_WAIT_L(0); PG8_BAR; PG8_MMA(0, 0, At, B0); PG8_MMA(0, 1, At, B1); PG8_BAR; PG8_SCHED;
.LBB0_1201:
	ds_read_b128 v[146:149], v200
	ds_read_b128 v[150:153], v200 offset:1024
	ds_read_b128 v[154:157], v200 offset:2048
	ds_read_b128 v[158:161], v200 offset:3072
	ds_read_b128 v[130:133], v201
	ds_read_b128 v[134:137], v201 offset:1024
	ds_read_b128 v[138:141], v201 offset:2048
	ds_read_b128 v[142:145], v201 offset:3072
	s_cmp_eq_u32 s27, 28
	s_cselect_b64 s[40:41], -1, 0
	s_add_i32 m0, s43, 0xc000
	v_mov_b32_e32 v166, v196
	s_add_u32 s30, s16, s28
	ds_read_b128 v[208:211], v202
	ds_read_b128 v[212:215], v202 offset:1024
	ds_read_b128 v[216:219], v202 offset:2048
	ds_read_b128 v[220:223], v202 offset:3072
	ds_read_b128 v[224:227], v202 offset:4096
	ds_read_b128 v[228:231], v202 offset:5120
	ds_read_b128 v[232:235], v202 offset:6144
	ds_read_b128 v[236:239], v202 offset:7168
	s_addc_u32 s31, s17, s29
	global_load_lds_dwordx4 v166, s[30:31]
	v_mov_b32_e32 v166, v197
	s_add_i32 m0, s43, 0xe000
	s_nop 0
	global_load_lds_dwordx4 v166, s[30:31]
	s_waitcnt vmcnt(8)
	s_waitcnt lgkmcnt(0)
	s_barrier
	s_setprio 1
	s_waitcnt lgkmcnt(0)
	v_mfma_f32_16x16x32_bf16 v[126:129], v[146:149], v[208:211], v[126:129]
	v_mfma_f32_16x16x32_bf16 v[122:125], v[154:157], v[208:211], v[122:125]
	v_mfma_f32_16x16x32_bf16 v[114:117], v[146:149], v[216:219], v[114:117]
	v_mfma_f32_16x16x32_bf16 v[106:109], v[154:157], v[216:219], v[106:109]
	v_mfma_f32_16x16x32_bf16 v[98:101], v[146:149], v[224:227], v[98:101]
	v_mfma_f32_16x16x32_bf16 v[90:93], v[154:157], v[224:227], v[90:93]
	v_mfma_f32_16x16x32_bf16 v[82:85], v[146:149], v[232:235], v[82:85]
	v_mfma_f32_16x16x32_bf16 v[74:77], v[154:157], v[232:235], v[74:77]
	v_mfma_f32_16x16x32_bf16 v[126:129], v[150:153], v[212:215], v[126:129]
	v_mfma_f32_16x16x32_bf16 v[122:125], v[158:161], v[212:215], v[122:125]
	v_mfma_f32_16x16x32_bf16 v[114:117], v[150:153], v[220:223], v[114:117]
	v_mfma_f32_16x16x32_bf16 v[106:109], v[158:161], v[220:223], v[106:109]
	v_mfma_f32_16x16x32_bf16 v[98:101], v[150:153], v[228:231], v[98:101]
	v_mfma_f32_16x16x32_bf16 v[90:93], v[158:161], v[228:231], v[90:93]
	v_mfma_f32_16x16x32_bf16 v[82:85], v[150:153], v[236:239], v[82:85]
	v_mfma_f32_16x16x32_bf16 v[74:77], v[158:161], v[236:239], v[74:77]
	v_mfma_f32_16x16x32_bf16 v[118:121], v[130:133], v[208:211], v[118:121]
	v_mfma_f32_16x16x32_bf16 v[110:113], v[138:141], v[208:211], v[110:113]
	v_mfma_f32_16x16x32_bf16 v[102:105], v[130:133], v[216:219], v[102:105]
	v_mfma_f32_16x16x32_bf16 v[94:97], v[138:141], v[216:219], v[94:97]
	v_mfma_f32_16x16x32_bf16 v[86:89], v[130:133], v[224:227], v[86:89]
	v_mfma_f32_16x16x32_bf16 v[78:81], v[138:141], v[224:227], v[78:81]
	v_mfma_f32_16x16x32_bf16 v[70:73], v[130:133], v[232:235], v[70:73]
	v_mfma_f32_16x16x32_bf16 v[66:69], v[138:141], v[232:235], v[66:69]
	v_mfma_f32_16x16x32_bf16 v[118:121], v[134:137], v[212:215], v[118:121]
	v_mfma_f32_16x16x32_bf16 v[110:113], v[142:145], v[212:215], v[110:113]
	v_mfma_f32_16x16x32_bf16 v[102:105], v[134:137], v[220:223], v[102:105]
	v_mfma_f32_16x16x32_bf16 v[94:97], v[142:145], v[220:223], v[94:97]
	v_mfma_f32_16x16x32_bf16 v[86:89], v[134:137], v[228:231], v[86:89]
	v_mfma_f32_16x16x32_bf16 v[78:81], v[142:145], v[228:231], v[78:81]
	v_mfma_f32_16x16x32_bf16 v[70:73], v[134:137], v[236:239], v[70:73]
	v_mfma_f32_16x16x32_bf16 v[66:69], v[142:145], v[236:239], v[66:69]
	s_setprio 0
	s_barrier
	s_and_b64 s[30:31], s[22:23], s[40:41]
	s_andn2_b64 vcc, exec, s[30:31]
	s_cbranch_vccnz .LBB0_1203
	v_mov_b32_e32 v197, v206
	v_mov_b32_e32 v196, v205
	v_mov_b32_e32 v195, v204
	v_mov_b32_e32 v194, v203
.LBB0_1203:
	s_add_u32 s30, s28, 0x100
	s_addc_u32 s31, s29, 0
	s_and_b64 s[34:35], s[40:41], exec
	s_cselect_b32 s34, 0, s30
	s_cselect_b32 s35, 0, s31
	s_add_u32 s34, s4, s34
	s_addc_u32 s35, s5, s35
	s_add_u32 s62, s6, s28
	s_addc_u32 s63, s21, s29
	s_and_b64 s[28:29], s[40:41], exec
	v_mov_b32_e32 v166, v187
	s_mov_b32 m0, s44
	s_cselect_b32 s29, s25, s63
	s_cselect_b32 s28, s24, s62
	ds_read_b128 v[208:211], v202 offset:16384
	ds_read_b128 v[212:215], v202 offset:17408
	ds_read_b128 v[216:219], v202 offset:18432
	ds_read_b128 v[220:223], v202 offset:19456
	ds_read_b128 v[224:227], v202 offset:20480
	ds_read_b128 v[228:231], v202 offset:21504
	ds_read_b128 v[232:235], v202 offset:22528
	ds_read_b128 v[236:239], v202 offset:23552
	s_add_u32 s40, s28, 0x80000
	global_load_lds_dwordx4 v166, s[28:29]
	v_mov_b32_e32 v166, v189
	s_mov_b32 m0, s45
	s_addc_u32 s41, s29, 0
	global_load_lds_dwordx4 v166, s[28:29]
	v_mov_b32_e32 v166, v187
	s_mov_b32 m0, s46
	s_nop 0
	global_load_lds_dwordx4 v166, s[40:41]
	v_mov_b32_e32 v166, v189
	s_mov_b32 m0, s47
	s_nop 0
	global_load_lds_dwordx4 v166, s[40:41]
	v_mov_b32_e32 v166, v194
	s_mov_b32 m0, s43
	s_nop 0
	global_load_lds_dwordx4 v166, s[34:35]
	v_mov_b32_e32 v166, v195
	s_mov_b32 m0, s48
	s_nop 0
	global_load_lds_dwordx4 v166, s[34:35]
	s_waitcnt vmcnt(8)
	s_waitcnt lgkmcnt(0)
	s_barrier
; #define PG8_STAGE(bufoff, gbase, voff) do { _Pragma("unroll") for (int _i = 0; _i < 2; ++_i) { unsigned vo_ = (voff)[_i]; asm volatile("" : "+v"(vo_));   \
;         __builtin_amdgcn_global_load_lds((const unsigned*)((const char*)(gbase) + vo_), (LAS unsigned*)(lds + (bufoff) + ldsw + _i * 8192), 16, 0, 0); } } while (0)
; #define PG8_LDA(dst, b, h) do { _Pragma("unroll") for (int m = 0; m < 4; ++m) _Pragma("unroll") for (int k = 0; k < 2; ++k) dst[m][k] = *(const LAS bf16x8*)(lds + PG8_SA(b, h) + aoff + m * 2048 + k * 1024); } while (0)
; #define PG8_LDB(dst, b, h) do { _Pragma("unroll") for (int n = 0; n < 2; ++n) _Pragma("unroll") for (int k = 0; k < 2; ++k) dst[n][k] = *(const LAS bf16x8*)(lds + PG8_SB(b, h) + boff + n * 2048 + k * 1024); } while (0)
; #define PG8_WAIT_V(n) asm volatile("s_waitcnt vmcnt(" #n ")" ::: "memory")
; #define PG8_WAIT_L(n) asm volatile("s_waitcnt lgkmcnt(" #n ")" ::: "memory")
; #define PG8_BAR __builtin_amdgcn_s_barrier()
; #define PG8_SCHED __builtin_amdgcn_sched_barrier(0)
;     ...
;             PG8_WAIT_V(8); PG8_WAIT_L(0); PG8_BAR; PG8_MMA(1, 0, At, B0); PG8_MMA(1, 1, At, B1); PG8_BAR; PG8_SCHED;
;             PG8_LDB(B0, 1, 0); PG8_LDB(B1, 1, 1); PG8_SCHED; PG8_LDA(At, 1, 0); PG8_STAGE(PG8_SA(0, 1), a2, va[1]);
;             PG8_WAIT_V(8); PG8_WAIT_L(0); PG8_BAR; PG8_MMA(0, 0, At, B0); PG8_MMA(0, 1, At, B1); PG8_BAR; PG8_SCHED;
;             PG8_LDA(At, 1, 1); PG8_STAGE(PG8_SB(1, 0), b3, voffB); PG8_STAGE(PG8_SB(1, 1), b3 + hstepB, voffB); PG8_STAGE(PG8_SA(1, 0), a3, va[0]);
;             PG8_WAIT_V(8); PG8_WAIT_L(0); PG8_BAR; PG8_MMA(1, 0, At, B0); PG8_MMA(1, 1, At, B1); PG8_BAR; PG8_SCHED;
	s_setprio 1
	s_waitcnt lgkmcnt(0)
	v_mfma_f32_16x16x32_bf16 v[62:65], v[146:149], v[208:211], v[62:65]
	v_mfma_f32_16x16x32_bf16 v[58:61], v[154:157], v[208:211], v[58:61]
	v_mfma_f32_16x16x32_bf16 v[50:53], v[146:149], v[216:219], v[50:53]
	v_mfma_f32_16x16x32_bf16 v[42:45], v[154:157], v[216:219], v[42:45]
	v_mfma_f32_16x16x32_bf16 v[34:37], v[146:149], v[224:227], v[34:37]
	v_mfma_f32_16x16x32_bf16 v[26:29], v[154:157], v[224:227], v[26:29]
	v_mfma_f32_16x16x32_bf16 v[18:21], v[146:149], v[232:235], v[18:21]
	v_mfma_f32_16x16x32_bf16 v[10:13], v[154:157], v[232:235], v[10:13]
	v_mfma_f32_16x16x32_bf16 v[62:65], v[150:153], v[212:215], v[62:65]
	v_mfma_f32_16x16x32_bf16 v[58:61], v[158:161], v[212:215], v[58:61]
	v_mfma_f32_16x16x32_bf16 v[50:53], v[150:153], v[220:223], v[50:53]
	v_mfma_f32_16x16x32_bf16 v[42:45], v[158:161], v[220:223], v[42:45]
	v_mfma_f32_16x16x32_bf16 v[34:37], v[150:153], v[228:231], v[34:37]
	v_mfma_f32_16x16x32_bf16 v[26:29], v[158:161], v[228:231], v[26:29]
	v_mfma_f32_16x16x32_bf16 v[18:21], v[150:153], v[236:239], v[18:21]
	v_mfma_f32_16x16x32_bf16 v[10:13], v[158:161], v[236:239], v[10:13]
	v_mfma_f32_16x16x32_bf16 v[54:57], v[130:133], v[208:211], v[54:57]
	v_mfma_f32_16x16x32_bf16 v[46:49], v[138:141], v[208:211], v[46:49]
	v_mfma_f32_16x16x32_bf16 v[38:41], v[130:133], v[216:219], v[38:41]
	v_mfma_f32_16x16x32_bf16 v[30:33], v[138:141], v[216:219], v[30:33]
	v_mfma_f32_16x16x32_bf16 v[22:25], v[130:133], v[224:227], v[22:25]
	v_mfma_f32_16x16x32_bf16 v[14:17], v[138:141], v[224:227], v[14:17]
	v_mfma_f32_16x16x32_bf16 v[6:9], v[130:133], v[232:235], v[6:9]
	v_mfma_f32_16x16x32_bf16 v[2:5], v[138:141], v[232:235], v[2:5]
	v_mfma_f32_16x16x32_bf16 v[54:57], v[134:137], v[212:215], v[54:57]
	v_mfma_f32_16x16x32_bf16 v[46:49], v[142:145], v[212:215], v[46:49]
	v_mfma_f32_16x16x32_bf16 v[38:41], v[134:137], v[220:223], v[38:41]
	v_mfma_f32_16x16x32_bf16 v[30:33], v[142:145], v[220:223], v[30:33]
	v_mfma_f32_16x16x32_bf16 v[22:25], v[134:137], v[228:231], v[22:25]
	v_mfma_f32_16x16x32_bf16 v[14:17], v[142:145], v[228:231], v[14:17]
	v_mfma_f32_16x16x32_bf16 v[6:9], v[134:137], v[236:239], v[6:9]
	v_mfma_f32_16x16x32_bf16 v[2:5], v[142:145], v[236:239], v[2:5]
	s_setprio 0
	s_barrier
	s_add_i32 s40, 0, 0x18000
	s_add_i32 s41, 0, 0x1c000
	v_add_u32_e32 v142, s40, v198
	v_add_u32_e32 v158, s41, v198
	ds_read_b128 v[130:133], v142
	ds_read_b128 v[134:137], v142 offset:1024
	ds_read_b128 v[138:141], v142 offset:2048
	ds_read_b128 v[142:145], v142 offset:3072
	ds_read_b128 v[146:149], v158
	ds_read_b128 v[150:153], v158 offset:1024
	ds_read_b128 v[154:157], v158 offset:2048
	ds_read_b128 v[158:161], v158 offset:3072
	v_mov_b32_e32 v166, v196
	s_mov_b32 m0, s49
	ds_read_b128 v[208:211], v202 offset:32768
	ds_read_b128 v[212:215], v202 offset:33792
	ds_read_b128 v[216:219], v202 offset:34816
	ds_read_b128 v[220:223], v202 offset:35840
	ds_read_b128 v[224:227], v202 offset:36864
	ds_read_b128 v[228:231], v202 offset:37888
	ds_read_b128 v[232:235], v202 offset:38912
	ds_read_b128 v[236:239], v202 offset:39936
	s_nop 0
	global_load_lds_dwordx4 v166, s[34:35]
	v_mov_b32_e32 v166, v197
	s_mov_b32 m0, s50
	s_nop 0
	global_load_lds_dwordx4 v166, s[34:35]
	s_waitcnt vmcnt(8)
	s_waitcnt lgkmcnt(0)
	s_barrier
	s_setprio 1
	s_waitcnt lgkmcnt(0)
	v_mfma_f32_16x16x32_bf16 v[126:129], v[130:133], v[208:211], v[126:129]
	v_mfma_f32_16x16x32_bf16 v[122:125], v[138:141], v[208:211], v[122:125]
	v_mfma_f32_16x16x32_bf16 v[114:117], v[130:133], v[216:219], v[114:117]
	v_mfma_f32_16x16x32_bf16 v[106:109], v[138:141], v[216:219], v[106:109]
	v_mfma_f32_16x16x32_bf16 v[98:101], v[130:133], v[224:227], v[98:101]
	v_mfma_f32_16x16x32_bf16 v[90:93], v[138:141], v[224:227], v[90:93]
	v_mfma_f32_16x16x32_bf16 v[82:85], v[130:133], v[232:235], v[82:85]
	v_mfma_f32_16x16x32_bf16 v[74:77], v[138:141], v[232:235], v[74:77]
	v_mfma_f32_16x16x32_bf16 v[126:129], v[134:137], v[212:215], v[126:129]
	v_mfma_f32_16x16x32_bf16 v[122:125], v[142:145], v[212:215], v[122:125]
	v_mfma_f32_16x16x32_bf16 v[114:117], v[134:137], v[220:223], v[114:117]
	v_mfma_f32_16x16x32_bf16 v[106:109], v[142:145], v[220:223], v[106:109]
	v_mfma_f32_16x16x32_bf16 v[98:101], v[134:137], v[228:231], v[98:101]
	v_mfma_f32_16x16x32_bf16 v[90:93], v[142:145], v[228:231], v[90:93]
	v_mfma_f32_16x16x32_bf16 v[82:85], v[134:137], v[236:239], v[82:85]
	v_mfma_f32_16x16x32_bf16 v[74:77], v[142:145], v[236:239], v[74:77]
	v_mfma_f32_16x16x32_bf16 v[118:121], v[146:149], v[208:211], v[118:121]
	v_mfma_f32_16x16x32_bf16 v[110:113], v[154:157], v[208:211], v[110:113]
	v_mfma_f32_16x16x32_bf16 v[102:105], v[146:149], v[216:219], v[102:105]
	v_mfma_f32_16x16x32_bf16 v[94:97], v[154:157], v[216:219], v[94:97]
	v_mfma_f32_16x16x32_bf16 v[86:89], v[146:149], v[224:227], v[86:89]
	v_mfma_f32_16x16x32_bf16 v[78:81], v[154:157], v[224:227], v[78:81]
	v_mfma_f32_16x16x32_bf16 v[70:73], v[146:149], v[232:235], v[70:73]
	v_mfma_f32_16x16x32_bf16 v[66:69], v[154:157], v[232:235], v[66:69]
	v_mfma_f32_16x16x32_bf16 v[118:121], v[150:153], v[212:215], v[118:121]
	v_mfma_f32_16x16x32_bf16 v[110:113], v[158:161], v[212:215], v[110:113]
	v_mfma_f32_16x16x32_bf16 v[102:105], v[150:153], v[220:223], v[102:105]
	v_mfma_f32_16x16x32_bf16 v[94:97], v[158:161], v[220:223], v[94:97]
	v_mfma_f32_16x16x32_bf16 v[86:89], v[150:153], v[228:231], v[86:89]
	v_mfma_f32_16x16x32_bf16 v[78:81], v[158:161], v[228:231], v[78:81]
	v_mfma_f32_16x16x32_bf16 v[70:73], v[150:153], v[236:239], v[70:73]
	v_mfma_f32_16x16x32_bf16 v[66:69], v[158:161], v[236:239], v[66:69]
	s_setprio 0
	s_barrier
; #define PG8_STAGE(bufoff, gbase, voff) do { _Pragma("unroll") for (int _i = 0; _i < 2; ++_i) { unsigned vo_ = (voff)[_i]; asm volatile("" : "+v"(vo_));   \
;         __builtin_amdgcn_global_load_lds((const unsigned*)((const char*)(gbase) + vo_), (LAS unsigned*)(lds + (bufoff) + ldsw + _i * 8192), 16, 0, 0); } } while (0)
; #define PG8_LDA(dst, b, h) do { _Pragma("unroll") for (int m = 0; m < 4; ++m) _Pragma("unroll") for (int k = 0; k < 2; ++k) dst[m][k] = *(const LAS bf16x8*)(lds + PG8_SA(b, h) + aoff + m * 2048 + k * 1024); } while (0)
; #define PG8_WAIT_V(n) asm volatile("s_waitcnt vmcnt(" #n ")" ::: "memory")
; #define PG8_WAIT_L(n) asm volatile("s_waitcnt lgkmcnt(" #n ")" ::: "memory")
; #define PG8_BAR __builtin_amdgcn_s_barrier()
; #define PG8_SCHED __builtin_amdgcn_sched_barrier(0)
;     ...
;             PG8_LDA(At, 1, 1); PG8_STAGE(PG8_SB(1, 0), b3, voffB); PG8_STAGE(PG8_SB(1, 1), b3 + hstepB, voffB); PG8_STAGE(PG8_SA(1, 0), a3, va[0]);
;             PG8_WAIT_V(8); PG8_WAIT_L(0); PG8_BAR; PG8_MMA(1, 0, At, B0); PG8_MMA(1, 1, At, B1); PG8_BAR; PG8_SCHED;
;         }
	v_mov_b32_e32 v166, v187
	ds_read_b128 v[208:211], v202 offset:49152
	ds_read_b128 v[212:215], v202 offset:50176
	ds_read_b128 v[216:219], v202 offset:51200
	ds_read_b128 v[220:223], v202 offset:52224
	ds_read_b128 v[224:227], v202 offset:53248
	ds_read_b128 v[228:231], v202 offset:54272
	ds_read_b128 v[232:235], v202 offset:55296
	ds_read_b128 v[236:239], v202 offset:56320
	s_add_i32 s40, s40, s42
	v_lshl_add_u64 v[240:241], s[28:29], 0, v[166:167]
	v_lshl_add_u64 v[240:241], v[240:241], 0, s[14:15]
	s_mov_b32 m0, s40
	v_mov_b32_e32 v166, v189
	global_load_lds_dwordx4 v[240:241], off
	s_add_i32 m0, s40, 0x2000
	s_nop 0
	v_lshl_add_u64 v[240:241], s[28:29], 0, v[166:167]
	s_add_u32 s28, s28, 0x80080
	v_lshl_add_u64 v[240:241], v[240:241], 0, s[14:15]
	s_addc_u32 s29, s29, 0
	v_mov_b32_e32 v166, v187
	s_add_i32 s40, s41, s42
	global_load_lds_dwordx4 v[240:241], off
	s_mov_b32 m0, s40
	s_nop 0
	global_load_lds_dwordx4 v166, s[28:29]
	v_mov_b32_e32 v166, v189
	s_add_i32 m0, s40, 0x2000
	s_nop 0
	global_load_lds_dwordx4 v166, s[28:29]
	v_mov_b32_e32 v166, v194
	s_mov_b32 m0, s56
	v_lshl_add_u64 v[240:241], s[34:35], 0, v[166:167]
	v_lshl_add_u64 v[240:241], v[240:241], 0, s[14:15]
	v_mov_b32_e32 v166, v195
	global_load_lds_dwordx4 v[240:241], off
	s_mov_b32 m0, s57
	v_lshl_add_u64 v[240:241], s[34:35], 0, v[166:167]
	v_lshl_add_u64 v[240:241], v[240:241], 0, s[14:15]
	global_load_lds_dwordx4 v[240:241], off
	s_waitcnt vmcnt(8)
	s_waitcnt lgkmcnt(0)
	s_barrier
	s_setprio 1
	s_waitcnt lgkmcnt(0)
	v_mfma_f32_16x16x32_bf16 v[62:65], v[130:133], v[208:211], v[62:65]
	v_mfma_f32_16x16x32_bf16 v[58:61], v[138:141], v[208:211], v[58:61]
	v_mfma_f32_16x16x32_bf16 v[50:53], v[130:133], v[216:219], v[50:53]
	v_mfma_f32_16x16x32_bf16 v[42:45], v[138:141], v[216:219], v[42:45]
	v_mfma_f32_16x16x32_bf16 v[34:37], v[130:133], v[224:227], v[34:37]
	v_mfma_f32_16x16x32_bf16 v[26:29], v[138:141], v[224:227], v[26:29]
	v_mfma_f32_16x16x32_bf16 v[18:21], v[130:133], v[232:235], v[18:21]
	v_mfma_f32_16x16x32_bf16 v[10:13], v[138:141], v[232:235], v[10:13]
	v_mfma_f32_16x16x32_bf16 v[62:65], v[134:137], v[212:215], v[62:65]
	v_mfma_f32_16x16x32_bf16 v[58:61], v[142:145], v[212:215], v[58:61]
	v_mfma_f32_16x16x32_bf16 v[50:53], v[134:137], v[220:223], v[50:53]
	v_mfma_f32_16x16x32_bf16 v[42:45], v[142:145], v[220:223], v[42:45]
	v_mfma_f32_16x16x32_bf16 v[34:37], v[134:137], v[228:231], v[34:37]
	v_mfma_f32_16x16x32_bf16 v[26:29], v[142:145], v[228:231], v[26:29]
	v_mfma_f32_16x16x32_bf16 v[18:21], v[134:137], v[236:239], v[18:21]
	v_mfma_f32_16x16x32_bf16 v[10:13], v[142:145], v[236:239], v[10:13]
	v_mfma_f32_16x16x32_bf16 v[54:57], v[146:149], v[208:211], v[54:57]
	v_mfma_f32_16x16x32_bf16 v[46:49], v[154:157], v[208:211], v[46:49]
	v_mfma_f32_16x16x32_bf16 v[38:41], v[146:149], v[216:219], v[38:41]
	v_mfma_f32_16x16x32_bf16 v[30:33], v[154:157], v[216:219], v[30:33]
	v_mfma_f32_16x16x32_bf16 v[22:25], v[146:149], v[224:227], v[22:25]
	v_mfma_f32_16x16x32_bf16 v[14:17], v[154:157], v[224:227], v[14:17]
	v_mfma_f32_16x16x32_bf16 v[6:9], v[146:149], v[232:235], v[6:9]
	v_mfma_f32_16x16x32_bf16 v[2:5], v[154:157], v[232:235], v[2:5]
	v_mfma_f32_16x16x32_bf16 v[54:57], v[150:153], v[212:215], v[54:57]
	v_mfma_f32_16x16x32_bf16 v[46:49], v[158:161], v[212:215], v[46:49]
	v_mfma_f32_16x16x32_bf16 v[38:41], v[150:153], v[220:223], v[38:41]
	v_mfma_f32_16x16x32_bf16 v[30:33], v[158:161], v[220:223], v[30:33]
	v_mfma_f32_16x16x32_bf16 v[22:25], v[150:153], v[228:231], v[22:25]
	v_mfma_f32_16x16x32_bf16 v[14:17], v[158:161], v[228:231], v[14:17]
	v_mfma_f32_16x16x32_bf16 v[6:9], v[150:153], v[236:239], v[6:9]
	v_mfma_f32_16x16x32_bf16 v[2:5], v[158:161], v[236:239], v[2:5]
	s_setprio 0
	s_barrier
	s_add_i32 s27, s27, 2
	s_cmp_gt_u32 s27, 29
	s_cbranch_scc1 .LBB0_1205
	s_mov_b64 s[28:29], s[30:31]
	s_branch .LBB0_1201

; #define PG8_STAGE(bufoff, gbase, voff) do { _Pragma("unroll") for (int _i = 0; _i < 2; ++_i) { unsigned vo_ = (voff)[_i]; asm volatile("" : "+v"(vo_));   \
;         __builtin_amdgcn_global_load_lds((const unsigned*)((const char*)(gbase) + vo_), (LAS unsigned*)(lds + (bufoff) + ldsw + _i * 8192), 16, 0, 0); } } while (0)
; #define PG8_LDA(dst, b, h) do { _Pragma("unroll") for (int m = 0; m < 4; ++m) _Pragma("unroll") for (int k = 0; k < 2; ++k) dst[m][k] = *(const LAS bf16x8*)(lds + PG8_SA(b, h) + aoff + m * 2048 + k * 1024); } while (0)
; #define PG8_LDB(dst, b, h) do { _Pragma("unroll") for (int n = 0; n < 2; ++n) _Pragma("unroll") for (int k = 0; k < 2; ++k) dst[n][k] = *(const LAS bf16x8*)(lds + PG8_SB(b, h) + boff + n * 2048 + k * 1024); } while (0)
; #define PG8_WAIT_V(n) asm volatile("s_waitcnt vmcnt(" #n ")" ::: "memory")
; #define PG8_WAIT_L(n) asm volatile("s_waitcnt lgkmcnt(" #n ")" ::: "memory")
; #define PG8_BAR __builtin_amdgcn_s_barrier()
; #define PG8_SCHED __builtin_amdgcn_sched_barrier(0)
; #define PG8_AOFFS(dst, un) do { _Pragma("unroll") for (int _h = 0; _h < 2; ++_h) _Pragma("unroll") for (int _i = 0; _i < 2; ++_i) dst[_h][_i] = S.Aoff(un, _h * HALF + Rr[_i]) + (unsigned)Cc[_i] * 2u; } while (0)
;     ...
;             PG8_LDB(B0, 0, 0); PG8_LDB(B1, 0, 1); PG8_SCHED; PG8_LDA(At, 0, 0); PG8_STAGE(PG8_SA(1, 1), a1, va[1]);
;             PG8_WAIT_V(8); PG8_WAIT_L(0); PG8_BAR; PG8_MMA(0, 0, At, B0); PG8_MMA(0, 1, At, B1); PG8_BAR; PG8_SCHED;
;             if (last && has_next) { PG8_AOFFS(va, nxt); }
;             PG8_LDA(At, 0, 1); PG8_STAGE(PG8_SB(0, 0), b2, voffB); PG8_STAGE(PG8_SB(0, 1), b2 + hstepB, voffB); PG8_STAGE(PG8_SA(0, 0), a2, va[0]);
;             PG8_WAIT_V(8); PG8_WAIT_L(0); PG8_BAR; PG8_MMA(1, 0, At, B0); PG8_MMA(1, 1, At, B1); PG8_BAR; PG8_SCHED;
;             PG8_LDB(B0, 1, 0); PG8_LDB(B1, 1, 1); PG8_SCHED; PG8_LDA(At, 1, 0); PG8_STAGE(PG8_SA(0, 1), a2, va[1]);
;             PG8_WAIT_V(8); PG8_WAIT_L(0); PG8_BAR; PG8_MMA(0, 0, At, B0); PG8_MMA(0, 1, At, B1); PG8_BAR; PG8_SCHED;
.LBB0_1234:
	ds_read_b128 v[146:149], v192
	ds_read_b128 v[150:153], v192 offset:1024
	ds_read_b128 v[154:157], v192 offset:2048
	ds_read_b128 v[158:161], v192 offset:3072
	ds_read_b128 v[130:133], v193
	ds_read_b128 v[134:137], v193 offset:1024
	ds_read_b128 v[138:141], v193 offset:2048
	ds_read_b128 v[142:145], v193 offset:3072
	s_cmp_eq_u32 s25, s35
	s_cselect_b64 s[50:51], -1, 0
	s_add_i32 m0, s41, 0xc000
	v_mov_b32_e32 v162, v182
	s_add_u32 s46, s16, s44
	ds_read_b128 v[200:203], v194
	ds_read_b128 v[204:207], v194 offset:1024
	ds_read_b128 v[208:211], v194 offset:2048
	ds_read_b128 v[212:215], v194 offset:3072
	ds_read_b128 v[216:219], v194 offset:4096
	ds_read_b128 v[220:223], v194 offset:5120
	ds_read_b128 v[224:227], v194 offset:6144
	ds_read_b128 v[228:231], v194 offset:7168
	s_addc_u32 s47, s17, s45
	global_load_lds_dwordx4 v162, s[46:47]
	v_mov_b32_e32 v162, v183
	s_add_i32 m0, s41, 0xe000
	s_nop 0
	global_load_lds_dwordx4 v162, s[46:47]
	s_waitcnt vmcnt(8)
	s_waitcnt lgkmcnt(0)
	s_barrier
	s_setprio 1
	s_waitcnt lgkmcnt(0)
	v_mfma_f32_16x16x32_bf16 v[126:129], v[146:149], v[200:203], v[126:129]
	v_mfma_f32_16x16x32_bf16 v[122:125], v[154:157], v[200:203], v[122:125]
	v_mfma_f32_16x16x32_bf16 v[118:121], v[146:149], v[208:211], v[118:121]
	v_mfma_f32_16x16x32_bf16 v[114:117], v[154:157], v[208:211], v[114:117]
	v_mfma_f32_16x16x32_bf16 v[110:113], v[146:149], v[216:219], v[110:113]
	v_mfma_f32_16x16x32_bf16 v[102:105], v[154:157], v[216:219], v[102:105]
	v_mfma_f32_16x16x32_bf16 v[94:97], v[146:149], v[224:227], v[94:97]
	v_mfma_f32_16x16x32_bf16 v[86:89], v[154:157], v[224:227], v[86:89]
	v_mfma_f32_16x16x32_bf16 v[126:129], v[150:153], v[204:207], v[126:129]
	v_mfma_f32_16x16x32_bf16 v[122:125], v[158:161], v[204:207], v[122:125]
	v_mfma_f32_16x16x32_bf16 v[118:121], v[150:153], v[212:215], v[118:121]
	v_mfma_f32_16x16x32_bf16 v[114:117], v[158:161], v[212:215], v[114:117]
	v_mfma_f32_16x16x32_bf16 v[110:113], v[150:153], v[220:223], v[110:113]
	v_mfma_f32_16x16x32_bf16 v[102:105], v[158:161], v[220:223], v[102:105]
	v_mfma_f32_16x16x32_bf16 v[94:97], v[150:153], v[228:231], v[94:97]
	v_mfma_f32_16x16x32_bf16 v[86:89], v[158:161], v[228:231], v[86:89]
	v_mfma_f32_16x16x32_bf16 v[106:109], v[130:133], v[200:203], v[106:109]
	v_mfma_f32_16x16x32_bf16 v[98:101], v[138:141], v[200:203], v[98:101]
	v_mfma_f32_16x16x32_bf16 v[90:93], v[130:133], v[208:211], v[90:93]
	v_mfma_f32_16x16x32_bf16 v[82:85], v[138:141], v[208:211], v[82:85]
	v_mfma_f32_16x16x32_bf16 v[78:81], v[130:133], v[216:219], v[78:81]
	v_mfma_f32_16x16x32_bf16 v[74:77], v[138:141], v[216:219], v[74:77]
	v_mfma_f32_16x16x32_bf16 v[70:73], v[130:133], v[224:227], v[70:73]
	v_mfma_f32_16x16x32_bf16 v[66:69], v[138:141], v[224:227], v[66:69]
	v_mfma_f32_16x16x32_bf16 v[106:109], v[134:137], v[204:207], v[106:109]
	v_mfma_f32_16x16x32_bf16 v[98:101], v[142:145], v[204:207], v[98:101]
	v_mfma_f32_16x16x32_bf16 v[90:93], v[134:137], v[212:215], v[90:93]
	v_mfma_f32_16x16x32_bf16 v[82:85], v[142:145], v[212:215], v[82:85]
	v_mfma_f32_16x16x32_bf16 v[78:81], v[134:137], v[220:223], v[78:81]
	v_mfma_f32_16x16x32_bf16 v[74:77], v[142:145], v[220:223], v[74:77]
	v_mfma_f32_16x16x32_bf16 v[70:73], v[134:137], v[228:231], v[70:73]
	v_mfma_f32_16x16x32_bf16 v[66:69], v[142:145], v[228:231], v[66:69]
	s_setprio 0
	s_barrier
	s_and_b64 s[46:47], s[42:43], s[50:51]
	s_andn2_b64 vcc, exec, s[46:47]
	s_cbranch_vccnz .LBB0_1236
	v_mov_b32_e32 v183, v198
	v_mov_b32_e32 v182, v197
	v_mov_b32_e32 v181, v196
	v_mov_b32_e32 v180, v195
.LBB0_1236:
	s_add_i32 s35, s35, 2
	s_add_u32 s46, s44, 0x100
	s_addc_u32 s47, s45, 0
	s_and_b64 s[48:49], s[50:51], exec
	s_cselect_b32 s48, 0, s46
	s_cselect_b32 s49, 0, s47
	s_add_u32 s48, s4, s48
	s_addc_u32 s49, s5, s49
	s_add_u32 s70, s27, s44
	s_addc_u32 s71, s31, s45
	s_and_b64 s[44:45], s[50:51], exec
	v_mov_b32_e32 v162, v187
	s_mov_b32 m0, s54
	s_cselect_b32 s45, s29, s71
	s_cselect_b32 s44, s28, s70
	ds_read_b128 v[200:203], v194 offset:16384
	ds_read_b128 v[204:207], v194 offset:17408
	ds_read_b128 v[208:211], v194 offset:18432
	ds_read_b128 v[212:215], v194 offset:19456
	ds_read_b128 v[216:219], v194 offset:20480
	ds_read_b128 v[220:223], v194 offset:21504
	ds_read_b128 v[224:227], v194 offset:22528
	ds_read_b128 v[228:231], v194 offset:23552
	s_add_u32 s50, s44, 0x80000
	global_load_lds_dwordx4 v162, s[44:45]
	v_mov_b32_e32 v162, v189
	s_mov_b32 m0, s55
	s_addc_u32 s51, s45, 0
	global_load_lds_dwordx4 v162, s[44:45]
	v_mov_b32_e32 v162, v187
	s_mov_b32 m0, s56
	s_nop 0
	global_load_lds_dwordx4 v162, s[50:51]
	v_mov_b32_e32 v162, v189
	s_mov_b32 m0, s57
	s_nop 0
	global_load_lds_dwordx4 v162, s[50:51]
	v_mov_b32_e32 v162, v180
	s_mov_b32 m0, s41
	s_nop 0
	global_load_lds_dwordx4 v162, s[48:49]
	v_mov_b32_e32 v162, v181
	s_mov_b32 m0, s58
	s_nop 0
	global_load_lds_dwordx4 v162, s[48:49]
	s_waitcnt vmcnt(8)
	s_waitcnt lgkmcnt(0)
	s_barrier
; #define PG8_STAGE(bufoff, gbase, voff) do { _Pragma("unroll") for (int _i = 0; _i < 2; ++_i) { unsigned vo_ = (voff)[_i]; asm volatile("" : "+v"(vo_));   \
;         __builtin_amdgcn_global_load_lds((const unsigned*)((const char*)(gbase) + vo_), (LAS unsigned*)(lds + (bufoff) + ldsw + _i * 8192), 16, 0, 0); } } while (0)
; #define PG8_LDA(dst, b, h) do { _Pragma("unroll") for (int m = 0; m < 4; ++m) _Pragma("unroll") for (int k = 0; k < 2; ++k) dst[m][k] = *(const LAS bf16x8*)(lds + PG8_SA(b, h) + aoff + m * 2048 + k * 1024); } while (0)
; #define PG8_LDB(dst, b, h) do { _Pragma("unroll") for (int n = 0; n < 2; ++n) _Pragma("unroll") for (int k = 0; k < 2; ++k) dst[n][k] = *(const LAS bf16x8*)(lds + PG8_SB(b, h) + boff + n * 2048 + k * 1024); } while (0)
; #define PG8_WAIT_V(n) asm volatile("s_waitcnt vmcnt(" #n ")" ::: "memory")
; #define PG8_WAIT_L(n) asm volatile("s_waitcnt lgkmcnt(" #n ")" ::: "memory")
;     ...
;         for (int t = 0; t < nt; t += 2) {
;             const bool last = (t == nt - 2);
;             const char* a1 = Abase + (size_t)(t + 1) * kstep;
;             const char* a2 = Abase + (last ? (size_t)0 : (size_t)(t + 2) * kstep); const char* b2 = last ? nB : cB + (size_t)(t + 2) * kstep;
;             const char* a3 = a2 + kstep; const char* b3 = b2 + kstep;
;             PG8_LDB(B0, 0, 0); PG8_LDB(B1, 0, 1); PG8_SCHED; PG8_LDA(At, 0, 0); PG8_STAGE(PG8_SA(1, 1), a1, va[1]);
;             PG8_WAIT_V(8); PG8_WAIT_L(0); PG8_BAR; PG8_MMA(0, 0, At, B0); PG8_MMA(0, 1, At, B1); PG8_BAR; PG8_SCHED;
;             if (last && has_next) { PG8_AOFFS(va, nxt); }
;             PG8_LDA(At, 0, 1); PG8_STAGE(PG8_SB(0, 0), b2, voffB); PG8_STAGE(PG8_SB(0, 1), b2 + hstepB, voffB); PG8_STAGE(PG8_SA(0, 0), a2, va[0]);
;             PG8_WAIT_V(8); PG8_WAIT_L(0); PG8_BAR; PG8_MMA(1, 0, At, B0); PG8_MMA(1, 1, At, B1); PG8_BAR; PG8_SCHED;
;             PG8_LDB(B0, 1, 0); PG8_LDB(B1, 1, 1); PG8_SCHED; PG8_LDA(At, 1, 0); PG8_STAGE(PG8_SA(0, 1), a2, va[1]);
;             PG8_WAIT_V(8); PG8_WAIT_L(0); PG8_BAR; PG8_MMA(0, 0, At, B0); PG8_MMA(0, 1, At, B1); PG8_BAR; PG8_SCHED;
;             PG8_LDA(At, 1, 1); PG8_STAGE(PG8_SB(1, 0), b3, voffB); PG8_STAGE(PG8_SB(1, 1), b3 + hstepB, voffB); PG8_STAGE(PG8_SA(1, 0), a3, va[0]);
;             PG8_WAIT_V(8); PG8_WAIT_L(0); PG8_BAR; PG8_MMA(1, 0, At, B0); PG8_MMA(1, 1, At, B1); PG8_BAR; PG8_SCHED;
;         }
	s_setprio 1
	s_waitcnt lgkmcnt(0)
	v_mfma_f32_16x16x32_bf16 v[62:65], v[146:149], v[200:203], v[62:65]
	v_mfma_f32_16x16x32_bf16 v[58:61], v[154:157], v[200:203], v[58:61]
	v_mfma_f32_16x16x32_bf16 v[54:57], v[146:149], v[208:211], v[54:57]
	v_mfma_f32_16x16x32_bf16 v[42:45], v[154:157], v[208:211], v[42:45]
	v_mfma_f32_16x16x32_bf16 v[38:41], v[146:149], v[216:219], v[38:41]
	v_mfma_f32_16x16x32_bf16 v[30:33], v[154:157], v[216:219], v[30:33]
	v_mfma_f32_16x16x32_bf16 v[22:25], v[146:149], v[224:227], v[22:25]
	v_mfma_f32_16x16x32_bf16 v[14:17], v[154:157], v[224:227], v[14:17]
	v_mfma_f32_16x16x32_bf16 v[62:65], v[150:153], v[204:207], v[62:65]
	v_mfma_f32_16x16x32_bf16 v[58:61], v[158:161], v[204:207], v[58:61]
	v_mfma_f32_16x16x32_bf16 v[54:57], v[150:153], v[212:215], v[54:57]
	v_mfma_f32_16x16x32_bf16 v[42:45], v[158:161], v[212:215], v[42:45]
	v_mfma_f32_16x16x32_bf16 v[38:41], v[150:153], v[220:223], v[38:41]
	v_mfma_f32_16x16x32_bf16 v[30:33], v[158:161], v[220:223], v[30:33]
	v_mfma_f32_16x16x32_bf16 v[22:25], v[150:153], v[228:231], v[22:25]
	v_mfma_f32_16x16x32_bf16 v[14:17], v[158:161], v[228:231], v[14:17]
	v_mfma_f32_16x16x32_bf16 v[50:53], v[130:133], v[200:203], v[50:53]
	v_mfma_f32_16x16x32_bf16 v[46:49], v[138:141], v[200:203], v[46:49]
	v_mfma_f32_16x16x32_bf16 v[34:37], v[130:133], v[208:211], v[34:37]
	v_mfma_f32_16x16x32_bf16 v[26:29], v[138:141], v[208:211], v[26:29]
	v_mfma_f32_16x16x32_bf16 v[18:21], v[130:133], v[216:219], v[18:21]
	v_mfma_f32_16x16x32_bf16 v[10:13], v[138:141], v[216:219], v[10:13]
	v_mfma_f32_16x16x32_bf16 v[6:9], v[130:133], v[224:227], v[6:9]
	v_mfma_f32_16x16x32_bf16 v[2:5], v[138:141], v[224:227], v[2:5]
	v_mfma_f32_16x16x32_bf16 v[50:53], v[134:137], v[204:207], v[50:53]
	v_mfma_f32_16x16x32_bf16 v[46:49], v[142:145], v[204:207], v[46:49]
	v_mfma_f32_16x16x32_bf16 v[34:37], v[134:137], v[212:215], v[34:37]
	v_mfma_f32_16x16x32_bf16 v[26:29], v[142:145], v[212:215], v[26:29]
	v_mfma_f32_16x16x32_bf16 v[18:21], v[134:137], v[220:223], v[18:21]
	v_mfma_f32_16x16x32_bf16 v[10:13], v[142:145], v[220:223], v[10:13]
	v_mfma_f32_16x16x32_bf16 v[6:9], v[134:137], v[228:231], v[6:9]
	v_mfma_f32_16x16x32_bf16 v[2:5], v[142:145], v[228:231], v[2:5]
	s_setprio 0
	s_barrier
	s_add_i32 s50, 0, 0x18000
	s_add_i32 s51, 0, 0x1c000
	v_add_u32_e32 v142, s50, v191
	v_add_u32_e32 v158, s51, v191
	ds_read_b128 v[130:133], v142
	ds_read_b128 v[134:137], v142 offset:1024
	ds_read_b128 v[138:141], v142 offset:2048
	ds_read_b128 v[142:145], v142 offset:3072
	ds_read_b128 v[146:149], v158
	ds_read_b128 v[150:153], v158 offset:1024
	ds_read_b128 v[154:157], v158 offset:2048
	ds_read_b128 v[158:161], v158 offset:3072
	v_mov_b32_e32 v162, v182
	s_mov_b32 m0, s59
	ds_read_b128 v[200:203], v194 offset:32768
	ds_read_b128 v[204:207], v194 offset:33792
	ds_read_b128 v[208:211], v194 offset:34816
	ds_read_b128 v[212:215], v194 offset:35840
	ds_read_b128 v[216:219], v194 offset:36864
	ds_read_b128 v[220:223], v194 offset:37888
	ds_read_b128 v[224:227], v194 offset:38912
	ds_read_b128 v[228:231], v194 offset:39936
	s_nop 0
	global_load_lds_dwordx4 v162, s[48:49]
	v_mov_b32_e32 v162, v183
	s_mov_b32 m0, s60
	s_nop 0
	global_load_lds_dwordx4 v162, s[48:49]
	s_waitcnt vmcnt(8)
	s_waitcnt lgkmcnt(0)
	s_barrier
	s_setprio 1
	s_waitcnt lgkmcnt(0)
	v_mfma_f32_16x16x32_bf16 v[126:129], v[130:133], v[200:203], v[126:129]
	v_mfma_f32_16x16x32_bf16 v[122:125], v[138:141], v[200:203], v[122:125]
	v_mfma_f32_16x16x32_bf16 v[118:121], v[130:133], v[208:211], v[118:121]
	v_mfma_f32_16x16x32_bf16 v[114:117], v[138:141], v[208:211], v[114:117]
	v_mfma_f32_16x16x32_bf16 v[110:113], v[130:133], v[216:219], v[110:113]
	v_mfma_f32_16x16x32_bf16 v[102:105], v[138:141], v[216:219], v[102:105]
	v_mfma_f32_16x16x32_bf16 v[94:97], v[130:133], v[224:227], v[94:97]
	v_mfma_f32_16x16x32_bf16 v[86:89], v[138:141], v[224:227], v[86:89]
	v_mfma_f32_16x16x32_bf16 v[126:129], v[134:137], v[204:207], v[126:129]
	v_mfma_f32_16x16x32_bf16 v[122:125], v[142:145], v[204:207], v[122:125]
	v_mfma_f32_16x16x32_bf16 v[118:121], v[134:137], v[212:215], v[118:121]
	v_mfma_f32_16x16x32_bf16 v[114:117], v[142:145], v[212:215], v[114:117]
	v_mfma_f32_16x16x32_bf16 v[110:113], v[134:137], v[220:223], v[110:113]
	v_mfma_f32_16x16x32_bf16 v[102:105], v[142:145], v[220:223], v[102:105]
	v_mfma_f32_16x16x32_bf16 v[94:97], v[134:137], v[228:231], v[94:97]
	v_mfma_f32_16x16x32_bf16 v[86:89], v[142:145], v[228:231], v[86:89]
	v_mfma_f32_16x16x32_bf16 v[106:109], v[146:149], v[200:203], v[106:109]
	v_mfma_f32_16x16x32_bf16 v[98:101], v[154:157], v[200:203], v[98:101]
	v_mfma_f32_16x16x32_bf16 v[90:93], v[146:149], v[208:211], v[90:93]
	v_mfma_f32_16x16x32_bf16 v[82:85], v[154:157], v[208:211], v[82:85]
	v_mfma_f32_16x16x32_bf16 v[78:81], v[146:149], v[216:219], v[78:81]
	v_mfma_f32_16x16x32_bf16 v[74:77], v[154:157], v[216:219], v[74:77]
	v_mfma_f32_16x16x32_bf16 v[70:73], v[146:149], v[224:227], v[70:73]
	v_mfma_f32_16x16x32_bf16 v[66:69], v[154:157], v[224:227], v[66:69]
	v_mfma_f32_16x16x32_bf16 v[106:109], v[150:153], v[204:207], v[106:109]
	v_mfma_f32_16x16x32_bf16 v[98:101], v[158:161], v[204:207], v[98:101]
	v_mfma_f32_16x16x32_bf16 v[90:93], v[150:153], v[212:215], v[90:93]
	v_mfma_f32_16x16x32_bf16 v[82:85], v[158:161], v[212:215], v[82:85]
	v_mfma_f32_16x16x32_bf16 v[78:81], v[150:153], v[220:223], v[78:81]
	v_mfma_f32_16x16x32_bf16 v[74:77], v[158:161], v[220:223], v[74:77]
	v_mfma_f32_16x16x32_bf16 v[70:73], v[150:153], v[228:231], v[70:73]
	v_mfma_f32_16x16x32_bf16 v[66:69], v[158:161], v[228:231], v[66:69]
	s_setprio 0
	s_barrier
; #define PG8_STAGE(bufoff, gbase, voff) do { _Pragma("unroll") for (int _i = 0; _i < 2; ++_i) { unsigned vo_ = (voff)[_i]; asm volatile("" : "+v"(vo_));   \
;         __builtin_amdgcn_global_load_lds((const unsigned*)((const char*)(gbase) + vo_), (LAS unsigned*)(lds + (bufoff) + ldsw + _i * 8192), 16, 0, 0); } } while (0)
; #define PG8_LDA(dst, b, h) do { _Pragma("unroll") for (int m = 0; m < 4; ++m) _Pragma("unroll") for (int k = 0; k < 2; ++k) dst[m][k] = *(const LAS bf16x8*)(lds + PG8_SA(b, h) + aoff + m * 2048 + k * 1024); } while (0)
; #define PG8_LDB(dst, b, h) do { _Pragma("unroll") for (int n = 0; n < 2; ++n) _Pragma("unroll") for (int k = 0; k < 2; ++k) dst[n][k] = *(const LAS bf16x8*)(lds + PG8_SB(b, h) + boff + n * 2048 + k * 1024); } while (0)
; #define PG8_WAIT_V(n) asm volatile("s_waitcnt vmcnt(" #n ")" ::: "memory")
; #define PG8_WAIT_L(n) asm volatile("s_waitcnt lgkmcnt(" #n ")" ::: "memory")
; #define PG8_BAR __builtin_amdgcn_s_barrier()
; #define PG8_SCHED __builtin_amdgcn_sched_barrier(0)
;     ...
;             PG8_LDA(At, 0, 1); PG8_STAGE(PG8_SB(0, 0), b2, voffB); PG8_STAGE(PG8_SB(0, 1), b2 + hstepB, voffB); PG8_STAGE(PG8_SA(0, 0), a2, va[0]);
;             PG8_WAIT_V(8); PG8_WAIT_L(0); PG8_BAR; PG8_MMA(1, 0, At, B0); PG8_MMA(1, 1, At, B1); PG8_BAR; PG8_SCHED;
;             PG8_LDB(B0, 1, 0); PG8_LDB(B1, 1, 1); PG8_SCHED; PG8_LDA(At, 1, 0); PG8_STAGE(PG8_SA(0, 1), a2, va[1]);
;             PG8_WAIT_V(8); PG8_WAIT_L(0); PG8_BAR; PG8_MMA(0, 0, At, B0); PG8_MMA(0, 1, At, B1); PG8_BAR; PG8_SCHED;
;             PG8_LDA(At, 1, 1); PG8_STAGE(PG8_SB(1, 0), b3, voffB); PG8_STAGE(PG8_SB(1, 1), b3 + hstepB, voffB); PG8_STAGE(PG8_SA(1, 0), a3, va[0]);
;             PG8_WAIT_V(8); PG8_WAIT_L(0); PG8_BAR; PG8_MMA(1, 0, At, B0); PG8_MMA(1, 1, At, B1); PG8_BAR; PG8_SCHED;
;         }
	v_mov_b32_e32 v162, v187
	ds_read_b128 v[200:203], v194 offset:49152
	ds_read_b128 v[204:207], v194 offset:50176
	ds_read_b128 v[208:211], v194 offset:51200
	ds_read_b128 v[212:215], v194 offset:52224
	ds_read_b128 v[216:219], v194 offset:53248
	ds_read_b128 v[220:223], v194 offset:54272
	ds_read_b128 v[224:227], v194 offset:55296
	ds_read_b128 v[228:231], v194 offset:56320
	s_add_i32 s50, s50, s53
	v_lshl_add_u64 v[232:233], s[44:45], 0, v[162:163]
	v_lshl_add_u64 v[232:233], v[232:233], 0, s[14:15]
	s_mov_b32 m0, s50
	v_mov_b32_e32 v162, v189
	global_load_lds_dwordx4 v[232:233], off
	s_add_i32 m0, s50, 0x2000
	s_nop 0
	v_lshl_add_u64 v[232:233], s[44:45], 0, v[162:163]
	s_add_u32 s44, s44, 0x80080
	v_lshl_add_u64 v[232:233], v[232:233], 0, s[14:15]
	s_addc_u32 s45, s45, 0
	v_mov_b32_e32 v162, v187
	s_add_i32 s50, s51, s53
	global_load_lds_dwordx4 v[232:233], off
	s_mov_b32 m0, s50
	s_nop 0
	global_load_lds_dwordx4 v162, s[44:45]
	v_mov_b32_e32 v162, v189
	s_add_i32 m0, s50, 0x2000
	s_nop 0
	global_load_lds_dwordx4 v162, s[44:45]
	v_mov_b32_e32 v162, v180
	s_mov_b32 m0, s64
	v_lshl_add_u64 v[232:233], s[48:49], 0, v[162:163]
	v_lshl_add_u64 v[232:233], v[232:233], 0, s[14:15]
	v_mov_b32_e32 v162, v181
	global_load_lds_dwordx4 v[232:233], off
	s_mov_b32 m0, s65
	v_lshl_add_u64 v[232:233], s[48:49], 0, v[162:163]
	v_lshl_add_u64 v[232:233], v[232:233], 0, s[14:15]
	global_load_lds_dwordx4 v[232:233], off
	s_waitcnt vmcnt(8)
	s_waitcnt lgkmcnt(0)
	s_barrier
	s_setprio 1
	s_waitcnt lgkmcnt(0)
	v_mfma_f32_16x16x32_bf16 v[62:65], v[130:133], v[200:203], v[62:65]
	v_mfma_f32_16x16x32_bf16 v[58:61], v[138:141], v[200:203], v[58:61]
	v_mfma_f32_16x16x32_bf16 v[54:57], v[130:133], v[208:211], v[54:57]
	v_mfma_f32_16x16x32_bf16 v[42:45], v[138:141], v[208:211], v[42:45]
	v_mfma_f32_16x16x32_bf16 v[38:41], v[130:133], v[216:219], v[38:41]
	v_mfma_f32_16x16x32_bf16 v[30:33], v[138:141], v[216:219], v[30:33]
	v_mfma_f32_16x16x32_bf16 v[22:25], v[130:133], v[224:227], v[22:25]
	v_mfma_f32_16x16x32_bf16 v[14:17], v[138:141], v[224:227], v[14:17]
	v_mfma_f32_16x16x32_bf16 v[62:65], v[134:137], v[204:207], v[62:65]
	v_mfma_f32_16x16x32_bf16 v[58:61], v[142:145], v[204:207], v[58:61]
	v_mfma_f32_16x16x32_bf16 v[54:57], v[134:137], v[212:215], v[54:57]
	v_mfma_f32_16x16x32_bf16 v[42:45], v[142:145], v[212:215], v[42:45]
	v_mfma_f32_16x16x32_bf16 v[38:41], v[134:137], v[220:223], v[38:41]
	v_mfma_f32_16x16x32_bf16 v[30:33], v[142:145], v[220:223], v[30:33]
	v_mfma_f32_16x16x32_bf16 v[22:25], v[134:137], v[228:231], v[22:25]
	v_mfma_f32_16x16x32_bf16 v[14:17], v[142:145], v[228:231], v[14:17]
	v_mfma_f32_16x16x32_bf16 v[50:53], v[146:149], v[200:203], v[50:53]
	v_mfma_f32_16x16x32_bf16 v[46:49], v[154:157], v[200:203], v[46:49]
	v_mfma_f32_16x16x32_bf16 v[34:37], v[146:149], v[208:211], v[34:37]
	v_mfma_f32_16x16x32_bf16 v[26:29], v[154:157], v[208:211], v[26:29]
	v_mfma_f32_16x16x32_bf16 v[18:21], v[146:149], v[216:219], v[18:21]
	v_mfma_f32_16x16x32_bf16 v[10:13], v[154:157], v[216:219], v[10:13]
	v_mfma_f32_16x16x32_bf16 v[6:9], v[146:149], v[224:227], v[6:9]
	v_mfma_f32_16x16x32_bf16 v[2:5], v[154:157], v[224:227], v[2:5]
	v_mfma_f32_16x16x32_bf16 v[50:53], v[150:153], v[204:207], v[50:53]
	v_mfma_f32_16x16x32_bf16 v[46:49], v[158:161], v[204:207], v[46:49]
	v_mfma_f32_16x16x32_bf16 v[34:37], v[150:153], v[212:215], v[34:37]
	v_mfma_f32_16x16x32_bf16 v[26:29], v[158:161], v[212:215], v[26:29]
	v_mfma_f32_16x16x32_bf16 v[18:21], v[150:153], v[220:223], v[18:21]
	v_mfma_f32_16x16x32_bf16 v[10:13], v[158:161], v[220:223], v[10:13]
	v_mfma_f32_16x16x32_bf16 v[6:9], v[150:153], v[228:231], v[6:9]
	v_mfma_f32_16x16x32_bf16 v[2:5], v[158:161], v[228:231], v[2:5]
	s_setprio 0
	s_barrier
	s_cmp_ge_i32 s35, s52
	s_cbranch_scc1 .LBB0_1238
	s_mov_b64 s[44:45], s[46:47]
	s_branch .LBB0_1234

; #define PG8_STAGE(bufoff, gbase, voff) do { _Pragma("unroll") for (int _i = 0; _i < 2; ++_i) { unsigned vo_ = (voff)[_i]; asm volatile("" : "+v"(vo_));   \
;         __builtin_amdgcn_global_load_lds((const unsigned*)((const char*)(gbase) + vo_), (LAS unsigned*)(lds + (bufoff) + ldsw + _i * 8192), 16, 0, 0); } } while (0)
; #define PG8_LDA(dst, b, h) do { _Pragma("unroll") for (int m = 0; m < 4; ++m) _Pragma("unroll") for (int k = 0; k < 2; ++k) dst[m][k] = *(const LAS bf16x8*)(lds + PG8_SA(b, h) + aoff + m * 2048 + k * 1024); } while (0)
; #define PG8_LDB(dst, b, h) do { _Pragma("unroll") for (int n = 0; n < 2; ++n) _Pragma("unroll") for (int k = 0; k < 2; ++k) dst[n][k] = *(const LAS bf16x8*)(lds + PG8_SB(b, h) + boff + n * 2048 + k * 1024); } while (0)
; #define PG8_WAIT_V(n) asm volatile("s_waitcnt vmcnt(" #n ")" ::: "memory")
; #define PG8_WAIT_L(n) asm volatile("s_waitcnt lgkmcnt(" #n ")" ::: "memory")
; #define PG8_BAR __builtin_amdgcn_s_barrier()
; #define PG8_SCHED __builtin_amdgcn_sched_barrier(0)
;     ...
;         for (int t = 0; t < nt; t += 2) {
;             const bool last = (t == nt - 2);
;             const char* a1 = Abase + (size_t)(t + 1) * kstep;
;             const char* a2 = Abase + (last ? (size_t)0 : (size_t)(t + 2) * kstep); const char* b2 = last ? nB : cB + (size_t)(t + 2) * kstep;
;             const char* a3 = a2 + kstep; const char* b3 = b2 + kstep;
;             PG8_LDB(B0, 0, 0); PG8_LDB(B1, 0, 1); PG8_SCHED; PG8_LDA(At, 0, 0); PG8_STAGE(PG8_SA(1, 1), a1, va[1]);
;             PG8_WAIT_V(8); PG8_WAIT_L(0); PG8_BAR; PG8_MMA(0, 0, At, B0); PG8_MMA(0, 1, At, B1); PG8_BAR; PG8_SCHED;
;             if (last && has_next) { PG8_AOFFS(va, nxt); }
;             PG8_LDA(At, 0, 1); PG8_STAGE(PG8_SB(0, 0), b2, voffB); PG8_STAGE(PG8_SB(0, 1), b2 + hstepB, voffB); PG8_STAGE(PG8_SA(0, 0), a2, va[0]);
;             PG8_WAIT_V(8); PG8_WAIT_L(0); PG8_BAR; PG8_MMA(1, 0, At, B0); PG8_MMA(1, 1, At, B1); PG8_BAR; PG8_SCHED;
;             PG8_LDB(B0, 1, 0); PG8_LDB(B1, 1, 1); PG8_SCHED; PG8_LDA(At, 1, 0); PG8_STAGE(PG8_SA(0, 1), a2, va[1]);
;             PG8_WAIT_V(8); PG8_WAIT_L(0); PG8_BAR; PG8_MMA(0, 0, At, B0); PG8_MMA(0, 1, At, B1); PG8_BAR; PG8_SCHED;
.LBB0_1414:
	ds_read_b128 v[146:149], v178
	ds_read_b128 v[150:153], v178 offset:1024
	ds_read_b128 v[154:157], v178 offset:2048
	ds_read_b128 v[158:161], v178 offset:3072
	ds_read_b128 v[130:133], v179
	ds_read_b128 v[134:137], v179 offset:1024
	ds_read_b128 v[138:141], v179 offset:2048
	ds_read_b128 v[142:145], v179 offset:3072
	s_cmp_eq_u32 s65, 12
	s_cselect_b64 s[44:45], -1, 0
	s_add_i32 m0, s47, 0xc000
	v_mov_b32_e32 v162, v173
	s_add_u32 s40, s20, s34
	ds_read_b128 v[186:189], v180
	ds_read_b128 v[190:193], v180 offset:1024
	ds_read_b128 v[194:197], v180 offset:2048
	ds_read_b128 v[198:201], v180 offset:3072
	ds_read_b128 v[202:205], v180 offset:4096
	ds_read_b128 v[206:209], v180 offset:5120
	ds_read_b128 v[210:213], v180 offset:6144
	ds_read_b128 v[214:217], v180 offset:7168
	s_addc_u32 s41, s21, s35
	global_load_lds_dwordx4 v162, s[40:41]
	v_mov_b32_e32 v162, v174
	s_add_i32 m0, s47, 0xe000
	s_nop 0
	global_load_lds_dwordx4 v162, s[40:41]
	s_waitcnt vmcnt(8)
	s_waitcnt lgkmcnt(0)
	s_barrier
	s_setprio 1
	s_waitcnt lgkmcnt(0)
	v_mfma_i32_16x16x64_i8 v[126:129], v[146:149], v[186:189], v[126:129]
	v_mfma_i32_16x16x64_i8 v[122:125], v[154:157], v[186:189], v[122:125]
	v_mfma_i32_16x16x64_i8 v[110:113], v[146:149], v[194:197], v[110:113]
	v_mfma_i32_16x16x64_i8 v[106:109], v[154:157], v[194:197], v[106:109]
	v_mfma_i32_16x16x64_i8 v[94:97], v[146:149], v[202:205], v[94:97]
	v_mfma_i32_16x16x64_i8 v[90:93], v[154:157], v[202:205], v[90:93]
	v_mfma_i32_16x16x64_i8 v[78:81], v[146:149], v[210:213], v[78:81]
	v_mfma_i32_16x16x64_i8 v[74:77], v[154:157], v[210:213], v[74:77]
	v_mfma_i32_16x16x64_i8 v[126:129], v[150:153], v[190:193], v[126:129]
	v_mfma_i32_16x16x64_i8 v[122:125], v[158:161], v[190:193], v[122:125]
	v_mfma_i32_16x16x64_i8 v[110:113], v[150:153], v[198:201], v[110:113]
	v_mfma_i32_16x16x64_i8 v[106:109], v[158:161], v[198:201], v[106:109]
	v_mfma_i32_16x16x64_i8 v[94:97], v[150:153], v[206:209], v[94:97]
	v_mfma_i32_16x16x64_i8 v[90:93], v[158:161], v[206:209], v[90:93]
	v_mfma_i32_16x16x64_i8 v[78:81], v[150:153], v[214:217], v[78:81]
	v_mfma_i32_16x16x64_i8 v[74:77], v[158:161], v[214:217], v[74:77]
	v_mfma_i32_16x16x64_i8 v[118:121], v[130:133], v[186:189], v[118:121]
	v_mfma_i32_16x16x64_i8 v[114:117], v[138:141], v[186:189], v[114:117]
	v_mfma_i32_16x16x64_i8 v[102:105], v[130:133], v[194:197], v[102:105]
	v_mfma_i32_16x16x64_i8 v[98:101], v[138:141], v[194:197], v[98:101]
	v_mfma_i32_16x16x64_i8 v[86:89], v[130:133], v[202:205], v[86:89]
	v_mfma_i32_16x16x64_i8 v[82:85], v[138:141], v[202:205], v[82:85]
	v_mfma_i32_16x16x64_i8 v[70:73], v[130:133], v[210:213], v[70:73]
	v_mfma_i32_16x16x64_i8 v[66:69], v[138:141], v[210:213], v[66:69]
	v_mfma_i32_16x16x64_i8 v[118:121], v[134:137], v[190:193], v[118:121]
	v_mfma_i32_16x16x64_i8 v[114:117], v[142:145], v[190:193], v[114:117]
	v_mfma_i32_16x16x64_i8 v[102:105], v[134:137], v[198:201], v[102:105]
	v_mfma_i32_16x16x64_i8 v[98:101], v[142:145], v[198:201], v[98:101]
	v_mfma_i32_16x16x64_i8 v[86:89], v[134:137], v[206:209], v[86:89]
	v_mfma_i32_16x16x64_i8 v[82:85], v[142:145], v[206:209], v[82:85]
	v_mfma_i32_16x16x64_i8 v[70:73], v[134:137], v[214:217], v[70:73]
	v_mfma_i32_16x16x64_i8 v[66:69], v[142:145], v[214:217], v[66:69]
	s_setprio 0
	s_barrier
	s_and_b64 s[40:41], s[28:29], s[44:45]
	s_andn2_b64 vcc, exec, s[40:41]
	s_cbranch_vccnz .LBB0_1416
	v_mov_b32_e32 v174, v185
	v_mov_b32_e32 v173, v184
	v_mov_b32_e32 v172, v183
	v_mov_b32_e32 v171, v182
.LBB0_1416:
	s_add_u32 s40, s34, 0x100
	s_addc_u32 s41, s35, 0
	s_and_b64 s[42:43], s[44:45], exec
	s_cselect_b32 s42, 0, s40
	s_cselect_b32 s43, 0, s41
	s_add_u32 s42, s2, s42
	s_addc_u32 s43, s3, s43
	s_add_u32 s66, s27, s34
	s_addc_u32 s67, s64, s35
	s_and_b64 s[34:35], s[44:45], exec
	v_mov_b32_e32 v162, v168
	s_mov_b32 m0, s48
	s_cselect_b32 s35, s31, s67
	s_cselect_b32 s34, s30, s66
	ds_read_b128 v[186:189], v180 offset:16384
	ds_read_b128 v[190:193], v180 offset:17408
	ds_read_b128 v[194:197], v180 offset:18432
	ds_read_b128 v[198:201], v180 offset:19456
	ds_read_b128 v[202:205], v180 offset:20480
	ds_read_b128 v[206:209], v180 offset:21504
	ds_read_b128 v[210:213], v180 offset:22528
	ds_read_b128 v[214:217], v180 offset:23552
	s_add_u32 s44, s34, 0x40000
	global_load_lds_dwordx4 v162, s[34:35]
	v_mov_b32_e32 v162, v170
	s_mov_b32 m0, s49
	s_addc_u32 s45, s35, 0
	global_load_lds_dwordx4 v162, s[34:35]
	v_mov_b32_e32 v162, v168
	s_mov_b32 m0, s50
	s_nop 0
	global_load_lds_dwordx4 v162, s[44:45]
	v_mov_b32_e32 v162, v170
	s_mov_b32 m0, s51
	s_nop 0
	global_load_lds_dwordx4 v162, s[44:45]
	v_mov_b32_e32 v162, v171
	s_mov_b32 m0, s47
	s_nop 0
	global_load_lds_dwordx4 v162, s[42:43]
	v_mov_b32_e32 v162, v172
	s_mov_b32 m0, s52
	s_nop 0
	global_load_lds_dwordx4 v162, s[42:43]
	s_waitcnt vmcnt(8)
	s_waitcnt lgkmcnt(0)
	s_barrier
; #define PG8_STAGE(bufoff, gbase, voff) do { _Pragma("unroll") for (int _i = 0; _i < 2; ++_i) { unsigned vo_ = (voff)[_i]; asm volatile("" : "+v"(vo_));   \
;         __builtin_amdgcn_global_load_lds((const unsigned*)((const char*)(gbase) + vo_), (LAS unsigned*)(lds + (bufoff) + ldsw + _i * 8192), 16, 0, 0); } } while (0)
; #define PG8_LDA(dst, b, h) do { _Pragma("unroll") for (int m = 0; m < 4; ++m) _Pragma("unroll") for (int k = 0; k < 2; ++k) dst[m][k] = *(const LAS bf16x8*)(lds + PG8_SA(b, h) + aoff + m * 2048 + k * 1024); } while (0)
; #define PG8_LDB(dst, b, h) do { _Pragma("unroll") for (int n = 0; n < 2; ++n) _Pragma("unroll") for (int k = 0; k < 2; ++k) dst[n][k] = *(const LAS bf16x8*)(lds + PG8_SB(b, h) + boff + n * 2048 + k * 1024); } while (0)
; #define PG8_WAIT_V(n) asm volatile("s_waitcnt vmcnt(" #n ")" ::: "memory")
; #define PG8_WAIT_L(n) asm volatile("s_waitcnt lgkmcnt(" #n ")" ::: "memory")
; #define PG8_BAR __builtin_amdgcn_s_barrier()
; #define PG8_SCHED __builtin_amdgcn_sched_barrier(0)
;     ...
;             PG8_WAIT_V(8); PG8_WAIT_L(0); PG8_BAR; PG8_MMA(1, 0, At, B0); PG8_MMA(1, 1, At, B1); PG8_BAR; PG8_SCHED;
;             PG8_LDB(B0, 1, 0); PG8_LDB(B1, 1, 1); PG8_SCHED; PG8_LDA(At, 1, 0); PG8_STAGE(PG8_SA(0, 1), a2, va[1]);
;             PG8_WAIT_V(8); PG8_WAIT_L(0); PG8_BAR; PG8_MMA(0, 0, At, B0); PG8_MMA(0, 1, At, B1); PG8_BAR; PG8_SCHED;
	s_setprio 1
	s_waitcnt lgkmcnt(0)
	v_mfma_i32_16x16x64_i8 v[62:65], v[146:149], v[186:189], v[62:65]
	v_mfma_i32_16x16x64_i8 v[58:61], v[154:157], v[186:189], v[58:61]
	v_mfma_i32_16x16x64_i8 v[46:49], v[146:149], v[194:197], v[46:49]
	v_mfma_i32_16x16x64_i8 v[42:45], v[154:157], v[194:197], v[42:45]
	v_mfma_i32_16x16x64_i8 v[30:33], v[146:149], v[202:205], v[30:33]
	v_mfma_i32_16x16x64_i8 v[26:29], v[154:157], v[202:205], v[26:29]
	v_mfma_i32_16x16x64_i8 v[14:17], v[146:149], v[210:213], v[14:17]
	v_mfma_i32_16x16x64_i8 v[10:13], v[154:157], v[210:213], v[10:13]
	v_mfma_i32_16x16x64_i8 v[62:65], v[150:153], v[190:193], v[62:65]
	v_mfma_i32_16x16x64_i8 v[58:61], v[158:161], v[190:193], v[58:61]
	v_mfma_i32_16x16x64_i8 v[46:49], v[150:153], v[198:201], v[46:49]
	v_mfma_i32_16x16x64_i8 v[42:45], v[158:161], v[198:201], v[42:45]
	v_mfma_i32_16x16x64_i8 v[30:33], v[150:153], v[206:209], v[30:33]
	v_mfma_i32_16x16x64_i8 v[26:29], v[158:161], v[206:209], v[26:29]
	v_mfma_i32_16x16x64_i8 v[14:17], v[150:153], v[214:217], v[14:17]
	v_mfma_i32_16x16x64_i8 v[10:13], v[158:161], v[214:217], v[10:13]
	v_mfma_i32_16x16x64_i8 v[54:57], v[130:133], v[186:189], v[54:57]
	v_mfma_i32_16x16x64_i8 v[50:53], v[138:141], v[186:189], v[50:53]
	v_mfma_i32_16x16x64_i8 v[38:41], v[130:133], v[194:197], v[38:41]
	v_mfma_i32_16x16x64_i8 v[34:37], v[138:141], v[194:197], v[34:37]
	v_mfma_i32_16x16x64_i8 v[22:25], v[130:133], v[202:205], v[22:25]
	v_mfma_i32_16x16x64_i8 v[18:21], v[138:141], v[202:205], v[18:21]
	v_mfma_i32_16x16x64_i8 v[6:9], v[130:133], v[210:213], v[6:9]
	v_mfma_i32_16x16x64_i8 v[2:5], v[138:141], v[210:213], v[2:5]
	v_mfma_i32_16x16x64_i8 v[54:57], v[134:137], v[190:193], v[54:57]
	v_mfma_i32_16x16x64_i8 v[50:53], v[142:145], v[190:193], v[50:53]
	v_mfma_i32_16x16x64_i8 v[38:41], v[134:137], v[198:201], v[38:41]
	v_mfma_i32_16x16x64_i8 v[34:37], v[142:145], v[198:201], v[34:37]
	v_mfma_i32_16x16x64_i8 v[22:25], v[134:137], v[206:209], v[22:25]
	v_mfma_i32_16x16x64_i8 v[18:21], v[142:145], v[206:209], v[18:21]
	v_mfma_i32_16x16x64_i8 v[6:9], v[134:137], v[214:217], v[6:9]
	v_mfma_i32_16x16x64_i8 v[2:5], v[142:145], v[214:217], v[2:5]
	s_setprio 0
	s_barrier
	s_add_i32 s44, 0, 0x18000
	s_add_i32 s45, 0, 0x1c000
	v_add_u32_e32 v142, s44, v176
	v_add_u32_e32 v158, s45, v176
	ds_read_b128 v[130:133], v142
	ds_read_b128 v[134:137], v142 offset:1024
	ds_read_b128 v[138:141], v142 offset:2048
	ds_read_b128 v[142:145], v142 offset:3072
	ds_read_b128 v[146:149], v158
	ds_read_b128 v[150:153], v158 offset:1024
	ds_read_b128 v[154:157], v158 offset:2048
	ds_read_b128 v[158:161], v158 offset:3072
	v_mov_b32_e32 v162, v173
	s_mov_b32 m0, s53
	ds_read_b128 v[186:189], v180 offset:32768
	ds_read_b128 v[190:193], v180 offset:33792
	ds_read_b128 v[194:197], v180 offset:34816
	ds_read_b128 v[198:201], v180 offset:35840
	ds_read_b128 v[202:205], v180 offset:36864
	ds_read_b128 v[206:209], v180 offset:37888
	ds_read_b128 v[210:213], v180 offset:38912
	ds_read_b128 v[214:217], v180 offset:39936
	s_nop 0
	global_load_lds_dwordx4 v162, s[42:43]
	v_mov_b32_e32 v162, v174
	s_mov_b32 m0, s54
	s_nop 0
	global_load_lds_dwordx4 v162, s[42:43]
	s_waitcnt vmcnt(8)
	s_waitcnt lgkmcnt(0)
	s_barrier
	s_setprio 1
	s_waitcnt lgkmcnt(0)
	v_mfma_i32_16x16x64_i8 v[126:129], v[130:133], v[186:189], v[126:129]
	v_mfma_i32_16x16x64_i8 v[122:125], v[138:141], v[186:189], v[122:125]
	v_mfma_i32_16x16x64_i8 v[110:113], v[130:133], v[194:197], v[110:113]
	v_mfma_i32_16x16x64_i8 v[106:109], v[138:141], v[194:197], v[106:109]
	v_mfma_i32_16x16x64_i8 v[94:97], v[130:133], v[202:205], v[94:97]
	v_mfma_i32_16x16x64_i8 v[90:93], v[138:141], v[202:205], v[90:93]
	v_mfma_i32_16x16x64_i8 v[78:81], v[130:133], v[210:213], v[78:81]
	v_mfma_i32_16x16x64_i8 v[74:77], v[138:141], v[210:213], v[74:77]
	v_mfma_i32_16x16x64_i8 v[126:129], v[134:137], v[190:193], v[126:129]
	v_mfma_i32_16x16x64_i8 v[122:125], v[142:145], v[190:193], v[122:125]
	v_mfma_i32_16x16x64_i8 v[110:113], v[134:137], v[198:201], v[110:113]
	v_mfma_i32_16x16x64_i8 v[106:109], v[142:145], v[198:201], v[106:109]
	v_mfma_i32_16x16x64_i8 v[94:97], v[134:137], v[206:209], v[94:97]
	v_mfma_i32_16x16x64_i8 v[90:93], v[142:145], v[206:209], v[90:93]
	v_mfma_i32_16x16x64_i8 v[78:81], v[134:137], v[214:217], v[78:81]
	v_mfma_i32_16x16x64_i8 v[74:77], v[142:145], v[214:217], v[74:77]
	v_mfma_i32_16x16x64_i8 v[118:121], v[146:149], v[186:189], v[118:121]
	v_mfma_i32_16x16x64_i8 v[114:117], v[154:157], v[186:189], v[114:117]
	v_mfma_i32_16x16x64_i8 v[102:105], v[146:149], v[194:197], v[102:105]
	v_mfma_i32_16x16x64_i8 v[98:101], v[154:157], v[194:197], v[98:101]
	v_mfma_i32_16x16x64_i8 v[86:89], v[146:149], v[202:205], v[86:89]
	v_mfma_i32_16x16x64_i8 v[82:85], v[154:157], v[202:205], v[82:85]
	v_mfma_i32_16x16x64_i8 v[70:73], v[146:149], v[210:213], v[70:73]
	v_mfma_i32_16x16x64_i8 v[66:69], v[154:157], v[210:213], v[66:69]
	v_mfma_i32_16x16x64_i8 v[118:121], v[150:153], v[190:193], v[118:121]
	v_mfma_i32_16x16x64_i8 v[114:117], v[158:161], v[190:193], v[114:117]
	v_mfma_i32_16x16x64_i8 v[102:105], v[150:153], v[198:201], v[102:105]
	v_mfma_i32_16x16x64_i8 v[98:101], v[158:161], v[198:201], v[98:101]
	v_mfma_i32_16x16x64_i8 v[86:89], v[150:153], v[206:209], v[86:89]
	v_mfma_i32_16x16x64_i8 v[82:85], v[158:161], v[206:209], v[82:85]
	v_mfma_i32_16x16x64_i8 v[70:73], v[150:153], v[214:217], v[70:73]
	v_mfma_i32_16x16x64_i8 v[66:69], v[158:161], v[214:217], v[66:69]
	s_setprio 0
	s_barrier
; #define PG8_STAGE(bufoff, gbase, voff) do { _Pragma("unroll") for (int _i = 0; _i < 2; ++_i) { unsigned vo_ = (voff)[_i]; asm volatile("" : "+v"(vo_));   \
;         __builtin_amdgcn_global_load_lds((const unsigned*)((const char*)(gbase) + vo_), (LAS unsigned*)(lds + (bufoff) + ldsw + _i * 8192), 16, 0, 0); } } while (0)
; #define PG8_LDA(dst, b, h) do { _Pragma("unroll") for (int m = 0; m < 4; ++m) _Pragma("unroll") for (int k = 0; k < 2; ++k) dst[m][k] = *(const LAS bf16x8*)(lds + PG8_SA(b, h) + aoff + m * 2048 + k * 1024); } while (0)
; #define PG8_WAIT_V(n) asm volatile("s_waitcnt vmcnt(" #n ")" ::: "memory")
; #define PG8_WAIT_L(n) asm volatile("s_waitcnt lgkmcnt(" #n ")" ::: "memory")
; #define PG8_BAR __builtin_amdgcn_s_barrier()
; #define PG8_SCHED __builtin_amdgcn_sched_barrier(0)
;     ...
;             PG8_LDA(At, 1, 1); PG8_STAGE(PG8_SB(1, 0), b3, voffB); PG8_STAGE(PG8_SB(1, 1), b3 + hstepB, voffB); PG8_STAGE(PG8_SA(1, 0), a3, va[0]);
;             PG8_WAIT_V(8); PG8_WAIT_L(0); PG8_BAR; PG8_MMA(1, 0, At, B0); PG8_MMA(1, 1, At, B1); PG8_BAR; PG8_SCHED;
;         }
	v_mov_b32_e32 v162, v168
	ds_read_b128 v[186:189], v180 offset:49152
	ds_read_b128 v[190:193], v180 offset:50176
	ds_read_b128 v[194:197], v180 offset:51200
	ds_read_b128 v[198:201], v180 offset:52224
	ds_read_b128 v[202:205], v180 offset:53248
	ds_read_b128 v[206:209], v180 offset:54272
	ds_read_b128 v[210:213], v180 offset:55296
	ds_read_b128 v[214:217], v180 offset:56320
	s_add_i32 s44, s44, s38
	v_lshl_add_u64 v[218:219], s[34:35], 0, v[162:163]
	v_lshl_add_u64 v[218:219], v[218:219], 0, s[18:19]
	s_mov_b32 m0, s44
	v_mov_b32_e32 v162, v170
	global_load_lds_dwordx4 v[218:219], off
	s_add_i32 m0, s44, 0x2000
	s_nop 0
	v_lshl_add_u64 v[218:219], s[34:35], 0, v[162:163]
	s_add_u32 s34, s34, 0x40080
	v_lshl_add_u64 v[218:219], v[218:219], 0, s[18:19]
	s_addc_u32 s35, s35, 0
	v_mov_b32_e32 v162, v168
	s_add_i32 s44, s45, s38
	global_load_lds_dwordx4 v[218:219], off
	s_mov_b32 m0, s44
	s_nop 0
	global_load_lds_dwordx4 v162, s[34:35]
	v_mov_b32_e32 v162, v170
	s_add_i32 m0, s44, 0x2000
	s_nop 0
	global_load_lds_dwordx4 v162, s[34:35]
	v_mov_b32_e32 v162, v171
	s_mov_b32 m0, s56
	v_lshl_add_u64 v[218:219], s[42:43], 0, v[162:163]
	v_lshl_add_u64 v[218:219], v[218:219], 0, s[18:19]
	v_mov_b32_e32 v162, v172
	global_load_lds_dwordx4 v[218:219], off
	s_mov_b32 m0, s57
	v_lshl_add_u64 v[218:219], s[42:43], 0, v[162:163]
	v_lshl_add_u64 v[218:219], v[218:219], 0, s[18:19]
	global_load_lds_dwordx4 v[218:219], off
	s_waitcnt vmcnt(8)
	s_waitcnt lgkmcnt(0)
	s_barrier
	s_setprio 1
	s_waitcnt lgkmcnt(0)
	v_mfma_i32_16x16x64_i8 v[62:65], v[130:133], v[186:189], v[62:65]
	v_mfma_i32_16x16x64_i8 v[58:61], v[138:141], v[186:189], v[58:61]
	v_mfma_i32_16x16x64_i8 v[46:49], v[130:133], v[194:197], v[46:49]
	v_mfma_i32_16x16x64_i8 v[42:45], v[138:141], v[194:197], v[42:45]
	v_mfma_i32_16x16x64_i8 v[30:33], v[130:133], v[202:205], v[30:33]
	v_mfma_i32_16x16x64_i8 v[26:29], v[138:141], v[202:205], v[26:29]
	v_mfma_i32_16x16x64_i8 v[14:17], v[130:133], v[210:213], v[14:17]
	v_mfma_i32_16x16x64_i8 v[10:13], v[138:141], v[210:213], v[10:13]
	v_mfma_i32_16x16x64_i8 v[62:65], v[134:137], v[190:193], v[62:65]
	v_mfma_i32_16x16x64_i8 v[58:61], v[142:145], v[190:193], v[58:61]
	v_mfma_i32_16x16x64_i8 v[46:49], v[134:137], v[198:201], v[46:49]
	v_mfma_i32_16x16x64_i8 v[42:45], v[142:145], v[198:201], v[42:45]
	v_mfma_i32_16x16x64_i8 v[30:33], v[134:137], v[206:209], v[30:33]
	v_mfma_i32_16x16x64_i8 v[26:29], v[142:145], v[206:209], v[26:29]
	v_mfma_i32_16x16x64_i8 v[14:17], v[134:137], v[214:217], v[14:17]
	v_mfma_i32_16x16x64_i8 v[10:13], v[142:145], v[214:217], v[10:13]
	v_mfma_i32_16x16x64_i8 v[54:57], v[146:149], v[186:189], v[54:57]
	v_mfma_i32_16x16x64_i8 v[50:53], v[154:157], v[186:189], v[50:53]
	v_mfma_i32_16x16x64_i8 v[38:41], v[146:149], v[194:197], v[38:41]
	v_mfma_i32_16x16x64_i8 v[34:37], v[154:157], v[194:197], v[34:37]
	v_mfma_i32_16x16x64_i8 v[22:25], v[146:149], v[202:205], v[22:25]
	v_mfma_i32_16x16x64_i8 v[18:21], v[154:157], v[202:205], v[18:21]
	v_mfma_i32_16x16x64_i8 v[6:9], v[146:149], v[210:213], v[6:9]
	v_mfma_i32_16x16x64_i8 v[2:5], v[154:157], v[210:213], v[2:5]
	v_mfma_i32_16x16x64_i8 v[54:57], v[150:153], v[190:193], v[54:57]
	v_mfma_i32_16x16x64_i8 v[50:53], v[158:161], v[190:193], v[50:53]
	v_mfma_i32_16x16x64_i8 v[38:41], v[150:153], v[198:201], v[38:41]
	v_mfma_i32_16x16x64_i8 v[34:37], v[158:161], v[198:201], v[34:37]
	v_mfma_i32_16x16x64_i8 v[22:25], v[150:153], v[206:209], v[22:25]
	v_mfma_i32_16x16x64_i8 v[18:21], v[158:161], v[206:209], v[18:21]
	v_mfma_i32_16x16x64_i8 v[6:9], v[150:153], v[214:217], v[6:9]
	v_mfma_i32_16x16x64_i8 v[2:5], v[158:161], v[214:217], v[2:5]
	s_setprio 0
	s_barrier
	s_add_i32 s65, s65, 2
	s_cmp_gt_u32 s65, 13
	s_cbranch_scc1 .LBB0_1418
	s_mov_b64 s[34:35], s[40:41]
	s_branch .LBB0_1414

; #define PG8_STAGE(bufoff, gbase, voff) do { _Pragma("unroll") for (int _i = 0; _i < 2; ++_i) { unsigned vo_ = (voff)[_i]; asm volatile("" : "+v"(vo_));   \
;         __builtin_amdgcn_global_load_lds((const unsigned*)((const char*)(gbase) + vo_), (LAS unsigned*)(lds + (bufoff) + ldsw + _i * 8192), 16, 0, 0); } } while (0)
; #define PG8_LDA(dst, b, h) do { _Pragma("unroll") for (int m = 0; m < 4; ++m) _Pragma("unroll") for (int k = 0; k < 2; ++k) dst[m][k] = *(const LAS bf16x8*)(lds + PG8_SA(b, h) + aoff + m * 2048 + k * 1024); } while (0)
; #define PG8_LDB(dst, b, h) do { _Pragma("unroll") for (int n = 0; n < 2; ++n) _Pragma("unroll") for (int k = 0; k < 2; ++k) dst[n][k] = *(const LAS bf16x8*)(lds + PG8_SB(b, h) + boff + n * 2048 + k * 1024); } while (0)
; #define PG8_WAIT_V(n) asm volatile("s_waitcnt vmcnt(" #n ")" ::: "memory")
; #define PG8_WAIT_L(n) asm volatile("s_waitcnt lgkmcnt(" #n ")" ::: "memory")
; #define PG8_BAR __builtin_amdgcn_s_barrier()
; #define PG8_SCHED __builtin_amdgcn_sched_barrier(0)
;     ...
;         for (int t = 0; t < nt; t += 2) {
;             const bool last = (t == nt - 2);
;             const char* a1 = Abase + (size_t)(t + 1) * kstep;
;             const char* a2 = Abase + (last ? (size_t)0 : (size_t)(t + 2) * kstep); const char* b2 = last ? nB : cB + (size_t)(t + 2) * kstep;
;             const char* a3 = a2 + kstep; const char* b3 = b2 + kstep;
;             PG8_LDB(B0, 0, 0); PG8_LDB(B1, 0, 1); PG8_SCHED; PG8_LDA(At, 0, 0); PG8_STAGE(PG8_SA(1, 1), a1, va[1]);
;             PG8_WAIT_V(8); PG8_WAIT_L(0); PG8_BAR; PG8_MMA(0, 0, At, B0); PG8_MMA(0, 1, At, B1); PG8_BAR; PG8_SCHED;
;             if (last && has_next) { PG8_AOFFS(va, nxt); }
;             PG8_LDA(At, 0, 1); PG8_STAGE(PG8_SB(0, 0), b2, voffB); PG8_STAGE(PG8_SB(0, 1), b2 + hstepB, voffB); PG8_STAGE(PG8_SA(0, 0), a2, va[0]);
;             PG8_WAIT_V(8); PG8_WAIT_L(0); PG8_BAR; PG8_MMA(1, 0, At, B0); PG8_MMA(1, 1, At, B1); PG8_BAR; PG8_SCHED;
;             PG8_LDB(B0, 1, 0); PG8_LDB(B1, 1, 1); PG8_SCHED; PG8_LDA(At, 1, 0); PG8_STAGE(PG8_SA(0, 1), a2, va[1]);
;             PG8_WAIT_V(8); PG8_WAIT_L(0); PG8_BAR; PG8_MMA(0, 0, At, B0); PG8_MMA(0, 1, At, B1); PG8_BAR; PG8_SCHED;
.LBB0_1531:
	ds_read_b128 v[18:21], v228
	ds_read_b128 v[22:25], v228 offset:1024
	ds_read_b128 v[26:29], v228 offset:2048
	ds_read_b128 v[30:33], v228 offset:3072
	ds_read_b128 v[2:5], v229
	ds_read_b128 v[6:9], v229 offset:1024
	ds_read_b128 v[10:13], v229 offset:2048
	ds_read_b128 v[14:17], v229 offset:3072
	s_cmp_eq_u32 s67, 40
	s_cselect_b64 s[42:43], -1, 0
	v_mov_b32_e32 v194, v224
	s_add_u32 s30, s18, s40
	s_mov_b32 m0, s61
	ds_read_b128 v[58:61], v230
	ds_read_b128 v[62:65], v230 offset:1024
	ds_read_b128 v[50:53], v230 offset:2048
	ds_read_b128 v[54:57], v230 offset:3072
	ds_read_b128 v[42:45], v230 offset:4096
	ds_read_b128 v[46:49], v230 offset:5120
	ds_read_b128 v[34:37], v230 offset:6144
	ds_read_b128 v[38:41], v230 offset:7168
	s_addc_u32 s31, s19, s41
	global_load_lds_dwordx4 v194, s[30:31]
	v_mov_b32_e32 v194, v225
	s_add_i32 m0, s45, 0xe000
	s_nop 0
	global_load_lds_dwordx4 v194, s[30:31]
	s_waitcnt vmcnt(8)
	s_waitcnt lgkmcnt(0)
	s_barrier
	s_setprio 1
	s_waitcnt lgkmcnt(0)
	v_mfma_scale_f32_16x16x128_f8f6f4 v[190:193], v[18:25], v[58:65], v[190:193], v231, v231 op_sel_hi:[0,0,0]
	v_mfma_scale_f32_16x16x128_f8f6f4 v[186:189], v[26:33], v[58:65], v[186:189], v231, v231 op_sel_hi:[0,0,0]
	v_mfma_scale_f32_16x16x128_f8f6f4 v[174:177], v[18:25], v[50:57], v[174:177], v231, v231 op_sel_hi:[0,0,0]
	v_mfma_scale_f32_16x16x128_f8f6f4 v[170:173], v[26:33], v[50:57], v[170:173], v231, v231 op_sel_hi:[0,0,0]
	v_mfma_scale_f32_16x16x128_f8f6f4 v[158:161], v[18:25], v[42:49], v[158:161], v231, v231 op_sel_hi:[0,0,0]
	v_mfma_scale_f32_16x16x128_f8f6f4 v[154:157], v[26:33], v[42:49], v[154:157], v231, v231 op_sel_hi:[0,0,0]
	v_mfma_scale_f32_16x16x128_f8f6f4 v[142:145], v[18:25], v[34:41], v[142:145], v231, v231 op_sel_hi:[0,0,0]
	v_mfma_scale_f32_16x16x128_f8f6f4 v[138:141], v[26:33], v[34:41], v[138:141], v231, v231 op_sel_hi:[0,0,0]
	v_mfma_scale_f32_16x16x128_f8f6f4 v[182:185], v[2:9], v[58:65], v[182:185], v231, v231 op_sel_hi:[0,0,0]
	v_mfma_scale_f32_16x16x128_f8f6f4 v[178:181], v[10:17], v[58:65], v[178:181], v231, v231 op_sel_hi:[0,0,0]
	v_mfma_scale_f32_16x16x128_f8f6f4 v[166:169], v[2:9], v[50:57], v[166:169], v231, v231 op_sel_hi:[0,0,0]
	v_mfma_scale_f32_16x16x128_f8f6f4 v[162:165], v[10:17], v[50:57], v[162:165], v231, v231 op_sel_hi:[0,0,0]
	v_mfma_scale_f32_16x16x128_f8f6f4 v[150:153], v[2:9], v[42:49], v[150:153], v231, v231 op_sel_hi:[0,0,0]
	v_mfma_scale_f32_16x16x128_f8f6f4 v[146:149], v[10:17], v[42:49], v[146:149], v231, v231 op_sel_hi:[0,0,0]
	v_mfma_scale_f32_16x16x128_f8f6f4 v[134:137], v[2:9], v[34:41], v[134:137], v231, v231 op_sel_hi:[0,0,0]
	v_mfma_scale_f32_16x16x128_f8f6f4 v[130:133], v[10:17], v[34:41], v[130:133], v231, v231 op_sel_hi:[0,0,0]
	s_setprio 0
	s_barrier
	s_and_b64 s[30:31], s[28:29], s[42:43]
	s_andn2_b64 vcc, exec, s[30:31]
	s_cbranch_vccnz .LBB0_1533
	v_mov_b32_e32 v225, v235
	v_mov_b32_e32 v224, v234
	v_mov_b32_e32 v223, v233
	v_mov_b32_e32 v222, v232
.LBB0_1533:
	s_add_u32 s30, s40, 0x100
	s_addc_u32 s31, s41, 0
	s_and_b64 s[34:35], s[42:43], exec
	s_cselect_b32 s34, 0, s30
	s_cselect_b32 s35, 0, s31
	s_add_u32 s34, s4, s34
	s_addc_u32 s35, s5, s35
	s_add_u32 s68, s14, s40
	s_addc_u32 s69, s27, s41
	s_and_b64 s[40:41], s[42:43], exec
	v_mov_b32_e32 v194, v215
	s_waitcnt lgkmcnt(0)
	s_cselect_b32 s41, s25, s69
	s_cselect_b32 s40, s24, s68
	s_mov_b32 m0, s46
	s_add_u32 s42, s40, 0xb0000
	s_addc_u32 s43, s41, 0
	ds_read_b128 v[58:61], v230 offset:16384
	ds_read_b128 v[62:65], v230 offset:17408
	ds_read_b128 v[50:53], v230 offset:18432
	ds_read_b128 v[54:57], v230 offset:19456
	ds_read_b128 v[42:45], v230 offset:20480
	ds_read_b128 v[46:49], v230 offset:21504
	ds_read_b128 v[34:37], v230 offset:22528
	ds_read_b128 v[38:41], v230 offset:23552
	s_nop 0
	global_load_lds_dwordx4 v194, s[40:41]
	v_mov_b32_e32 v194, v217
	s_mov_b32 m0, s47
	s_nop 0
	global_load_lds_dwordx4 v194, s[40:41]
	v_mov_b32_e32 v194, v215
	s_mov_b32 m0, s48
	s_nop 0
	global_load_lds_dwordx4 v194, s[42:43]
	v_mov_b32_e32 v194, v217
	s_mov_b32 m0, s49
	s_nop 0
	global_load_lds_dwordx4 v194, s[42:43]
	v_mov_b32_e32 v194, v222
	s_mov_b32 m0, s45
	s_nop 0
	global_load_lds_dwordx4 v194, s[34:35]
	v_mov_b32_e32 v194, v223
	s_mov_b32 m0, s50
	s_nop 0
	global_load_lds_dwordx4 v194, s[34:35]
	s_waitcnt vmcnt(8)
	s_waitcnt lgkmcnt(0)
	s_barrier
	s_setprio 1
	s_waitcnt lgkmcnt(0)
	v_mfma_scale_f32_16x16x128_f8f6f4 v[126:129], v[18:25], v[58:65], v[126:129], v231, v231 op_sel_hi:[0,0,0]
	v_mfma_scale_f32_16x16x128_f8f6f4 v[122:125], v[26:33], v[58:65], v[122:125], v231, v231 op_sel_hi:[0,0,0]
	v_mfma_scale_f32_16x16x128_f8f6f4 v[114:117], v[18:25], v[50:57], v[114:117], v231, v231 op_sel_hi:[0,0,0]
	v_mfma_scale_f32_16x16x128_f8f6f4 v[106:109], v[26:33], v[50:57], v[106:109], v231, v231 op_sel_hi:[0,0,0]
	v_mfma_scale_f32_16x16x128_f8f6f4 v[98:101], v[18:25], v[42:49], v[98:101], v231, v231 op_sel_hi:[0,0,0]
	v_mfma_scale_f32_16x16x128_f8f6f4 v[90:93], v[26:33], v[42:49], v[90:93], v231, v231 op_sel_hi:[0,0,0]
	v_mfma_scale_f32_16x16x128_f8f6f4 v[82:85], v[18:25], v[34:41], v[82:85], v231, v231 op_sel_hi:[0,0,0]
	v_mfma_scale_f32_16x16x128_f8f6f4 v[74:77], v[26:33], v[34:41], v[74:77], v231, v231 op_sel_hi:[0,0,0]
	v_mfma_scale_f32_16x16x128_f8f6f4 v[118:121], v[2:9], v[58:65], v[118:121], v231, v231 op_sel_hi:[0,0,0]
	v_mfma_scale_f32_16x16x128_f8f6f4 v[110:113], v[10:17], v[58:65], v[110:113], v231, v231 op_sel_hi:[0,0,0]
	v_mfma_scale_f32_16x16x128_f8f6f4 v[102:105], v[2:9], v[50:57], v[102:105], v231, v231 op_sel_hi:[0,0,0]
	v_mfma_scale_f32_16x16x128_f8f6f4 v[94:97], v[10:17], v[50:57], v[94:97], v231, v231 op_sel_hi:[0,0,0]
	v_mfma_scale_f32_16x16x128_f8f6f4 v[86:89], v[2:9], v[42:49], v[86:89], v231, v231 op_sel_hi:[0,0,0]
	v_mfma_scale_f32_16x16x128_f8f6f4 v[78:81], v[10:17], v[42:49], v[78:81], v231, v231 op_sel_hi:[0,0,0]
	v_mfma_scale_f32_16x16x128_f8f6f4 v[70:73], v[2:9], v[34:41], v[70:73], v231, v231 op_sel_hi:[0,0,0]
	v_mfma_scale_f32_16x16x128_f8f6f4 v[66:69], v[10:17], v[34:41], v[66:69], v231, v231 op_sel_hi:[0,0,0]
	s_setprio 0
	s_barrier
; #define PG8_STAGE(bufoff, gbase, voff) do { _Pragma("unroll") for (int _i = 0; _i < 2; ++_i) { unsigned vo_ = (voff)[_i]; asm volatile("" : "+v"(vo_));   \
;         __builtin_amdgcn_global_load_lds((const unsigned*)((const char*)(gbase) + vo_), (LAS unsigned*)(lds + (bufoff) + ldsw + _i * 8192), 16, 0, 0); } } while (0)
; #define PG8_LDA(dst, b, h) do { _Pragma("unroll") for (int m = 0; m < 4; ++m) _Pragma("unroll") for (int k = 0; k < 2; ++k) dst[m][k] = *(const LAS bf16x8*)(lds + PG8_SA(b, h) + aoff + m * 2048 + k * 1024); } while (0)
; #define PG8_LDB(dst, b, h) do { _Pragma("unroll") for (int n = 0; n < 2; ++n) _Pragma("unroll") for (int k = 0; k < 2; ++k) dst[n][k] = *(const LAS bf16x8*)(lds + PG8_SB(b, h) + boff + n * 2048 + k * 1024); } while (0)
; #define PG8_WAIT_V(n) asm volatile("s_waitcnt vmcnt(" #n ")" ::: "memory")
; #define PG8_WAIT_L(n) asm volatile("s_waitcnt lgkmcnt(" #n ")" ::: "memory")
; #define PG8_BAR __builtin_amdgcn_s_barrier()
; #define PG8_SCHED __builtin_amdgcn_sched_barrier(0)
;     ...
;             PG8_LDB(B0, 1, 0); PG8_LDB(B1, 1, 1); PG8_SCHED; PG8_LDA(At, 1, 0); PG8_STAGE(PG8_SA(0, 1), a2, va[1]);
;             PG8_WAIT_V(8); PG8_WAIT_L(0); PG8_BAR; PG8_MMA(0, 0, At, B0); PG8_MMA(0, 1, At, B1); PG8_BAR; PG8_SCHED;
;             PG8_LDA(At, 1, 1); PG8_STAGE(PG8_SB(1, 0), b3, voffB); PG8_STAGE(PG8_SB(1, 1), b3 + hstepB, voffB); PG8_STAGE(PG8_SA(1, 0), a3, va[0]);
;             PG8_WAIT_V(8); PG8_WAIT_L(0); PG8_BAR; PG8_MMA(1, 0, At, B0); PG8_MMA(1, 1, At, B1); PG8_BAR; PG8_SCHED;
;         }
	s_add_i32 s42, 0, 0x18000
	s_add_i32 s43, 0, 0x1c000
	v_add_u32_e32 v14, s42, v226
	v_add_u32_e32 v30, s43, v226
	ds_read_b128 v[2:5], v14
	ds_read_b128 v[6:9], v14 offset:1024
	ds_read_b128 v[10:13], v14 offset:2048
	ds_read_b128 v[14:17], v14 offset:3072
	ds_read_b128 v[18:21], v30
	ds_read_b128 v[22:25], v30 offset:1024
	ds_read_b128 v[26:29], v30 offset:2048
	ds_read_b128 v[30:33], v30 offset:3072
	v_mov_b32_e32 v194, v224
	s_mov_b32 m0, s51
	ds_read_b128 v[34:37], v230 offset:32768
	ds_read_b128 v[38:41], v230 offset:33792
	ds_read_b128 v[42:45], v230 offset:34816
	ds_read_b128 v[46:49], v230 offset:35840
	ds_read_b128 v[50:53], v230 offset:36864
	ds_read_b128 v[54:57], v230 offset:37888
	ds_read_b128 v[58:61], v230 offset:38912
	ds_read_b128 v[62:65], v230 offset:39936
	s_nop 0
	global_load_lds_dwordx4 v194, s[34:35]
	v_mov_b32_e32 v194, v225
	s_mov_b32 m0, s52
	s_nop 0
	global_load_lds_dwordx4 v194, s[34:35]
	s_waitcnt vmcnt(8)
	s_waitcnt lgkmcnt(0)
	s_barrier
	s_setprio 1
	s_waitcnt lgkmcnt(0)
	v_mfma_scale_f32_16x16x128_f8f6f4 v[190:193], v[2:9], v[34:41], v[190:193], v231, v231 op_sel_hi:[0,0,0]
	v_mfma_scale_f32_16x16x128_f8f6f4 v[186:189], v[10:17], v[34:41], v[186:189], v231, v231 op_sel_hi:[0,0,0]
	v_mfma_scale_f32_16x16x128_f8f6f4 v[174:177], v[2:9], v[42:49], v[174:177], v231, v231 op_sel_hi:[0,0,0]
	v_mfma_scale_f32_16x16x128_f8f6f4 v[170:173], v[10:17], v[42:49], v[170:173], v231, v231 op_sel_hi:[0,0,0]
	v_mfma_scale_f32_16x16x128_f8f6f4 v[158:161], v[2:9], v[50:57], v[158:161], v231, v231 op_sel_hi:[0,0,0]
	v_mfma_scale_f32_16x16x128_f8f6f4 v[154:157], v[10:17], v[50:57], v[154:157], v231, v231 op_sel_hi:[0,0,0]
	v_mfma_scale_f32_16x16x128_f8f6f4 v[142:145], v[2:9], v[58:65], v[142:145], v231, v231 op_sel_hi:[0,0,0]
	v_mfma_scale_f32_16x16x128_f8f6f4 v[138:141], v[10:17], v[58:65], v[138:141], v231, v231 op_sel_hi:[0,0,0]
	v_mfma_scale_f32_16x16x128_f8f6f4 v[182:185], v[18:25], v[34:41], v[182:185], v231, v231 op_sel_hi:[0,0,0]
	v_mfma_scale_f32_16x16x128_f8f6f4 v[178:181], v[26:33], v[34:41], v[178:181], v231, v231 op_sel_hi:[0,0,0]
	v_mfma_scale_f32_16x16x128_f8f6f4 v[166:169], v[18:25], v[42:49], v[166:169], v231, v231 op_sel_hi:[0,0,0]
	v_mfma_scale_f32_16x16x128_f8f6f4 v[162:165], v[26:33], v[42:49], v[162:165], v231, v231 op_sel_hi:[0,0,0]
	v_mfma_scale_f32_16x16x128_f8f6f4 v[150:153], v[18:25], v[50:57], v[150:153], v231, v231 op_sel_hi:[0,0,0]
	v_mfma_scale_f32_16x16x128_f8f6f4 v[146:149], v[26:33], v[50:57], v[146:149], v231, v231 op_sel_hi:[0,0,0]
	v_mfma_scale_f32_16x16x128_f8f6f4 v[134:137], v[18:25], v[58:65], v[134:137], v231, v231 op_sel_hi:[0,0,0]
	v_mfma_scale_f32_16x16x128_f8f6f4 v[130:133], v[26:33], v[58:65], v[130:133], v231, v231 op_sel_hi:[0,0,0]
	s_setprio 0
	s_barrier
	v_mov_b32_e32 v194, v215
	ds_read_b128 v[34:37], v230 offset:49152
	ds_read_b128 v[38:41], v230 offset:50176
	ds_read_b128 v[42:45], v230 offset:51200
	ds_read_b128 v[46:49], v230 offset:52224
	ds_read_b128 v[50:53], v230 offset:53248
	ds_read_b128 v[54:57], v230 offset:54272
	ds_read_b128 v[58:61], v230 offset:55296
	ds_read_b128 v[62:65], v230 offset:56320
	s_add_i32 s42, s42, s38
	v_lshl_add_u64 v[236:237], s[40:41], 0, v[194:195]
	v_lshl_add_u64 v[236:237], v[236:237], 0, s[16:17]
	s_mov_b32 m0, s42
	v_mov_b32_e32 v194, v217
	global_load_lds_dwordx4 v[236:237], off
	s_add_i32 m0, s42, 0x2000
	s_nop 0
	v_lshl_add_u64 v[236:237], s[40:41], 0, v[194:195]
	s_add_u32 s40, s40, 0xb0080
	v_lshl_add_u64 v[236:237], v[236:237], 0, s[16:17]
	s_addc_u32 s41, s41, 0
	v_mov_b32_e32 v194, v215
	s_add_i32 s42, s43, s38
	global_load_lds_dwordx4 v[236:237], off
	s_mov_b32 m0, s42
	s_nop 0
	global_load_lds_dwordx4 v194, s[40:41]
	v_mov_b32_e32 v194, v217
	s_add_i32 m0, s42, 0x2000
	s_nop 0
	global_load_lds_dwordx4 v194, s[40:41]
	v_mov_b32_e32 v194, v222
	s_mov_b32 m0, s59
	v_lshl_add_u64 v[236:237], s[34:35], 0, v[194:195]
	v_lshl_add_u64 v[236:237], v[236:237], 0, s[16:17]
	v_mov_b32_e32 v194, v223
	global_load_lds_dwordx4 v[236:237], off
	s_mov_b32 m0, s60
	v_lshl_add_u64 v[236:237], s[34:35], 0, v[194:195]
	v_lshl_add_u64 v[236:237], v[236:237], 0, s[16:17]
	global_load_lds_dwordx4 v[236:237], off
	s_waitcnt vmcnt(8)
	s_waitcnt lgkmcnt(0)
	s_barrier
	s_setprio 1
	s_waitcnt lgkmcnt(0)
	v_mfma_scale_f32_16x16x128_f8f6f4 v[126:129], v[2:9], v[34:41], v[126:129], v231, v231 op_sel_hi:[0,0,0]
	v_mfma_scale_f32_16x16x128_f8f6f4 v[122:125], v[10:17], v[34:41], v[122:125], v231, v231 op_sel_hi:[0,0,0]
	v_mfma_scale_f32_16x16x128_f8f6f4 v[114:117], v[2:9], v[42:49], v[114:117], v231, v231 op_sel_hi:[0,0,0]
	v_mfma_scale_f32_16x16x128_f8f6f4 v[106:109], v[10:17], v[42:49], v[106:109], v231, v231 op_sel_hi:[0,0,0]
	v_mfma_scale_f32_16x16x128_f8f6f4 v[98:101], v[2:9], v[50:57], v[98:101], v231, v231 op_sel_hi:[0,0,0]
	v_mfma_scale_f32_16x16x128_f8f6f4 v[90:93], v[10:17], v[50:57], v[90:93], v231, v231 op_sel_hi:[0,0,0]
	v_mfma_scale_f32_16x16x128_f8f6f4 v[82:85], v[2:9], v[58:65], v[82:85], v231, v231 op_sel_hi:[0,0,0]
	v_mfma_scale_f32_16x16x128_f8f6f4 v[74:77], v[10:17], v[58:65], v[74:77], v231, v231 op_sel_hi:[0,0,0]
	v_mfma_scale_f32_16x16x128_f8f6f4 v[118:121], v[18:25], v[34:41], v[118:121], v231, v231 op_sel_hi:[0,0,0]
	v_mfma_scale_f32_16x16x128_f8f6f4 v[110:113], v[26:33], v[34:41], v[110:113], v231, v231 op_sel_hi:[0,0,0]
	v_mfma_scale_f32_16x16x128_f8f6f4 v[102:105], v[18:25], v[42:49], v[102:105], v231, v231 op_sel_hi:[0,0,0]
	v_mfma_scale_f32_16x16x128_f8f6f4 v[94:97], v[26:33], v[42:49], v[94:97], v231, v231 op_sel_hi:[0,0,0]
	v_mfma_scale_f32_16x16x128_f8f6f4 v[86:89], v[18:25], v[50:57], v[86:89], v231, v231 op_sel_hi:[0,0,0]
	v_mfma_scale_f32_16x16x128_f8f6f4 v[78:81], v[26:33], v[50:57], v[78:81], v231, v231 op_sel_hi:[0,0,0]
	v_mfma_scale_f32_16x16x128_f8f6f4 v[70:73], v[18:25], v[58:65], v[70:73], v231, v231 op_sel_hi:[0,0,0]
	v_mfma_scale_f32_16x16x128_f8f6f4 v[66:69], v[26:33], v[58:65], v[66:69], v231, v231 op_sel_hi:[0,0,0]
	s_setprio 0
	s_barrier
	s_add_i32 s67, s67, 2
	s_cmp_gt_u32 s67, 41
	s_cbranch_scc1 .LBB0_1535
	s_mov_b64 s[40:41], s[30:31]
	s_branch .LBB0_1531

; #define PG8_STAGE(bufoff, gbase, voff) do { _Pragma("unroll") for (int _i = 0; _i < 2; ++_i) { unsigned vo_ = (voff)[_i]; asm volatile("" : "+v"(vo_));   \
;         __builtin_amdgcn_global_load_lds((const unsigned*)((const char*)(gbase) + vo_), (LAS unsigned*)(lds + (bufoff) + ldsw + _i * 8192), 16, 0, 0); } } while (0)
; #define PG8_LDA(dst, b, h) do { _Pragma("unroll") for (int m = 0; m < 4; ++m) _Pragma("unroll") for (int k = 0; k < 2; ++k) dst[m][k] = *(const LAS bf16x8*)(lds + PG8_SA(b, h) + aoff + m * 2048 + k * 1024); } while (0)
; #define PG8_LDB(dst, b, h) do { _Pragma("unroll") for (int n = 0; n < 2; ++n) _Pragma("unroll") for (int k = 0; k < 2; ++k) dst[n][k] = *(const LAS bf16x8*)(lds + PG8_SB(b, h) + boff + n * 2048 + k * 1024); } while (0)
; #define PG8_WAIT_V(n) asm volatile("s_waitcnt vmcnt(" #n ")" ::: "memory")
; #define PG8_WAIT_L(n) asm volatile("s_waitcnt lgkmcnt(" #n ")" ::: "memory")
; #define PG8_BAR __builtin_amdgcn_s_barrier()
; #define PG8_SCHED __builtin_amdgcn_sched_barrier(0)
;     ...
;         for (int t = 0; t < nt; t += 2) {
;             const bool last = (t == nt - 2);
;             const char* a1 = Abase + (size_t)(t + 1) * kstep;
;             const char* a2 = Abase + (last ? (size_t)0 : (size_t)(t + 2) * kstep); const char* b2 = last ? nB : cB + (size_t)(t + 2) * kstep;
;             const char* a3 = a2 + kstep; const char* b3 = b2 + kstep;
;             PG8_LDB(B0, 0, 0); PG8_LDB(B1, 0, 1); PG8_SCHED; PG8_LDA(At, 0, 0); PG8_STAGE(PG8_SA(1, 1), a1, va[1]);
;             PG8_WAIT_V(8); PG8_WAIT_L(0); PG8_BAR; PG8_MMA(0, 0, At, B0); PG8_MMA(0, 1, At, B1); PG8_BAR; PG8_SCHED;
;             if (last && has_next) { PG8_AOFFS(va, nxt); }
;             PG8_LDA(At, 0, 1); PG8_STAGE(PG8_SB(0, 0), b2, voffB); PG8_STAGE(PG8_SB(0, 1), b2 + hstepB, voffB); PG8_STAGE(PG8_SA(0, 0), a2, va[0]);
;             PG8_WAIT_V(8); PG8_WAIT_L(0); PG8_BAR; PG8_MMA(1, 0, At, B0); PG8_MMA(1, 1, At, B1); PG8_BAR; PG8_SCHED;
;             PG8_LDB(B0, 1, 0); PG8_LDB(B1, 1, 1); PG8_SCHED; PG8_LDA(At, 1, 0); PG8_STAGE(PG8_SA(0, 1), a2, va[1]);
;             PG8_WAIT_V(8); PG8_WAIT_L(0); PG8_BAR; PG8_MMA(0, 0, At, B0); PG8_MMA(0, 1, At, B1); PG8_BAR; PG8_SCHED;
.LBB0_1564:
	ds_read_b128 v[18:21], v220
	ds_read_b128 v[22:25], v220 offset:1024
	ds_read_b128 v[26:29], v220 offset:2048
	ds_read_b128 v[30:33], v220 offset:3072
	ds_read_b128 v[2:5], v221
	ds_read_b128 v[6:9], v221 offset:1024
	ds_read_b128 v[10:13], v221 offset:2048
	ds_read_b128 v[14:17], v221 offset:3072
	s_cmp_eq_u32 s27, s71
	s_cselect_b64 s[48:49], -1, 0
	s_add_i32 m0, s51, 0xc000
	v_mov_b32_e32 v194, v224
	s_add_u32 s42, s16, s46
	ds_read_b128 v[58:61], v226
	ds_read_b128 v[62:65], v226 offset:1024
	ds_read_b128 v[50:53], v226 offset:2048
	ds_read_b128 v[54:57], v226 offset:3072
	ds_read_b128 v[42:45], v226 offset:4096
	ds_read_b128 v[46:49], v226 offset:5120
	ds_read_b128 v[34:37], v226 offset:6144
	ds_read_b128 v[38:41], v226 offset:7168
	s_addc_u32 s43, s17, s47
	global_load_lds_dwordx4 v194, s[42:43]
	v_mov_b32_e32 v194, v225
	s_add_i32 m0, s51, 0xe000
	s_nop 0
	global_load_lds_dwordx4 v194, s[42:43]
	s_waitcnt vmcnt(8)
	s_waitcnt lgkmcnt(0)
	s_barrier
	s_setprio 1
	s_waitcnt lgkmcnt(0)
	v_mfma_scale_f32_16x16x128_f8f6f4 v[178:181], v[18:25], v[58:65], v[178:181], v227, v227 op_sel_hi:[0,0,0]
	v_mfma_scale_f32_16x16x128_f8f6f4 v[182:185], v[26:33], v[58:65], v[182:185], v227, v227 op_sel_hi:[0,0,0]
	v_mfma_scale_f32_16x16x128_f8f6f4 v[174:177], v[18:25], v[50:57], v[174:177], v227, v227 op_sel_hi:[0,0,0]
	v_mfma_scale_f32_16x16x128_f8f6f4 v[166:169], v[26:33], v[50:57], v[166:169], v227, v227 op_sel_hi:[0,0,0]
	v_mfma_scale_f32_16x16x128_f8f6f4 v[162:165], v[18:25], v[42:49], v[162:165], v227, v227 op_sel_hi:[0,0,0]
	v_mfma_scale_f32_16x16x128_f8f6f4 v[154:157], v[26:33], v[42:49], v[154:157], v227, v227 op_sel_hi:[0,0,0]
	v_mfma_scale_f32_16x16x128_f8f6f4 v[150:153], v[18:25], v[34:41], v[150:153], v227, v227 op_sel_hi:[0,0,0]
	v_mfma_scale_f32_16x16x128_f8f6f4 v[142:145], v[26:33], v[34:41], v[142:145], v227, v227 op_sel_hi:[0,0,0]
	v_mfma_scale_f32_16x16x128_f8f6f4 v[186:189], v[2:9], v[58:65], v[186:189], v227, v227 op_sel_hi:[0,0,0]
	v_mfma_scale_f32_16x16x128_f8f6f4 v[190:193], v[10:17], v[58:65], v[190:193], v227, v227 op_sel_hi:[0,0,0]
	v_mfma_scale_f32_16x16x128_f8f6f4 v[170:173], v[2:9], v[50:57], v[170:173], v227, v227 op_sel_hi:[0,0,0]
	v_mfma_scale_f32_16x16x128_f8f6f4 v[158:161], v[10:17], v[50:57], v[158:161], v227, v227 op_sel_hi:[0,0,0]
	v_mfma_scale_f32_16x16x128_f8f6f4 v[146:149], v[2:9], v[42:49], v[146:149], v227, v227 op_sel_hi:[0,0,0]
	v_mfma_scale_f32_16x16x128_f8f6f4 v[138:141], v[10:17], v[42:49], v[138:141], v227, v227 op_sel_hi:[0,0,0]
	v_mfma_scale_f32_16x16x128_f8f6f4 v[134:137], v[2:9], v[34:41], v[134:137], v227, v227 op_sel_hi:[0,0,0]
	v_mfma_scale_f32_16x16x128_f8f6f4 v[130:133], v[10:17], v[34:41], v[130:133], v227, v227 op_sel_hi:[0,0,0]
	s_setprio 0
	s_barrier
	s_and_b64 s[42:43], s[40:41], s[48:49]
	s_andn2_b64 vcc, exec, s[42:43]
	s_cbranch_vccnz .LBB0_1566
	v_mov_b32_e32 v225, v231
	v_mov_b32_e32 v224, v230
	v_mov_b32_e32 v223, v229
	v_mov_b32_e32 v222, v228
.LBB0_1566:
	s_add_i32 s71, s71, 2
	s_add_u32 s42, s46, 0x100
	s_addc_u32 s43, s47, 0
	s_and_b64 s[44:45], s[48:49], exec
	s_cselect_b32 s44, 0, s42
	s_cselect_b32 s45, 0, s43
	s_add_u32 s44, s4, s44
	s_addc_u32 s45, s5, s45
	s_add_u32 s72, s69, s46
	s_addc_u32 s73, s70, s47
	s_and_b64 s[46:47], s[48:49], exec
	v_mov_b32_e32 v194, v215
	s_waitcnt lgkmcnt(0)
	s_cselect_b32 s47, s29, s73
	s_cselect_b32 s46, s28, s72
	s_mov_b32 m0, s52
	s_add_u32 s48, s46, 0xb0000
	s_addc_u32 s49, s47, 0
	ds_read_b128 v[58:61], v226 offset:16384
	ds_read_b128 v[62:65], v226 offset:17408
	ds_read_b128 v[50:53], v226 offset:18432
	ds_read_b128 v[54:57], v226 offset:19456
	ds_read_b128 v[42:45], v226 offset:20480
	ds_read_b128 v[46:49], v226 offset:21504
	ds_read_b128 v[34:37], v226 offset:22528
	ds_read_b128 v[38:41], v226 offset:23552
	s_nop 0
	global_load_lds_dwordx4 v194, s[46:47]
	v_mov_b32_e32 v194, v217
	s_mov_b32 m0, s53
	s_nop 0
	global_load_lds_dwordx4 v194, s[46:47]
	v_mov_b32_e32 v194, v215
	s_mov_b32 m0, s54
	s_nop 0
	global_load_lds_dwordx4 v194, s[48:49]
	v_mov_b32_e32 v194, v217
	s_mov_b32 m0, s55
	s_nop 0
	global_load_lds_dwordx4 v194, s[48:49]
	v_mov_b32_e32 v194, v222
	s_mov_b32 m0, s51
	s_nop 0
	global_load_lds_dwordx4 v194, s[44:45]
	v_mov_b32_e32 v194, v223
	s_mov_b32 m0, s56
	s_nop 0
	global_load_lds_dwordx4 v194, s[44:45]
	s_waitcnt vmcnt(8)
	s_waitcnt lgkmcnt(0)
	s_barrier
	s_setprio 1
	s_waitcnt lgkmcnt(0)
	v_mfma_scale_f32_16x16x128_f8f6f4 v[126:129], v[18:25], v[58:65], v[126:129], v227, v227 op_sel_hi:[0,0,0]
	v_mfma_scale_f32_16x16x128_f8f6f4 v[122:125], v[26:33], v[58:65], v[122:125], v227, v227 op_sel_hi:[0,0,0]
	v_mfma_scale_f32_16x16x128_f8f6f4 v[114:117], v[18:25], v[50:57], v[114:117], v227, v227 op_sel_hi:[0,0,0]
	v_mfma_scale_f32_16x16x128_f8f6f4 v[110:113], v[26:33], v[50:57], v[110:113], v227, v227 op_sel_hi:[0,0,0]
	v_mfma_scale_f32_16x16x128_f8f6f4 v[102:105], v[18:25], v[42:49], v[102:105], v227, v227 op_sel_hi:[0,0,0]
	v_mfma_scale_f32_16x16x128_f8f6f4 v[94:97], v[26:33], v[42:49], v[94:97], v227, v227 op_sel_hi:[0,0,0]
	v_mfma_scale_f32_16x16x128_f8f6f4 v[86:89], v[18:25], v[34:41], v[86:89], v227, v227 op_sel_hi:[0,0,0]
	v_mfma_scale_f32_16x16x128_f8f6f4 v[78:81], v[26:33], v[34:41], v[78:81], v227, v227 op_sel_hi:[0,0,0]
	v_mfma_scale_f32_16x16x128_f8f6f4 v[118:121], v[2:9], v[58:65], v[118:121], v227, v227 op_sel_hi:[0,0,0]
	v_mfma_scale_f32_16x16x128_f8f6f4 v[106:109], v[10:17], v[58:65], v[106:109], v227, v227 op_sel_hi:[0,0,0]
	v_mfma_scale_f32_16x16x128_f8f6f4 v[98:101], v[2:9], v[50:57], v[98:101], v227, v227 op_sel_hi:[0,0,0]
	v_mfma_scale_f32_16x16x128_f8f6f4 v[90:93], v[10:17], v[50:57], v[90:93], v227, v227 op_sel_hi:[0,0,0]
	v_mfma_scale_f32_16x16x128_f8f6f4 v[82:85], v[2:9], v[42:49], v[82:85], v227, v227 op_sel_hi:[0,0,0]
	v_mfma_scale_f32_16x16x128_f8f6f4 v[74:77], v[10:17], v[42:49], v[74:77], v227, v227 op_sel_hi:[0,0,0]
	v_mfma_scale_f32_16x16x128_f8f6f4 v[70:73], v[2:9], v[34:41], v[70:73], v227, v227 op_sel_hi:[0,0,0]
	v_mfma_scale_f32_16x16x128_f8f6f4 v[66:69], v[10:17], v[34:41], v[66:69], v227, v227 op_sel_hi:[0,0,0]
	s_setprio 0
	s_barrier
; #define PG8_STAGE(bufoff, gbase, voff) do { _Pragma("unroll") for (int _i = 0; _i < 2; ++_i) { unsigned vo_ = (voff)[_i]; asm volatile("" : "+v"(vo_));   \
;         __builtin_amdgcn_global_load_lds((const unsigned*)((const char*)(gbase) + vo_), (LAS unsigned*)(lds + (bufoff) + ldsw + _i * 8192), 16, 0, 0); } } while (0)
; #define PG8_LDA(dst, b, h) do { _Pragma("unroll") for (int m = 0; m < 4; ++m) _Pragma("unroll") for (int k = 0; k < 2; ++k) dst[m][k] = *(const LAS bf16x8*)(lds + PG8_SA(b, h) + aoff + m * 2048 + k * 1024); } while (0)
; #define PG8_LDB(dst, b, h) do { _Pragma("unroll") for (int n = 0; n < 2; ++n) _Pragma("unroll") for (int k = 0; k < 2; ++k) dst[n][k] = *(const LAS bf16x8*)(lds + PG8_SB(b, h) + boff + n * 2048 + k * 1024); } while (0)
; #define PG8_WAIT_V(n) asm volatile("s_waitcnt vmcnt(" #n ")" ::: "memory")
; #define PG8_WAIT_L(n) asm volatile("s_waitcnt lgkmcnt(" #n ")" ::: "memory")
; #define PG8_BAR __builtin_amdgcn_s_barrier()
; #define PG8_SCHED __builtin_amdgcn_sched_barrier(0)
;     ...
;             PG8_LDB(B0, 1, 0); PG8_LDB(B1, 1, 1); PG8_SCHED; PG8_LDA(At, 1, 0); PG8_STAGE(PG8_SA(0, 1), a2, va[1]);
;             PG8_WAIT_V(8); PG8_WAIT_L(0); PG8_BAR; PG8_MMA(0, 0, At, B0); PG8_MMA(0, 1, At, B1); PG8_BAR; PG8_SCHED;
;             PG8_LDA(At, 1, 1); PG8_STAGE(PG8_SB(1, 0), b3, voffB); PG8_STAGE(PG8_SB(1, 1), b3 + hstepB, voffB); PG8_STAGE(PG8_SA(1, 0), a3, va[0]);
;             PG8_WAIT_V(8); PG8_WAIT_L(0); PG8_BAR; PG8_MMA(1, 0, At, B0); PG8_MMA(1, 1, At, B1); PG8_BAR; PG8_SCHED;
;         }
	s_add_i32 s48, 0, 0x18000
	s_add_i32 s49, 0, 0x1c000
	v_add_u32_e32 v14, s48, v219
	v_add_u32_e32 v30, s49, v219
	ds_read_b128 v[2:5], v14
	ds_read_b128 v[6:9], v14 offset:1024
	ds_read_b128 v[10:13], v14 offset:2048
	ds_read_b128 v[14:17], v14 offset:3072
	ds_read_b128 v[18:21], v30
	ds_read_b128 v[22:25], v30 offset:1024
	ds_read_b128 v[26:29], v30 offset:2048
	ds_read_b128 v[30:33], v30 offset:3072
	v_mov_b32_e32 v194, v224
	s_mov_b32 m0, s57
	ds_read_b128 v[34:37], v226 offset:32768
	ds_read_b128 v[38:41], v226 offset:33792
	ds_read_b128 v[42:45], v226 offset:34816
	ds_read_b128 v[46:49], v226 offset:35840
	ds_read_b128 v[50:53], v226 offset:36864
	ds_read_b128 v[54:57], v226 offset:37888
	ds_read_b128 v[58:61], v226 offset:38912
	ds_read_b128 v[62:65], v226 offset:39936
	s_nop 0
	global_load_lds_dwordx4 v194, s[44:45]
	v_mov_b32_e32 v194, v225
	s_mov_b32 m0, s58
	s_nop 0
	global_load_lds_dwordx4 v194, s[44:45]
	s_waitcnt vmcnt(8)
	s_waitcnt lgkmcnt(0)
	s_barrier
	s_setprio 1
	s_waitcnt lgkmcnt(0)
	v_mfma_scale_f32_16x16x128_f8f6f4 v[178:181], v[2:9], v[34:41], v[178:181], v227, v227 op_sel_hi:[0,0,0]
	v_mfma_scale_f32_16x16x128_f8f6f4 v[182:185], v[10:17], v[34:41], v[182:185], v227, v227 op_sel_hi:[0,0,0]
	v_mfma_scale_f32_16x16x128_f8f6f4 v[174:177], v[2:9], v[42:49], v[174:177], v227, v227 op_sel_hi:[0,0,0]
	v_mfma_scale_f32_16x16x128_f8f6f4 v[166:169], v[10:17], v[42:49], v[166:169], v227, v227 op_sel_hi:[0,0,0]
	v_mfma_scale_f32_16x16x128_f8f6f4 v[162:165], v[2:9], v[50:57], v[162:165], v227, v227 op_sel_hi:[0,0,0]
	v_mfma_scale_f32_16x16x128_f8f6f4 v[154:157], v[10:17], v[50:57], v[154:157], v227, v227 op_sel_hi:[0,0,0]
	v_mfma_scale_f32_16x16x128_f8f6f4 v[150:153], v[2:9], v[58:65], v[150:153], v227, v227 op_sel_hi:[0,0,0]
	v_mfma_scale_f32_16x16x128_f8f6f4 v[142:145], v[10:17], v[58:65], v[142:145], v227, v227 op_sel_hi:[0,0,0]
	v_mfma_scale_f32_16x16x128_f8f6f4 v[186:189], v[18:25], v[34:41], v[186:189], v227, v227 op_sel_hi:[0,0,0]
	v_mfma_scale_f32_16x16x128_f8f6f4 v[190:193], v[26:33], v[34:41], v[190:193], v227, v227 op_sel_hi:[0,0,0]
	v_mfma_scale_f32_16x16x128_f8f6f4 v[170:173], v[18:25], v[42:49], v[170:173], v227, v227 op_sel_hi:[0,0,0]
	v_mfma_scale_f32_16x16x128_f8f6f4 v[158:161], v[26:33], v[42:49], v[158:161], v227, v227 op_sel_hi:[0,0,0]
	v_mfma_scale_f32_16x16x128_f8f6f4 v[146:149], v[18:25], v[50:57], v[146:149], v227, v227 op_sel_hi:[0,0,0]
	v_mfma_scale_f32_16x16x128_f8f6f4 v[138:141], v[26:33], v[50:57], v[138:141], v227, v227 op_sel_hi:[0,0,0]
	v_mfma_scale_f32_16x16x128_f8f6f4 v[134:137], v[18:25], v[58:65], v[134:137], v227, v227 op_sel_hi:[0,0,0]
	v_mfma_scale_f32_16x16x128_f8f6f4 v[130:133], v[26:33], v[58:65], v[130:133], v227, v227 op_sel_hi:[0,0,0]
	s_setprio 0
	s_barrier
	v_mov_b32_e32 v194, v215
	ds_read_b128 v[34:37], v226 offset:49152
	ds_read_b128 v[38:41], v226 offset:50176
	ds_read_b128 v[42:45], v226 offset:51200
	ds_read_b128 v[46:49], v226 offset:52224
	ds_read_b128 v[50:53], v226 offset:53248
	ds_read_b128 v[54:57], v226 offset:54272
	ds_read_b128 v[58:61], v226 offset:55296
	ds_read_b128 v[62:65], v226 offset:56320
	s_add_i32 s48, s48, s38
	v_lshl_add_u64 v[232:233], s[46:47], 0, v[194:195]
	v_lshl_add_u64 v[232:233], v[232:233], 0, s[14:15]
	s_mov_b32 m0, s48
	v_mov_b32_e32 v194, v217
	global_load_lds_dwordx4 v[232:233], off
	s_add_i32 m0, s48, 0x2000
	s_nop 0
	v_lshl_add_u64 v[232:233], s[46:47], 0, v[194:195]
	s_add_u32 s46, s46, 0xb0080
	v_lshl_add_u64 v[232:233], v[232:233], 0, s[14:15]
	s_addc_u32 s47, s47, 0
	v_mov_b32_e32 v194, v215
	s_add_i32 s48, s49, s38
	global_load_lds_dwordx4 v[232:233], off
	s_mov_b32 m0, s48
	s_nop 0
	global_load_lds_dwordx4 v194, s[46:47]
	v_mov_b32_e32 v194, v217
	s_add_i32 m0, s48, 0x2000
	s_nop 0
	global_load_lds_dwordx4 v194, s[46:47]
	v_mov_b32_e32 v194, v222
	s_mov_b32 m0, s62
	v_lshl_add_u64 v[232:233], s[44:45], 0, v[194:195]
	v_lshl_add_u64 v[232:233], v[232:233], 0, s[14:15]
	v_mov_b32_e32 v194, v223
	global_load_lds_dwordx4 v[232:233], off
	s_mov_b32 m0, s63
	v_lshl_add_u64 v[232:233], s[44:45], 0, v[194:195]
	v_lshl_add_u64 v[232:233], v[232:233], 0, s[14:15]
	global_load_lds_dwordx4 v[232:233], off
	s_waitcnt vmcnt(8)
	s_waitcnt lgkmcnt(0)
	s_barrier
	s_setprio 1
	s_waitcnt lgkmcnt(0)
	v_mfma_scale_f32_16x16x128_f8f6f4 v[126:129], v[2:9], v[34:41], v[126:129], v227, v227 op_sel_hi:[0,0,0]
	v_mfma_scale_f32_16x16x128_f8f6f4 v[122:125], v[10:17], v[34:41], v[122:125], v227, v227 op_sel_hi:[0,0,0]
	v_mfma_scale_f32_16x16x128_f8f6f4 v[114:117], v[2:9], v[42:49], v[114:117], v227, v227 op_sel_hi:[0,0,0]
	v_mfma_scale_f32_16x16x128_f8f6f4 v[110:113], v[10:17], v[42:49], v[110:113], v227, v227 op_sel_hi:[0,0,0]
	v_mfma_scale_f32_16x16x128_f8f6f4 v[102:105], v[2:9], v[50:57], v[102:105], v227, v227 op_sel_hi:[0,0,0]
	v_mfma_scale_f32_16x16x128_f8f6f4 v[94:97], v[10:17], v[50:57], v[94:97], v227, v227 op_sel_hi:[0,0,0]
	v_mfma_scale_f32_16x16x128_f8f6f4 v[86:89], v[2:9], v[58:65], v[86:89], v227, v227 op_sel_hi:[0,0,0]
	v_mfma_scale_f32_16x16x128_f8f6f4 v[78:81], v[10:17], v[58:65], v[78:81], v227, v227 op_sel_hi:[0,0,0]
	v_mfma_scale_f32_16x16x128_f8f6f4 v[118:121], v[18:25], v[34:41], v[118:121], v227, v227 op_sel_hi:[0,0,0]
	v_mfma_scale_f32_16x16x128_f8f6f4 v[106:109], v[26:33], v[34:41], v[106:109], v227, v227 op_sel_hi:[0,0,0]
	v_mfma_scale_f32_16x16x128_f8f6f4 v[98:101], v[18:25], v[42:49], v[98:101], v227, v227 op_sel_hi:[0,0,0]
	v_mfma_scale_f32_16x16x128_f8f6f4 v[90:93], v[26:33], v[42:49], v[90:93], v227, v227 op_sel_hi:[0,0,0]
	v_mfma_scale_f32_16x16x128_f8f6f4 v[82:85], v[18:25], v[50:57], v[82:85], v227, v227 op_sel_hi:[0,0,0]
	v_mfma_scale_f32_16x16x128_f8f6f4 v[74:77], v[26:33], v[50:57], v[74:77], v227, v227 op_sel_hi:[0,0,0]
	v_mfma_scale_f32_16x16x128_f8f6f4 v[70:73], v[18:25], v[58:65], v[70:73], v227, v227 op_sel_hi:[0,0,0]
	v_mfma_scale_f32_16x16x128_f8f6f4 v[66:69], v[26:33], v[58:65], v[66:69], v227, v227 op_sel_hi:[0,0,0]
	s_setprio 0
	s_barrier
	s_cmp_ge_i32 s71, s35
	s_cbranch_scc1 .LBB0_1568
	s_mov_b64 s[46:47], s[42:43]
	s_branch .LBB0_1564

; #define PG8_STAGE(bufoff, gbase, voff) do { _Pragma("unroll") for (int _i = 0; _i < 2; ++_i) { unsigned vo_ = (voff)[_i]; asm volatile("" : "+v"(vo_));   \
;         __builtin_amdgcn_global_load_lds((const unsigned*)((const char*)(gbase) + vo_), (LAS unsigned*)(lds + (bufoff) + ldsw + _i * 8192), 16, 0, 0); } } while (0)
; #define PG8_LDA(dst, b, h) do { _Pragma("unroll") for (int m = 0; m < 4; ++m) _Pragma("unroll") for (int k = 0; k < 2; ++k) dst[m][k] = *(const LAS bf16x8*)(lds + PG8_SA(b, h) + aoff + m * 2048 + k * 1024); } while (0)
; #define PG8_LDB(dst, b, h) do { _Pragma("unroll") for (int n = 0; n < 2; ++n) _Pragma("unroll") for (int k = 0; k < 2; ++k) dst[n][k] = *(const LAS bf16x8*)(lds + PG8_SB(b, h) + boff + n * 2048 + k * 1024); } while (0)
; #define PG8_WAIT_V(n) asm volatile("s_waitcnt vmcnt(" #n ")" ::: "memory")
; #define PG8_WAIT_L(n) asm volatile("s_waitcnt lgkmcnt(" #n ")" ::: "memory")
; #define PG8_BAR __builtin_amdgcn_s_barrier()
; #define PG8_SCHED __builtin_amdgcn_sched_barrier(0)
;     ...
;         for (int t = 0; t < nt; t += 2) {
;             const bool last = (t == nt - 2);
;             const char* a1 = Abase + (size_t)(t + 1) * kstep;
;             const char* a2 = Abase + (last ? (size_t)0 : (size_t)(t + 2) * kstep); const char* b2 = last ? nB : cB + (size_t)(t + 2) * kstep;
;             const char* a3 = a2 + kstep; const char* b3 = b2 + kstep;
;             PG8_LDB(B0, 0, 0); PG8_LDB(B1, 0, 1); PG8_SCHED; PG8_LDA(At, 0, 0); PG8_STAGE(PG8_SA(1, 1), a1, va[1]);
;             PG8_WAIT_V(8); PG8_WAIT_L(0); PG8_BAR; PG8_MMA(0, 0, At, B0); PG8_MMA(0, 1, At, B1); PG8_BAR; PG8_SCHED;
;             if (last && has_next) { PG8_AOFFS(va, nxt); }
;             PG8_LDA(At, 0, 1); PG8_STAGE(PG8_SB(0, 0), b2, voffB); PG8_STAGE(PG8_SB(0, 1), b2 + hstepB, voffB); PG8_STAGE(PG8_SA(0, 0), a2, va[0]);
;             PG8_WAIT_V(8); PG8_WAIT_L(0); PG8_BAR; PG8_MMA(1, 0, At, B0); PG8_MMA(1, 1, At, B1); PG8_BAR; PG8_SCHED;
;             PG8_LDB(B0, 1, 0); PG8_LDB(B1, 1, 1); PG8_SCHED; PG8_LDA(At, 1, 0); PG8_STAGE(PG8_SA(0, 1), a2, va[1]);
;             PG8_WAIT_V(8); PG8_WAIT_L(0); PG8_BAR; PG8_MMA(0, 0, At, B0); PG8_MMA(0, 1, At, B1); PG8_BAR; PG8_SCHED;
.LBB0_1754:
	ds_read_b128 v[146:149], v183
	ds_read_b128 v[150:153], v183 offset:1024
	ds_read_b128 v[154:157], v183 offset:2048
	ds_read_b128 v[158:161], v183 offset:3072
	ds_read_b128 v[130:133], v184
	ds_read_b128 v[134:137], v184 offset:1024
	ds_read_b128 v[138:141], v184 offset:2048
	ds_read_b128 v[142:145], v184 offset:3072
	s_cmp_eq_u32 s87, 12
	s_cselect_b64 s[66:67], -1, 0
	s_add_i32 m0, s61, 0xc000
	v_mov_b32_e32 v162, v177
	s_add_u32 s62, s28, s6
	ds_read_b128 v[192:195], v185
	ds_read_b128 v[196:199], v185 offset:1024
	ds_read_b128 v[200:203], v185 offset:2048
	ds_read_b128 v[204:207], v185 offset:3072
	ds_read_b128 v[208:211], v185 offset:4096
	ds_read_b128 v[212:215], v185 offset:5120
	ds_read_b128 v[216:219], v185 offset:6144
	ds_read_b128 v[220:223], v185 offset:7168
	s_addc_u32 s63, s29, s7
	global_load_lds_dwordx4 v162, s[62:63]
	v_mov_b32_e32 v162, v178
	s_add_i32 m0, s61, 0xe000
	s_nop 0
	global_load_lds_dwordx4 v162, s[62:63]
	s_waitcnt vmcnt(8)
	s_waitcnt lgkmcnt(0)
	s_barrier
	s_setprio 1
	s_waitcnt lgkmcnt(0)
	v_mfma_i32_16x16x64_i8 v[126:129], v[146:149], v[192:195], v[126:129]
	v_mfma_i32_16x16x64_i8 v[122:125], v[154:157], v[192:195], v[122:125]
	v_mfma_i32_16x16x64_i8 v[110:113], v[146:149], v[200:203], v[110:113]
	v_mfma_i32_16x16x64_i8 v[106:109], v[154:157], v[200:203], v[106:109]
	v_mfma_i32_16x16x64_i8 v[94:97], v[146:149], v[208:211], v[94:97]
	v_mfma_i32_16x16x64_i8 v[90:93], v[154:157], v[208:211], v[90:93]
	v_mfma_i32_16x16x64_i8 v[78:81], v[146:149], v[216:219], v[78:81]
	v_mfma_i32_16x16x64_i8 v[74:77], v[154:157], v[216:219], v[74:77]
	v_mfma_i32_16x16x64_i8 v[126:129], v[150:153], v[196:199], v[126:129]
	v_mfma_i32_16x16x64_i8 v[122:125], v[158:161], v[196:199], v[122:125]
	v_mfma_i32_16x16x64_i8 v[110:113], v[150:153], v[204:207], v[110:113]
	v_mfma_i32_16x16x64_i8 v[106:109], v[158:161], v[204:207], v[106:109]
	v_mfma_i32_16x16x64_i8 v[94:97], v[150:153], v[212:215], v[94:97]
	v_mfma_i32_16x16x64_i8 v[90:93], v[158:161], v[212:215], v[90:93]
	v_mfma_i32_16x16x64_i8 v[78:81], v[150:153], v[220:223], v[78:81]
	v_mfma_i32_16x16x64_i8 v[74:77], v[158:161], v[220:223], v[74:77]
	v_mfma_i32_16x16x64_i8 v[118:121], v[130:133], v[192:195], v[118:121]
	v_mfma_i32_16x16x64_i8 v[114:117], v[138:141], v[192:195], v[114:117]
	v_mfma_i32_16x16x64_i8 v[102:105], v[130:133], v[200:203], v[102:105]
	v_mfma_i32_16x16x64_i8 v[98:101], v[138:141], v[200:203], v[98:101]
	v_mfma_i32_16x16x64_i8 v[86:89], v[130:133], v[208:211], v[86:89]
	v_mfma_i32_16x16x64_i8 v[82:85], v[138:141], v[208:211], v[82:85]
	v_mfma_i32_16x16x64_i8 v[70:73], v[130:133], v[216:219], v[70:73]
	v_mfma_i32_16x16x64_i8 v[66:69], v[138:141], v[216:219], v[66:69]
	v_mfma_i32_16x16x64_i8 v[118:121], v[134:137], v[196:199], v[118:121]
	v_mfma_i32_16x16x64_i8 v[114:117], v[142:145], v[196:199], v[114:117]
	v_mfma_i32_16x16x64_i8 v[102:105], v[134:137], v[204:207], v[102:105]
	v_mfma_i32_16x16x64_i8 v[98:101], v[142:145], v[204:207], v[98:101]
	v_mfma_i32_16x16x64_i8 v[86:89], v[134:137], v[212:215], v[86:89]
	v_mfma_i32_16x16x64_i8 v[82:85], v[142:145], v[212:215], v[82:85]
	v_mfma_i32_16x16x64_i8 v[70:73], v[134:137], v[220:223], v[70:73]
	v_mfma_i32_16x16x64_i8 v[66:69], v[142:145], v[220:223], v[66:69]
	s_setprio 0
	s_barrier
	s_and_b64 s[62:63], s[58:59], s[66:67]
	s_andn2_b64 vcc, exec, s[62:63]
	s_cbranch_vccnz .LBB0_1756
	v_mov_b32_e32 v178, v191
	v_mov_b32_e32 v177, v190
	v_mov_b32_e32 v176, v189
	v_mov_b32_e32 v175, v188
.LBB0_1756:
	s_add_u32 s62, s6, 0x100
	s_addc_u32 s63, s7, 0
	s_and_b64 s[64:65], s[66:67], exec
	s_cselect_b32 s64, 0, s62
	s_cselect_b32 s65, 0, s63
	s_add_u32 s64, s14, s64
	s_addc_u32 s65, s15, s65
	s_add_u32 vcc_lo, s55, s6
	s_addc_u32 vcc_hi, s86, s7
	s_and_b64 s[6:7], s[66:67], exec
	v_mov_b32_e32 v162, v172
	s_mov_b32 m0, s70
	s_cselect_b32 s7, s57, vcc_hi
	s_cselect_b32 s6, s56, vcc_lo
	ds_read_b128 v[192:195], v185 offset:16384
	ds_read_b128 v[196:199], v185 offset:17408
	ds_read_b128 v[200:203], v185 offset:18432
	ds_read_b128 v[204:207], v185 offset:19456
	ds_read_b128 v[208:211], v185 offset:20480
	ds_read_b128 v[212:215], v185 offset:21504
	ds_read_b128 v[216:219], v185 offset:22528
	ds_read_b128 v[220:223], v185 offset:23552
	s_add_u32 s66, s6, 0x40000
	global_load_lds_dwordx4 v162, s[6:7]
	v_mov_b32_e32 v162, v174
	s_mov_b32 m0, s71
	s_addc_u32 s67, s7, 0
	global_load_lds_dwordx4 v162, s[6:7]
	v_mov_b32_e32 v162, v172
	s_mov_b32 m0, s72
	s_nop 0
	global_load_lds_dwordx4 v162, s[66:67]
	v_mov_b32_e32 v162, v174
	s_mov_b32 m0, s73
	s_nop 0
	global_load_lds_dwordx4 v162, s[66:67]
	v_mov_b32_e32 v162, v175
	s_mov_b32 m0, s61
	s_nop 0
	global_load_lds_dwordx4 v162, s[64:65]
	v_mov_b32_e32 v162, v176
	s_mov_b32 m0, s74
	s_nop 0
	global_load_lds_dwordx4 v162, s[64:65]
	s_waitcnt vmcnt(8)
	s_waitcnt lgkmcnt(0)
	s_barrier
; #define PG8_STAGE(bufoff, gbase, voff) do { _Pragma("unroll") for (int _i = 0; _i < 2; ++_i) { unsigned vo_ = (voff)[_i]; asm volatile("" : "+v"(vo_));   \
;         __builtin_amdgcn_global_load_lds((const unsigned*)((const char*)(gbase) + vo_), (LAS unsigned*)(lds + (bufoff) + ldsw + _i * 8192), 16, 0, 0); } } while (0)
; #define PG8_LDA(dst, b, h) do { _Pragma("unroll") for (int m = 0; m < 4; ++m) _Pragma("unroll") for (int k = 0; k < 2; ++k) dst[m][k] = *(const LAS bf16x8*)(lds + PG8_SA(b, h) + aoff + m * 2048 + k * 1024); } while (0)
; #define PG8_LDB(dst, b, h) do { _Pragma("unroll") for (int n = 0; n < 2; ++n) _Pragma("unroll") for (int k = 0; k < 2; ++k) dst[n][k] = *(const LAS bf16x8*)(lds + PG8_SB(b, h) + boff + n * 2048 + k * 1024); } while (0)
; #define PG8_WAIT_V(n) asm volatile("s_waitcnt vmcnt(" #n ")" ::: "memory")
; #define PG8_WAIT_L(n) asm volatile("s_waitcnt lgkmcnt(" #n ")" ::: "memory")
; #define PG8_BAR __builtin_amdgcn_s_barrier()
; #define PG8_SCHED __builtin_amdgcn_sched_barrier(0)
;     ...
;             PG8_WAIT_V(8); PG8_WAIT_L(0); PG8_BAR; PG8_MMA(1, 0, At, B0); PG8_MMA(1, 1, At, B1); PG8_BAR; PG8_SCHED;
;             PG8_LDB(B0, 1, 0); PG8_LDB(B1, 1, 1); PG8_SCHED; PG8_LDA(At, 1, 0); PG8_STAGE(PG8_SA(0, 1), a2, va[1]);
;             PG8_WAIT_V(8); PG8_WAIT_L(0); PG8_BAR; PG8_MMA(0, 0, At, B0); PG8_MMA(0, 1, At, B1); PG8_BAR; PG8_SCHED;
	s_setprio 1
	s_waitcnt lgkmcnt(0)
	v_mfma_i32_16x16x64_i8 v[62:65], v[146:149], v[192:195], v[62:65]
	v_mfma_i32_16x16x64_i8 v[58:61], v[154:157], v[192:195], v[58:61]
	v_mfma_i32_16x16x64_i8 v[46:49], v[146:149], v[200:203], v[46:49]
	v_mfma_i32_16x16x64_i8 v[42:45], v[154:157], v[200:203], v[42:45]
	v_mfma_i32_16x16x64_i8 v[30:33], v[146:149], v[208:211], v[30:33]
	v_mfma_i32_16x16x64_i8 v[26:29], v[154:157], v[208:211], v[26:29]
	v_mfma_i32_16x16x64_i8 v[14:17], v[146:149], v[216:219], v[14:17]
	v_mfma_i32_16x16x64_i8 v[10:13], v[154:157], v[216:219], v[10:13]
	v_mfma_i32_16x16x64_i8 v[62:65], v[150:153], v[196:199], v[62:65]
	v_mfma_i32_16x16x64_i8 v[58:61], v[158:161], v[196:199], v[58:61]
	v_mfma_i32_16x16x64_i8 v[46:49], v[150:153], v[204:207], v[46:49]
	v_mfma_i32_16x16x64_i8 v[42:45], v[158:161], v[204:207], v[42:45]
	v_mfma_i32_16x16x64_i8 v[30:33], v[150:153], v[212:215], v[30:33]
	v_mfma_i32_16x16x64_i8 v[26:29], v[158:161], v[212:215], v[26:29]
	v_mfma_i32_16x16x64_i8 v[14:17], v[150:153], v[220:223], v[14:17]
	v_mfma_i32_16x16x64_i8 v[10:13], v[158:161], v[220:223], v[10:13]
	v_mfma_i32_16x16x64_i8 v[54:57], v[130:133], v[192:195], v[54:57]
	v_mfma_i32_16x16x64_i8 v[50:53], v[138:141], v[192:195], v[50:53]
	v_mfma_i32_16x16x64_i8 v[38:41], v[130:133], v[200:203], v[38:41]
	v_mfma_i32_16x16x64_i8 v[34:37], v[138:141], v[200:203], v[34:37]
	v_mfma_i32_16x16x64_i8 v[22:25], v[130:133], v[208:211], v[22:25]
	v_mfma_i32_16x16x64_i8 v[18:21], v[138:141], v[208:211], v[18:21]
	v_mfma_i32_16x16x64_i8 v[6:9], v[130:133], v[216:219], v[6:9]
	v_mfma_i32_16x16x64_i8 v[2:5], v[138:141], v[216:219], v[2:5]
	v_mfma_i32_16x16x64_i8 v[54:57], v[134:137], v[196:199], v[54:57]
	v_mfma_i32_16x16x64_i8 v[50:53], v[142:145], v[196:199], v[50:53]
	v_mfma_i32_16x16x64_i8 v[38:41], v[134:137], v[204:207], v[38:41]
	v_mfma_i32_16x16x64_i8 v[34:37], v[142:145], v[204:207], v[34:37]
	v_mfma_i32_16x16x64_i8 v[22:25], v[134:137], v[212:215], v[22:25]
	v_mfma_i32_16x16x64_i8 v[18:21], v[142:145], v[212:215], v[18:21]
	v_mfma_i32_16x16x64_i8 v[6:9], v[134:137], v[220:223], v[6:9]
	v_mfma_i32_16x16x64_i8 v[2:5], v[142:145], v[220:223], v[2:5]
	s_setprio 0
	s_barrier
	s_add_i32 s66, 0, 0x18000
	s_add_i32 s67, 0, 0x1c000
	v_add_u32_e32 v142, s66, v181
	v_add_u32_e32 v158, s67, v181
	ds_read_b128 v[130:133], v142
	ds_read_b128 v[134:137], v142 offset:1024
	ds_read_b128 v[138:141], v142 offset:2048
	ds_read_b128 v[142:145], v142 offset:3072
	ds_read_b128 v[146:149], v158
	ds_read_b128 v[150:153], v158 offset:1024
	ds_read_b128 v[154:157], v158 offset:2048
	ds_read_b128 v[158:161], v158 offset:3072
	v_mov_b32_e32 v162, v177
	s_mov_b32 m0, s75
	ds_read_b128 v[192:195], v185 offset:32768
	ds_read_b128 v[196:199], v185 offset:33792
	ds_read_b128 v[200:203], v185 offset:34816
	ds_read_b128 v[204:207], v185 offset:35840
	ds_read_b128 v[208:211], v185 offset:36864
	ds_read_b128 v[212:215], v185 offset:37888
	ds_read_b128 v[216:219], v185 offset:38912
	ds_read_b128 v[220:223], v185 offset:39936
	s_nop 0
	global_load_lds_dwordx4 v162, s[64:65]
	v_mov_b32_e32 v162, v178
	s_mov_b32 m0, s76
	s_nop 0
	global_load_lds_dwordx4 v162, s[64:65]
	s_waitcnt vmcnt(8)
	s_waitcnt lgkmcnt(0)
	s_barrier
	s_setprio 1
	s_waitcnt lgkmcnt(0)
	v_mfma_i32_16x16x64_i8 v[126:129], v[130:133], v[192:195], v[126:129]
	v_mfma_i32_16x16x64_i8 v[122:125], v[138:141], v[192:195], v[122:125]
	v_mfma_i32_16x16x64_i8 v[110:113], v[130:133], v[200:203], v[110:113]
	v_mfma_i32_16x16x64_i8 v[106:109], v[138:141], v[200:203], v[106:109]
	v_mfma_i32_16x16x64_i8 v[94:97], v[130:133], v[208:211], v[94:97]
	v_mfma_i32_16x16x64_i8 v[90:93], v[138:141], v[208:211], v[90:93]
	v_mfma_i32_16x16x64_i8 v[78:81], v[130:133], v[216:219], v[78:81]
	v_mfma_i32_16x16x64_i8 v[74:77], v[138:141], v[216:219], v[74:77]
	v_mfma_i32_16x16x64_i8 v[126:129], v[134:137], v[196:199], v[126:129]
	v_mfma_i32_16x16x64_i8 v[122:125], v[142:145], v[196:199], v[122:125]
	v_mfma_i32_16x16x64_i8 v[110:113], v[134:137], v[204:207], v[110:113]
	v_mfma_i32_16x16x64_i8 v[106:109], v[142:145], v[204:207], v[106:109]
	v_mfma_i32_16x16x64_i8 v[94:97], v[134:137], v[212:215], v[94:97]
	v_mfma_i32_16x16x64_i8 v[90:93], v[142:145], v[212:215], v[90:93]
	v_mfma_i32_16x16x64_i8 v[78:81], v[134:137], v[220:223], v[78:81]
	v_mfma_i32_16x16x64_i8 v[74:77], v[142:145], v[220:223], v[74:77]
	v_mfma_i32_16x16x64_i8 v[118:121], v[146:149], v[192:195], v[118:121]
	v_mfma_i32_16x16x64_i8 v[114:117], v[154:157], v[192:195], v[114:117]
	v_mfma_i32_16x16x64_i8 v[102:105], v[146:149], v[200:203], v[102:105]
	v_mfma_i32_16x16x64_i8 v[98:101], v[154:157], v[200:203], v[98:101]
	v_mfma_i32_16x16x64_i8 v[86:89], v[146:149], v[208:211], v[86:89]
	v_mfma_i32_16x16x64_i8 v[82:85], v[154:157], v[208:211], v[82:85]
	v_mfma_i32_16x16x64_i8 v[70:73], v[146:149], v[216:219], v[70:73]
	v_mfma_i32_16x16x64_i8 v[66:69], v[154:157], v[216:219], v[66:69]
	v_mfma_i32_16x16x64_i8 v[118:121], v[150:153], v[196:199], v[118:121]
	v_mfma_i32_16x16x64_i8 v[114:117], v[158:161], v[196:199], v[114:117]
	v_mfma_i32_16x16x64_i8 v[102:105], v[150:153], v[204:207], v[102:105]
	v_mfma_i32_16x16x64_i8 v[98:101], v[158:161], v[204:207], v[98:101]
	v_mfma_i32_16x16x64_i8 v[86:89], v[150:153], v[212:215], v[86:89]
	v_mfma_i32_16x16x64_i8 v[82:85], v[158:161], v[212:215], v[82:85]
	v_mfma_i32_16x16x64_i8 v[70:73], v[150:153], v[220:223], v[70:73]
	v_mfma_i32_16x16x64_i8 v[66:69], v[158:161], v[220:223], v[66:69]
	s_setprio 0
	s_barrier
; #define PG8_STAGE(bufoff, gbase, voff) do { _Pragma("unroll") for (int _i = 0; _i < 2; ++_i) { unsigned vo_ = (voff)[_i]; asm volatile("" : "+v"(vo_));   \
;         __builtin_amdgcn_global_load_lds((const unsigned*)((const char*)(gbase) + vo_), (LAS unsigned*)(lds + (bufoff) + ldsw + _i * 8192), 16, 0, 0); } } while (0)
; #define PG8_LDA(dst, b, h) do { _Pragma("unroll") for (int m = 0; m < 4; ++m) _Pragma("unroll") for (int k = 0; k < 2; ++k) dst[m][k] = *(const LAS bf16x8*)(lds + PG8_SA(b, h) + aoff + m * 2048 + k * 1024); } while (0)
; #define PG8_WAIT_V(n) asm volatile("s_waitcnt vmcnt(" #n ")" ::: "memory")
; #define PG8_WAIT_L(n) asm volatile("s_waitcnt lgkmcnt(" #n ")" ::: "memory")
; #define PG8_BAR __builtin_amdgcn_s_barrier()
; #define PG8_SCHED __builtin_amdgcn_sched_barrier(0)
;     ...
;             PG8_LDA(At, 1, 1); PG8_STAGE(PG8_SB(1, 0), b3, voffB); PG8_STAGE(PG8_SB(1, 1), b3 + hstepB, voffB); PG8_STAGE(PG8_SA(1, 0), a3, va[0]);
;             PG8_WAIT_V(8); PG8_WAIT_L(0); PG8_BAR; PG8_MMA(1, 0, At, B0); PG8_MMA(1, 1, At, B1); PG8_BAR; PG8_SCHED;
;         }
	v_mov_b32_e32 v162, v172
	ds_read_b128 v[192:195], v185 offset:49152
	ds_read_b128 v[196:199], v185 offset:50176
	ds_read_b128 v[200:203], v185 offset:51200
	ds_read_b128 v[204:207], v185 offset:52224
	ds_read_b128 v[208:211], v185 offset:53248
	ds_read_b128 v[212:215], v185 offset:54272
	ds_read_b128 v[216:219], v185 offset:55296
	ds_read_b128 v[220:223], v185 offset:56320
	s_add_i32 s66, s66, s69
	v_lshl_add_u64 v[224:225], s[6:7], 0, v[162:163]
	v_lshl_add_u64 v[224:225], v[224:225], 0, s[26:27]
	s_mov_b32 m0, s66
	v_mov_b32_e32 v162, v174
	global_load_lds_dwordx4 v[224:225], off
	s_add_i32 m0, s66, 0x2000
	s_nop 0
	v_lshl_add_u64 v[224:225], s[6:7], 0, v[162:163]
	s_add_u32 s6, s6, 0x40080
	v_lshl_add_u64 v[224:225], v[224:225], 0, s[26:27]
	s_addc_u32 s7, s7, 0
	v_mov_b32_e32 v162, v172
	s_add_i32 s66, s67, s69
	global_load_lds_dwordx4 v[224:225], off
	s_mov_b32 m0, s66
	s_nop 0
	global_load_lds_dwordx4 v162, s[6:7]
	v_mov_b32_e32 v162, v174
	s_add_i32 m0, s66, 0x2000
	s_nop 0
	global_load_lds_dwordx4 v162, s[6:7]
	v_mov_b32_e32 v162, v175
	s_mov_b32 m0, s78
	v_lshl_add_u64 v[224:225], s[64:65], 0, v[162:163]
	v_lshl_add_u64 v[224:225], v[224:225], 0, s[26:27]
	v_mov_b32_e32 v162, v176
	global_load_lds_dwordx4 v[224:225], off
	s_mov_b32 m0, s79
	v_lshl_add_u64 v[224:225], s[64:65], 0, v[162:163]
	v_lshl_add_u64 v[224:225], v[224:225], 0, s[26:27]
	global_load_lds_dwordx4 v[224:225], off
	s_waitcnt vmcnt(8)
	s_waitcnt lgkmcnt(0)
	s_barrier
	s_setprio 1
	s_waitcnt lgkmcnt(0)
	v_mfma_i32_16x16x64_i8 v[62:65], v[130:133], v[192:195], v[62:65]
	v_mfma_i32_16x16x64_i8 v[58:61], v[138:141], v[192:195], v[58:61]
	v_mfma_i32_16x16x64_i8 v[46:49], v[130:133], v[200:203], v[46:49]
	v_mfma_i32_16x16x64_i8 v[42:45], v[138:141], v[200:203], v[42:45]
	v_mfma_i32_16x16x64_i8 v[30:33], v[130:133], v[208:211], v[30:33]
	v_mfma_i32_16x16x64_i8 v[26:29], v[138:141], v[208:211], v[26:29]
	v_mfma_i32_16x16x64_i8 v[14:17], v[130:133], v[216:219], v[14:17]
	v_mfma_i32_16x16x64_i8 v[10:13], v[138:141], v[216:219], v[10:13]
	v_mfma_i32_16x16x64_i8 v[62:65], v[134:137], v[196:199], v[62:65]
	v_mfma_i32_16x16x64_i8 v[58:61], v[142:145], v[196:199], v[58:61]
	v_mfma_i32_16x16x64_i8 v[46:49], v[134:137], v[204:207], v[46:49]
	v_mfma_i32_16x16x64_i8 v[42:45], v[142:145], v[204:207], v[42:45]
	v_mfma_i32_16x16x64_i8 v[30:33], v[134:137], v[212:215], v[30:33]
	v_mfma_i32_16x16x64_i8 v[26:29], v[142:145], v[212:215], v[26:29]
	v_mfma_i32_16x16x64_i8 v[14:17], v[134:137], v[220:223], v[14:17]
	v_mfma_i32_16x16x64_i8 v[10:13], v[142:145], v[220:223], v[10:13]
	v_mfma_i32_16x16x64_i8 v[54:57], v[146:149], v[192:195], v[54:57]
	v_mfma_i32_16x16x64_i8 v[50:53], v[154:157], v[192:195], v[50:53]
	v_mfma_i32_16x16x64_i8 v[38:41], v[146:149], v[200:203], v[38:41]
	v_mfma_i32_16x16x64_i8 v[34:37], v[154:157], v[200:203], v[34:37]
	v_mfma_i32_16x16x64_i8 v[22:25], v[146:149], v[208:211], v[22:25]
	v_mfma_i32_16x16x64_i8 v[18:21], v[154:157], v[208:211], v[18:21]
	v_mfma_i32_16x16x64_i8 v[6:9], v[146:149], v[216:219], v[6:9]
	v_mfma_i32_16x16x64_i8 v[2:5], v[154:157], v[216:219], v[2:5]
	v_mfma_i32_16x16x64_i8 v[54:57], v[150:153], v[196:199], v[54:57]
	v_mfma_i32_16x16x64_i8 v[50:53], v[158:161], v[196:199], v[50:53]
	v_mfma_i32_16x16x64_i8 v[38:41], v[150:153], v[204:207], v[38:41]
	v_mfma_i32_16x16x64_i8 v[34:37], v[158:161], v[204:207], v[34:37]
	v_mfma_i32_16x16x64_i8 v[22:25], v[150:153], v[212:215], v[22:25]
	v_mfma_i32_16x16x64_i8 v[18:21], v[158:161], v[212:215], v[18:21]
	v_mfma_i32_16x16x64_i8 v[6:9], v[150:153], v[220:223], v[6:9]
	v_mfma_i32_16x16x64_i8 v[2:5], v[158:161], v[220:223], v[2:5]
	s_setprio 0
	s_barrier
	s_add_i32 s87, s87, 2
	s_cmp_gt_u32 s87, 13
	s_cbranch_scc1 .LBB0_1758
	s_mov_b64 s[6:7], s[62:63]
	s_branch .LBB0_1754

; #define PG8_STAGE(bufoff, gbase, voff) do { _Pragma("unroll") for (int _i = 0; _i < 2; ++_i) { unsigned vo_ = (voff)[_i]; asm volatile("" : "+v"(vo_));   \
;         __builtin_amdgcn_global_load_lds((const unsigned*)((const char*)(gbase) + vo_), (LAS unsigned*)(lds + (bufoff) + ldsw + _i * 8192), 16, 0, 0); } } while (0)
; #define PG8_LDA(dst, b, h) do { _Pragma("unroll") for (int m = 0; m < 4; ++m) _Pragma("unroll") for (int k = 0; k < 2; ++k) dst[m][k] = *(const LAS bf16x8*)(lds + PG8_SA(b, h) + aoff + m * 2048 + k * 1024); } while (0)
; #define PG8_LDB(dst, b, h) do { _Pragma("unroll") for (int n = 0; n < 2; ++n) _Pragma("unroll") for (int k = 0; k < 2; ++k) dst[n][k] = *(const LAS bf16x8*)(lds + PG8_SB(b, h) + boff + n * 2048 + k * 1024); } while (0)
; #define PG8_WAIT_V(n) asm volatile("s_waitcnt vmcnt(" #n ")" ::: "memory")
; #define PG8_WAIT_L(n) asm volatile("s_waitcnt lgkmcnt(" #n ")" ::: "memory")
; #define PG8_BAR __builtin_amdgcn_s_barrier()
; #define PG8_SCHED __builtin_amdgcn_sched_barrier(0)
;     ...
;         for (int t = 0; t < nt; t += 2) {
;             const bool last = (t == nt - 2);
;             const char* a1 = Abase + (size_t)(t + 1) * kstep;
;             const char* a2 = Abase + (last ? (size_t)0 : (size_t)(t + 2) * kstep); const char* b2 = last ? nB : cB + (size_t)(t + 2) * kstep;
;             const char* a3 = a2 + kstep; const char* b3 = b2 + kstep;
;             PG8_LDB(B0, 0, 0); PG8_LDB(B1, 0, 1); PG8_SCHED; PG8_LDA(At, 0, 0); PG8_STAGE(PG8_SA(1, 1), a1, va[1]);
;             PG8_WAIT_V(8); PG8_WAIT_L(0); PG8_BAR; PG8_MMA(0, 0, At, B0); PG8_MMA(0, 1, At, B1); PG8_BAR; PG8_SCHED;
;             if (last && has_next) { PG8_AOFFS(va, nxt); }
;             PG8_LDA(At, 0, 1); PG8_STAGE(PG8_SB(0, 0), b2, voffB); PG8_STAGE(PG8_SB(0, 1), b2 + hstepB, voffB); PG8_STAGE(PG8_SA(0, 0), a2, va[0]);
;             PG8_WAIT_V(8); PG8_WAIT_L(0); PG8_BAR; PG8_MMA(1, 0, At, B0); PG8_MMA(1, 1, At, B1); PG8_BAR; PG8_SCHED;
;             PG8_LDB(B0, 1, 0); PG8_LDB(B1, 1, 1); PG8_SCHED; PG8_LDA(At, 1, 0); PG8_STAGE(PG8_SA(0, 1), a2, va[1]);
;             PG8_WAIT_V(8); PG8_WAIT_L(0); PG8_BAR; PG8_MMA(0, 0, At, B0); PG8_MMA(0, 1, At, B1); PG8_BAR; PG8_SCHED;
.LBB0_1986:
	ds_read_b128 v[146:149], v186
	ds_read_b128 v[150:153], v186 offset:1024
	ds_read_b128 v[154:157], v186 offset:2048
	ds_read_b128 v[158:161], v186 offset:3072
	ds_read_b128 v[130:133], v187
	ds_read_b128 v[134:137], v187 offset:1024
	ds_read_b128 v[138:141], v187 offset:2048
	ds_read_b128 v[142:145], v187 offset:3072
	s_cmp_eq_u32 s96, 4
	s_cselect_b64 s[58:59], -1, 0
	s_add_i32 m0, s45, 0xc000
	v_mov_b32_e32 v164, v182
	s_add_u32 s54, s42, s52
	ds_read_b128 v[196:199], v188
	ds_read_b128 v[200:203], v188 offset:1024
	ds_read_b128 v[204:207], v188 offset:2048
	ds_read_b128 v[208:211], v188 offset:3072
	ds_read_b128 v[212:215], v188 offset:4096
	ds_read_b128 v[216:219], v188 offset:5120
	ds_read_b128 v[220:223], v188 offset:6144
	ds_read_b128 v[224:227], v188 offset:7168
	s_addc_u32 s55, s43, s53
	global_load_lds_dwordx4 v164, s[54:55]
	v_mov_b32_e32 v164, v183
	s_add_i32 m0, s45, 0xe000
	s_nop 0
	global_load_lds_dwordx4 v164, s[54:55]
	s_waitcnt vmcnt(8)
	s_waitcnt lgkmcnt(0)
	s_barrier
	s_setprio 1
	s_waitcnt lgkmcnt(0)
	v_mfma_f32_16x16x32_bf16 v[126:129], v[146:149], v[196:199], v[126:129]
	v_mfma_f32_16x16x32_bf16 v[122:125], v[154:157], v[196:199], v[122:125]
	v_mfma_f32_16x16x32_bf16 v[110:113], v[146:149], v[204:207], v[110:113]
	v_mfma_f32_16x16x32_bf16 v[106:109], v[154:157], v[204:207], v[106:109]
	v_mfma_f32_16x16x32_bf16 v[94:97], v[146:149], v[212:215], v[94:97]
	v_mfma_f32_16x16x32_bf16 v[90:93], v[154:157], v[212:215], v[90:93]
	v_mfma_f32_16x16x32_bf16 v[78:81], v[146:149], v[220:223], v[78:81]
	v_mfma_f32_16x16x32_bf16 v[74:77], v[154:157], v[220:223], v[74:77]
	v_mfma_f32_16x16x32_bf16 v[126:129], v[150:153], v[200:203], v[126:129]
	v_mfma_f32_16x16x32_bf16 v[122:125], v[158:161], v[200:203], v[122:125]
	v_mfma_f32_16x16x32_bf16 v[110:113], v[150:153], v[208:211], v[110:113]
	v_mfma_f32_16x16x32_bf16 v[106:109], v[158:161], v[208:211], v[106:109]
	v_mfma_f32_16x16x32_bf16 v[94:97], v[150:153], v[216:219], v[94:97]
	v_mfma_f32_16x16x32_bf16 v[90:93], v[158:161], v[216:219], v[90:93]
	v_mfma_f32_16x16x32_bf16 v[78:81], v[150:153], v[224:227], v[78:81]
	v_mfma_f32_16x16x32_bf16 v[74:77], v[158:161], v[224:227], v[74:77]
	v_mfma_f32_16x16x32_bf16 v[118:121], v[130:133], v[196:199], v[118:121]
	v_mfma_f32_16x16x32_bf16 v[114:117], v[138:141], v[196:199], v[114:117]
	v_mfma_f32_16x16x32_bf16 v[102:105], v[130:133], v[204:207], v[102:105]
	v_mfma_f32_16x16x32_bf16 v[98:101], v[138:141], v[204:207], v[98:101]
	v_mfma_f32_16x16x32_bf16 v[86:89], v[130:133], v[212:215], v[86:89]
	v_mfma_f32_16x16x32_bf16 v[82:85], v[138:141], v[212:215], v[82:85]
	v_mfma_f32_16x16x32_bf16 v[70:73], v[130:133], v[220:223], v[70:73]
	v_mfma_f32_16x16x32_bf16 v[66:69], v[138:141], v[220:223], v[66:69]
	v_mfma_f32_16x16x32_bf16 v[118:121], v[134:137], v[200:203], v[118:121]
	v_mfma_f32_16x16x32_bf16 v[114:117], v[142:145], v[200:203], v[114:117]
	v_mfma_f32_16x16x32_bf16 v[102:105], v[134:137], v[208:211], v[102:105]
	v_mfma_f32_16x16x32_bf16 v[98:101], v[142:145], v[208:211], v[98:101]
	v_mfma_f32_16x16x32_bf16 v[86:89], v[134:137], v[216:219], v[86:89]
	v_mfma_f32_16x16x32_bf16 v[82:85], v[142:145], v[216:219], v[82:85]
	v_mfma_f32_16x16x32_bf16 v[70:73], v[134:137], v[224:227], v[70:73]
	v_mfma_f32_16x16x32_bf16 v[66:69], v[142:145], v[224:227], v[66:69]
	s_setprio 0
	s_barrier
	s_and_b64 s[54:55], s[6:7], s[58:59]
	s_andn2_b64 vcc, exec, s[54:55]
	s_cbranch_vccnz .LBB0_1988
	v_mov_b32_e32 v183, v194
	v_mov_b32_e32 v182, v193
	v_mov_b32_e32 v181, v192
	v_mov_b32_e32 v180, v191
.LBB0_1988:
	s_add_u32 s54, s52, 0x100
	s_addc_u32 s55, s53, 0
	s_and_b64 s[56:57], s[58:59], exec
	s_cselect_b32 s56, 0, s54
	s_cselect_b32 s57, 0, s55
	s_add_u32 s56, s14, s56
	s_addc_u32 s57, s15, s57
	s_add_u32 s97, s49, s52
	s_addc_u32 vcc_lo, s95, s53
	s_and_b64 s[52:53], s[58:59], exec
	v_mov_b32_e32 v164, v177
	s_mov_b32 m0, s63
	s_cselect_b32 s53, s51, vcc_lo
	s_cselect_b32 s52, s50, s97
	ds_read_b128 v[196:199], v188 offset:16384
	ds_read_b128 v[200:203], v188 offset:17408
	ds_read_b128 v[204:207], v188 offset:18432
	ds_read_b128 v[208:211], v188 offset:19456
	ds_read_b128 v[212:215], v188 offset:20480
	ds_read_b128 v[216:219], v188 offset:21504
	ds_read_b128 v[220:223], v188 offset:22528
	ds_read_b128 v[224:227], v188 offset:23552
	s_add_u32 s58, s52, 0x20000
	global_load_lds_dwordx4 v164, s[52:53]
	v_mov_b32_e32 v164, v179
	s_mov_b32 m0, s64
	s_addc_u32 s59, s53, 0
	global_load_lds_dwordx4 v164, s[52:53]
	v_mov_b32_e32 v164, v177
	s_mov_b32 m0, s65
	s_nop 0
	global_load_lds_dwordx4 v164, s[58:59]
	v_mov_b32_e32 v164, v179
	s_mov_b32 m0, s66
	s_nop 0
	global_load_lds_dwordx4 v164, s[58:59]
	v_mov_b32_e32 v164, v180
	s_mov_b32 m0, s45
	s_nop 0
	global_load_lds_dwordx4 v164, s[56:57]
	v_mov_b32_e32 v164, v181
	s_mov_b32 m0, s67
	s_nop 0
	global_load_lds_dwordx4 v164, s[56:57]
	s_waitcnt vmcnt(8)
	s_waitcnt lgkmcnt(0)
	s_barrier
; #define PG8_STAGE(bufoff, gbase, voff) do { _Pragma("unroll") for (int _i = 0; _i < 2; ++_i) { unsigned vo_ = (voff)[_i]; asm volatile("" : "+v"(vo_));   \
;         __builtin_amdgcn_global_load_lds((const unsigned*)((const char*)(gbase) + vo_), (LAS unsigned*)(lds + (bufoff) + ldsw + _i * 8192), 16, 0, 0); } } while (0)
; #define PG8_LDA(dst, b, h) do { _Pragma("unroll") for (int m = 0; m < 4; ++m) _Pragma("unroll") for (int k = 0; k < 2; ++k) dst[m][k] = *(const LAS bf16x8*)(lds + PG8_SA(b, h) + aoff + m * 2048 + k * 1024); } while (0)
; #define PG8_LDB(dst, b, h) do { _Pragma("unroll") for (int n = 0; n < 2; ++n) _Pragma("unroll") for (int k = 0; k < 2; ++k) dst[n][k] = *(const LAS bf16x8*)(lds + PG8_SB(b, h) + boff + n * 2048 + k * 1024); } while (0)
; #define PG8_WAIT_V(n) asm volatile("s_waitcnt vmcnt(" #n ")" ::: "memory")
; #define PG8_WAIT_L(n) asm volatile("s_waitcnt lgkmcnt(" #n ")" ::: "memory")
; #define PG8_BAR __builtin_amdgcn_s_barrier()
; #define PG8_SCHED __builtin_amdgcn_sched_barrier(0)
;     ...
;             PG8_WAIT_V(8); PG8_WAIT_L(0); PG8_BAR; PG8_MMA(1, 0, At, B0); PG8_MMA(1, 1, At, B1); PG8_BAR; PG8_SCHED;
;             PG8_LDB(B0, 1, 0); PG8_LDB(B1, 1, 1); PG8_SCHED; PG8_LDA(At, 1, 0); PG8_STAGE(PG8_SA(0, 1), a2, va[1]);
;             PG8_WAIT_V(8); PG8_WAIT_L(0); PG8_BAR; PG8_MMA(0, 0, At, B0); PG8_MMA(0, 1, At, B1); PG8_BAR; PG8_SCHED;
	s_setprio 1
	s_waitcnt lgkmcnt(0)
	v_mfma_f32_16x16x32_bf16 v[62:65], v[146:149], v[196:199], v[62:65]
	v_mfma_f32_16x16x32_bf16 v[58:61], v[154:157], v[196:199], v[58:61]
	v_mfma_f32_16x16x32_bf16 v[46:49], v[146:149], v[204:207], v[46:49]
	v_mfma_f32_16x16x32_bf16 v[42:45], v[154:157], v[204:207], v[42:45]
	v_mfma_f32_16x16x32_bf16 v[30:33], v[146:149], v[212:215], v[30:33]
	v_mfma_f32_16x16x32_bf16 v[26:29], v[154:157], v[212:215], v[26:29]
	v_mfma_f32_16x16x32_bf16 v[14:17], v[146:149], v[220:223], v[14:17]
	v_mfma_f32_16x16x32_bf16 v[10:13], v[154:157], v[220:223], v[10:13]
	v_mfma_f32_16x16x32_bf16 v[62:65], v[150:153], v[200:203], v[62:65]
	v_mfma_f32_16x16x32_bf16 v[58:61], v[158:161], v[200:203], v[58:61]
	v_mfma_f32_16x16x32_bf16 v[46:49], v[150:153], v[208:211], v[46:49]
	v_mfma_f32_16x16x32_bf16 v[42:45], v[158:161], v[208:211], v[42:45]
	v_mfma_f32_16x16x32_bf16 v[30:33], v[150:153], v[216:219], v[30:33]
	v_mfma_f32_16x16x32_bf16 v[26:29], v[158:161], v[216:219], v[26:29]
	v_mfma_f32_16x16x32_bf16 v[14:17], v[150:153], v[224:227], v[14:17]
	v_mfma_f32_16x16x32_bf16 v[10:13], v[158:161], v[224:227], v[10:13]
	v_mfma_f32_16x16x32_bf16 v[54:57], v[130:133], v[196:199], v[54:57]
	v_mfma_f32_16x16x32_bf16 v[50:53], v[138:141], v[196:199], v[50:53]
	v_mfma_f32_16x16x32_bf16 v[38:41], v[130:133], v[204:207], v[38:41]
	v_mfma_f32_16x16x32_bf16 v[34:37], v[138:141], v[204:207], v[34:37]
	v_mfma_f32_16x16x32_bf16 v[22:25], v[130:133], v[212:215], v[22:25]
	v_mfma_f32_16x16x32_bf16 v[18:21], v[138:141], v[212:215], v[18:21]
	v_mfma_f32_16x16x32_bf16 v[6:9], v[130:133], v[220:223], v[6:9]
	v_mfma_f32_16x16x32_bf16 v[2:5], v[138:141], v[220:223], v[2:5]
	v_mfma_f32_16x16x32_bf16 v[54:57], v[134:137], v[200:203], v[54:57]
	v_mfma_f32_16x16x32_bf16 v[50:53], v[142:145], v[200:203], v[50:53]
	v_mfma_f32_16x16x32_bf16 v[38:41], v[134:137], v[208:211], v[38:41]
	v_mfma_f32_16x16x32_bf16 v[34:37], v[142:145], v[208:211], v[34:37]
	v_mfma_f32_16x16x32_bf16 v[22:25], v[134:137], v[216:219], v[22:25]
	v_mfma_f32_16x16x32_bf16 v[18:21], v[142:145], v[216:219], v[18:21]
	v_mfma_f32_16x16x32_bf16 v[6:9], v[134:137], v[224:227], v[6:9]
	v_mfma_f32_16x16x32_bf16 v[2:5], v[142:145], v[224:227], v[2:5]
	s_setprio 0
	s_barrier
	s_add_i32 s58, 0, 0x18000
	s_add_i32 s59, 0, 0x1c000
	v_add_u32_e32 v142, s58, v185
	v_add_u32_e32 v158, s59, v185
	ds_read_b128 v[130:133], v142
	ds_read_b128 v[134:137], v142 offset:1024
	ds_read_b128 v[138:141], v142 offset:2048
	ds_read_b128 v[142:145], v142 offset:3072
	ds_read_b128 v[146:149], v158
	ds_read_b128 v[150:153], v158 offset:1024
	ds_read_b128 v[154:157], v158 offset:2048
	ds_read_b128 v[158:161], v158 offset:3072
	v_mov_b32_e32 v164, v182
	s_mov_b32 m0, s68
	ds_read_b128 v[196:199], v188 offset:32768
	ds_read_b128 v[200:203], v188 offset:33792
	ds_read_b128 v[204:207], v188 offset:34816
	ds_read_b128 v[208:211], v188 offset:35840
	ds_read_b128 v[212:215], v188 offset:36864
	ds_read_b128 v[216:219], v188 offset:37888
	ds_read_b128 v[220:223], v188 offset:38912
	ds_read_b128 v[224:227], v188 offset:39936
	s_nop 0
	global_load_lds_dwordx4 v164, s[56:57]
	v_mov_b32_e32 v164, v183
	s_mov_b32 m0, s69
	s_nop 0
	global_load_lds_dwordx4 v164, s[56:57]
	s_waitcnt vmcnt(8)
	s_waitcnt lgkmcnt(0)
	s_barrier
	s_setprio 1
	s_waitcnt lgkmcnt(0)
	v_mfma_f32_16x16x32_bf16 v[126:129], v[130:133], v[196:199], v[126:129]
	v_mfma_f32_16x16x32_bf16 v[122:125], v[138:141], v[196:199], v[122:125]
	v_mfma_f32_16x16x32_bf16 v[110:113], v[130:133], v[204:207], v[110:113]
	v_mfma_f32_16x16x32_bf16 v[106:109], v[138:141], v[204:207], v[106:109]
	v_mfma_f32_16x16x32_bf16 v[94:97], v[130:133], v[212:215], v[94:97]
	v_mfma_f32_16x16x32_bf16 v[90:93], v[138:141], v[212:215], v[90:93]
	v_mfma_f32_16x16x32_bf16 v[78:81], v[130:133], v[220:223], v[78:81]
	v_mfma_f32_16x16x32_bf16 v[74:77], v[138:141], v[220:223], v[74:77]
	v_mfma_f32_16x16x32_bf16 v[126:129], v[134:137], v[200:203], v[126:129]
	v_mfma_f32_16x16x32_bf16 v[122:125], v[142:145], v[200:203], v[122:125]
	v_mfma_f32_16x16x32_bf16 v[110:113], v[134:137], v[208:211], v[110:113]
	v_mfma_f32_16x16x32_bf16 v[106:109], v[142:145], v[208:211], v[106:109]
	v_mfma_f32_16x16x32_bf16 v[94:97], v[134:137], v[216:219], v[94:97]
	v_mfma_f32_16x16x32_bf16 v[90:93], v[142:145], v[216:219], v[90:93]
	v_mfma_f32_16x16x32_bf16 v[78:81], v[134:137], v[224:227], v[78:81]
	v_mfma_f32_16x16x32_bf16 v[74:77], v[142:145], v[224:227], v[74:77]
	v_mfma_f32_16x16x32_bf16 v[118:121], v[146:149], v[196:199], v[118:121]
	v_mfma_f32_16x16x32_bf16 v[114:117], v[154:157], v[196:199], v[114:117]
	v_mfma_f32_16x16x32_bf16 v[102:105], v[146:149], v[204:207], v[102:105]
	v_mfma_f32_16x16x32_bf16 v[98:101], v[154:157], v[204:207], v[98:101]
	v_mfma_f32_16x16x32_bf16 v[86:89], v[146:149], v[212:215], v[86:89]
	v_mfma_f32_16x16x32_bf16 v[82:85], v[154:157], v[212:215], v[82:85]
	v_mfma_f32_16x16x32_bf16 v[70:73], v[146:149], v[220:223], v[70:73]
	v_mfma_f32_16x16x32_bf16 v[66:69], v[154:157], v[220:223], v[66:69]
	v_mfma_f32_16x16x32_bf16 v[118:121], v[150:153], v[200:203], v[118:121]
	v_mfma_f32_16x16x32_bf16 v[114:117], v[158:161], v[200:203], v[114:117]
	v_mfma_f32_16x16x32_bf16 v[102:105], v[150:153], v[208:211], v[102:105]
	v_mfma_f32_16x16x32_bf16 v[98:101], v[158:161], v[208:211], v[98:101]
	v_mfma_f32_16x16x32_bf16 v[86:89], v[150:153], v[216:219], v[86:89]
	v_mfma_f32_16x16x32_bf16 v[82:85], v[158:161], v[216:219], v[82:85]
	v_mfma_f32_16x16x32_bf16 v[70:73], v[150:153], v[224:227], v[70:73]
	v_mfma_f32_16x16x32_bf16 v[66:69], v[158:161], v[224:227], v[66:69]
	s_setprio 0
	s_barrier
; #define PG8_STAGE(bufoff, gbase, voff) do { _Pragma("unroll") for (int _i = 0; _i < 2; ++_i) { unsigned vo_ = (voff)[_i]; asm volatile("" : "+v"(vo_));   \
;         __builtin_amdgcn_global_load_lds((const unsigned*)((const char*)(gbase) + vo_), (LAS unsigned*)(lds + (bufoff) + ldsw + _i * 8192), 16, 0, 0); } } while (0)
; #define PG8_LDA(dst, b, h) do { _Pragma("unroll") for (int m = 0; m < 4; ++m) _Pragma("unroll") for (int k = 0; k < 2; ++k) dst[m][k] = *(const LAS bf16x8*)(lds + PG8_SA(b, h) + aoff + m * 2048 + k * 1024); } while (0)
; #define PG8_WAIT_V(n) asm volatile("s_waitcnt vmcnt(" #n ")" ::: "memory")
; #define PG8_WAIT_L(n) asm volatile("s_waitcnt lgkmcnt(" #n ")" ::: "memory")
; #define PG8_BAR __builtin_amdgcn_s_barrier()
; #define PG8_SCHED __builtin_amdgcn_sched_barrier(0)
;     ...
;             PG8_LDA(At, 1, 1); PG8_STAGE(PG8_SB(1, 0), b3, voffB); PG8_STAGE(PG8_SB(1, 1), b3 + hstepB, voffB); PG8_STAGE(PG8_SA(1, 0), a3, va[0]);
;             PG8_WAIT_V(8); PG8_WAIT_L(0); PG8_BAR; PG8_MMA(1, 0, At, B0); PG8_MMA(1, 1, At, B1); PG8_BAR; PG8_SCHED;
;         }
	v_mov_b32_e32 v164, v177
	ds_read_b128 v[196:199], v188 offset:49152
	ds_read_b128 v[200:203], v188 offset:50176
	ds_read_b128 v[204:207], v188 offset:51200
	ds_read_b128 v[208:211], v188 offset:52224
	ds_read_b128 v[212:215], v188 offset:53248
	ds_read_b128 v[216:219], v188 offset:54272
	ds_read_b128 v[220:223], v188 offset:55296
	ds_read_b128 v[224:227], v188 offset:56320
	s_add_i32 s58, s58, s62
	v_lshl_add_u64 v[228:229], s[52:53], 0, v[164:165]
	v_lshl_add_u64 v[228:229], v[228:229], 0, s[40:41]
	s_mov_b32 m0, s58
	v_mov_b32_e32 v164, v179
	global_load_lds_dwordx4 v[228:229], off
	s_add_i32 m0, s58, 0x2000
	s_nop 0
	v_lshl_add_u64 v[228:229], s[52:53], 0, v[164:165]
	s_add_u32 s52, s52, 0x20080
	v_lshl_add_u64 v[228:229], v[228:229], 0, s[40:41]
	s_addc_u32 s53, s53, 0
	v_mov_b32_e32 v164, v177
	s_add_i32 s58, s59, s62
	global_load_lds_dwordx4 v[228:229], off
	s_mov_b32 m0, s58
	s_nop 0
	global_load_lds_dwordx4 v164, s[52:53]
	v_mov_b32_e32 v164, v179
	s_add_i32 m0, s58, 0x2000
	s_nop 0
	global_load_lds_dwordx4 v164, s[52:53]
	v_mov_b32_e32 v164, v180
	s_mov_b32 m0, s70
	v_lshl_add_u64 v[228:229], s[56:57], 0, v[164:165]
	v_lshl_add_u64 v[228:229], v[228:229], 0, s[40:41]
	v_mov_b32_e32 v164, v181
	global_load_lds_dwordx4 v[228:229], off
	s_mov_b32 m0, s71
	v_lshl_add_u64 v[228:229], s[56:57], 0, v[164:165]
	v_lshl_add_u64 v[228:229], v[228:229], 0, s[40:41]
	global_load_lds_dwordx4 v[228:229], off
	s_waitcnt vmcnt(8)
	s_waitcnt lgkmcnt(0)
	s_barrier
	s_setprio 1
	s_waitcnt lgkmcnt(0)
	v_mfma_f32_16x16x32_bf16 v[62:65], v[130:133], v[196:199], v[62:65]
	v_mfma_f32_16x16x32_bf16 v[58:61], v[138:141], v[196:199], v[58:61]
	v_mfma_f32_16x16x32_bf16 v[46:49], v[130:133], v[204:207], v[46:49]
	v_mfma_f32_16x16x32_bf16 v[42:45], v[138:141], v[204:207], v[42:45]
	v_mfma_f32_16x16x32_bf16 v[30:33], v[130:133], v[212:215], v[30:33]
	v_mfma_f32_16x16x32_bf16 v[26:29], v[138:141], v[212:215], v[26:29]
	v_mfma_f32_16x16x32_bf16 v[14:17], v[130:133], v[220:223], v[14:17]
	v_mfma_f32_16x16x32_bf16 v[10:13], v[138:141], v[220:223], v[10:13]
	v_mfma_f32_16x16x32_bf16 v[62:65], v[134:137], v[200:203], v[62:65]
	v_mfma_f32_16x16x32_bf16 v[58:61], v[142:145], v[200:203], v[58:61]
	v_mfma_f32_16x16x32_bf16 v[46:49], v[134:137], v[208:211], v[46:49]
	v_mfma_f32_16x16x32_bf16 v[42:45], v[142:145], v[208:211], v[42:45]
	v_mfma_f32_16x16x32_bf16 v[30:33], v[134:137], v[216:219], v[30:33]
	v_mfma_f32_16x16x32_bf16 v[26:29], v[142:145], v[216:219], v[26:29]
	v_mfma_f32_16x16x32_bf16 v[14:17], v[134:137], v[224:227], v[14:17]
	v_mfma_f32_16x16x32_bf16 v[10:13], v[142:145], v[224:227], v[10:13]
	v_mfma_f32_16x16x32_bf16 v[54:57], v[146:149], v[196:199], v[54:57]
	v_mfma_f32_16x16x32_bf16 v[50:53], v[154:157], v[196:199], v[50:53]
	v_mfma_f32_16x16x32_bf16 v[38:41], v[146:149], v[204:207], v[38:41]
	v_mfma_f32_16x16x32_bf16 v[34:37], v[154:157], v[204:207], v[34:37]
	v_mfma_f32_16x16x32_bf16 v[22:25], v[146:149], v[212:215], v[22:25]
	v_mfma_f32_16x16x32_bf16 v[18:21], v[154:157], v[212:215], v[18:21]
	v_mfma_f32_16x16x32_bf16 v[6:9], v[146:149], v[220:223], v[6:9]
	v_mfma_f32_16x16x32_bf16 v[2:5], v[154:157], v[220:223], v[2:5]
	v_mfma_f32_16x16x32_bf16 v[54:57], v[150:153], v[200:203], v[54:57]
	v_mfma_f32_16x16x32_bf16 v[50:53], v[158:161], v[200:203], v[50:53]
	v_mfma_f32_16x16x32_bf16 v[38:41], v[150:153], v[208:211], v[38:41]
	v_mfma_f32_16x16x32_bf16 v[34:37], v[158:161], v[208:211], v[34:37]
	v_mfma_f32_16x16x32_bf16 v[22:25], v[150:153], v[216:219], v[22:25]
	v_mfma_f32_16x16x32_bf16 v[18:21], v[158:161], v[216:219], v[18:21]
	v_mfma_f32_16x16x32_bf16 v[6:9], v[150:153], v[224:227], v[6:9]
	v_mfma_f32_16x16x32_bf16 v[2:5], v[158:161], v[224:227], v[2:5]
	s_setprio 0
	s_barrier
	s_add_i32 s96, s96, 2
	s_cmp_gt_u32 s96, 5
	s_cbranch_scc1 .LBB0_1990
	s_mov_b64 s[52:53], s[54:55]
	s_branch .LBB0_1986

; #define PG8_STAGE(bufoff, gbase, voff) do { _Pragma("unroll") for (int _i = 0; _i < 2; ++_i) { unsigned vo_ = (voff)[_i]; asm volatile("" : "+v"(vo_));   \
;         __builtin_amdgcn_global_load_lds((const unsigned*)((const char*)(gbase) + vo_), (LAS unsigned*)(lds + (bufoff) + ldsw + _i * 8192), 16, 0, 0); } } while (0)
; #define PG8_LDA(dst, b, h) do { _Pragma("unroll") for (int m = 0; m < 4; ++m) _Pragma("unroll") for (int k = 0; k < 2; ++k) dst[m][k] = *(const LAS bf16x8*)(lds + PG8_SA(b, h) + aoff + m * 2048 + k * 1024); } while (0)
; #define PG8_LDB(dst, b, h) do { _Pragma("unroll") for (int n = 0; n < 2; ++n) _Pragma("unroll") for (int k = 0; k < 2; ++k) dst[n][k] = *(const LAS bf16x8*)(lds + PG8_SB(b, h) + boff + n * 2048 + k * 1024); } while (0)
; #define PG8_WAIT_V(n) asm volatile("s_waitcnt vmcnt(" #n ")" ::: "memory")
; #define PG8_WAIT_L(n) asm volatile("s_waitcnt lgkmcnt(" #n ")" ::: "memory")
; #define PG8_BAR __builtin_amdgcn_s_barrier()
; #define PG8_SCHED __builtin_amdgcn_sched_barrier(0)
;     ...
;         for (int t = 0; t < nt; t += 2) {
;             const bool last = (t == nt - 2);
;             const char* a1 = Abase + (size_t)(t + 1) * kstep;
;             const char* a2 = Abase + (last ? (size_t)0 : (size_t)(t + 2) * kstep); const char* b2 = last ? nB : cB + (size_t)(t + 2) * kstep;
;             const char* a3 = a2 + kstep; const char* b3 = b2 + kstep;
;             PG8_LDB(B0, 0, 0); PG8_LDB(B1, 0, 1); PG8_SCHED; PG8_LDA(At, 0, 0); PG8_STAGE(PG8_SA(1, 1), a1, va[1]);
;             PG8_WAIT_V(8); PG8_WAIT_L(0); PG8_BAR; PG8_MMA(0, 0, At, B0); PG8_MMA(0, 1, At, B1); PG8_BAR; PG8_SCHED;
;             if (last && has_next) { PG8_AOFFS(va, nxt); }
;             PG8_LDA(At, 0, 1); PG8_STAGE(PG8_SB(0, 0), b2, voffB); PG8_STAGE(PG8_SB(0, 1), b2 + hstepB, voffB); PG8_STAGE(PG8_SA(0, 0), a2, va[0]);
;             PG8_WAIT_V(8); PG8_WAIT_L(0); PG8_BAR; PG8_MMA(1, 0, At, B0); PG8_MMA(1, 1, At, B1); PG8_BAR; PG8_SCHED;
;             PG8_LDB(B0, 1, 0); PG8_LDB(B1, 1, 1); PG8_SCHED; PG8_LDA(At, 1, 0); PG8_STAGE(PG8_SA(0, 1), a2, va[1]);
;             PG8_WAIT_V(8); PG8_WAIT_L(0); PG8_BAR; PG8_MMA(0, 0, At, B0); PG8_MMA(0, 1, At, B1); PG8_BAR; PG8_SCHED;
.LBB0_2259:
	ds_read_b128 v[154:157], v198
	ds_read_b128 v[158:161], v198 offset:1024
	ds_read_b128 v[162:165], v198 offset:2048
	ds_read_b128 v[166:169], v198 offset:3072
	ds_read_b128 v[134:137], v199
	ds_read_b128 v[138:141], v199 offset:1024
	ds_read_b128 v[146:149], v199 offset:2048
	ds_read_b128 v[150:153], v199 offset:3072
	s_cmp_eq_u32 s25, 28
	s_cselect_b64 s[34:35], -1, 0
	s_add_i32 m0, s41, 0xc000
	v_mov_b32_e32 v122, v194
	s_add_u32 s28, s14, s26
	ds_read_b128 v[206:209], v200
	ds_read_b128 v[210:213], v200 offset:1024
	ds_read_b128 v[214:217], v200 offset:2048
	ds_read_b128 v[218:221], v200 offset:3072
	ds_read_b128 v[222:225], v200 offset:4096
	ds_read_b128 v[226:229], v200 offset:5120
	ds_read_b128 v[230:233], v200 offset:6144
	ds_read_b128 v[234:237], v200 offset:7168
	s_addc_u32 s29, s15, s27
	global_load_lds_dwordx4 v122, s[28:29]
	v_mov_b32_e32 v122, v195
	s_add_i32 m0, s41, 0xe000
	s_nop 0
	global_load_lds_dwordx4 v122, s[28:29]
	s_waitcnt vmcnt(8)
	s_waitcnt lgkmcnt(0)
	s_barrier
	s_setprio 1
	s_waitcnt lgkmcnt(0)
	v_mfma_f32_16x16x32_bf16 v[122:125], v[154:157], v[206:209], v[142:145]
	v_mfma_f32_16x16x32_bf16 v[126:129], v[162:165], v[206:209], v[130:133]
	v_mfma_f32_16x16x32_bf16 v[114:117], v[154:157], v[214:217], v[114:117]
	v_mfma_f32_16x16x32_bf16 v[106:109], v[162:165], v[214:217], v[106:109]
	v_mfma_f32_16x16x32_bf16 v[98:101], v[154:157], v[222:225], v[98:101]
	v_mfma_f32_16x16x32_bf16 v[90:93], v[162:165], v[222:225], v[90:93]
	v_mfma_f32_16x16x32_bf16 v[82:85], v[154:157], v[230:233], v[82:85]
	v_mfma_f32_16x16x32_bf16 v[74:77], v[162:165], v[230:233], v[74:77]
	v_mfma_f32_16x16x32_bf16 v[122:125], v[158:161], v[210:213], v[122:125]
	v_mfma_f32_16x16x32_bf16 v[126:129], v[166:169], v[210:213], v[126:129]
	v_mfma_f32_16x16x32_bf16 v[114:117], v[158:161], v[218:221], v[114:117]
	v_mfma_f32_16x16x32_bf16 v[106:109], v[166:169], v[218:221], v[106:109]
	v_mfma_f32_16x16x32_bf16 v[98:101], v[158:161], v[226:229], v[98:101]
	v_mfma_f32_16x16x32_bf16 v[90:93], v[166:169], v[226:229], v[90:93]
	v_mfma_f32_16x16x32_bf16 v[82:85], v[158:161], v[234:237], v[82:85]
	v_mfma_f32_16x16x32_bf16 v[74:77], v[166:169], v[234:237], v[74:77]
	v_mfma_f32_16x16x32_bf16 v[118:121], v[134:137], v[206:209], v[118:121]
	v_mfma_f32_16x16x32_bf16 v[110:113], v[146:149], v[206:209], v[110:113]
	v_mfma_f32_16x16x32_bf16 v[102:105], v[134:137], v[214:217], v[102:105]
	v_mfma_f32_16x16x32_bf16 v[94:97], v[146:149], v[214:217], v[94:97]
	v_mfma_f32_16x16x32_bf16 v[86:89], v[134:137], v[222:225], v[86:89]
	v_mfma_f32_16x16x32_bf16 v[78:81], v[146:149], v[222:225], v[78:81]
	v_mfma_f32_16x16x32_bf16 v[70:73], v[134:137], v[230:233], v[70:73]
	v_mfma_f32_16x16x32_bf16 v[66:69], v[146:149], v[230:233], v[66:69]
	v_mfma_f32_16x16x32_bf16 v[118:121], v[138:141], v[210:213], v[118:121]
	v_mfma_f32_16x16x32_bf16 v[110:113], v[150:153], v[210:213], v[110:113]
	v_mfma_f32_16x16x32_bf16 v[102:105], v[138:141], v[218:221], v[102:105]
	v_mfma_f32_16x16x32_bf16 v[94:97], v[150:153], v[218:221], v[94:97]
	v_mfma_f32_16x16x32_bf16 v[86:89], v[138:141], v[226:229], v[86:89]
	v_mfma_f32_16x16x32_bf16 v[78:81], v[150:153], v[226:229], v[78:81]
	v_mfma_f32_16x16x32_bf16 v[70:73], v[138:141], v[234:237], v[70:73]
	v_mfma_f32_16x16x32_bf16 v[66:69], v[150:153], v[234:237], v[66:69]
	s_setprio 0
	s_barrier
	s_and_b64 s[28:29], s[20:21], s[34:35]
	s_andn2_b64 vcc, exec, s[28:29]
	s_cbranch_vccnz .LBB0_2261
	v_mov_b32_e32 v195, v204
	v_mov_b32_e32 v194, v203
	v_mov_b32_e32 v193, v202
	v_mov_b32_e32 v192, v201
.LBB0_2261:
	s_add_u32 s28, s26, 0x100
	s_addc_u32 s29, s27, 0
	s_and_b64 s[30:31], s[34:35], exec
	s_cselect_b32 s30, 0, s28
	s_cselect_b32 s31, 0, s29
	s_add_u32 s30, s4, s30
	s_addc_u32 s31, s5, s31
	s_add_u32 s61, s10, s26
	s_addc_u32 s62, s19, s27
	s_and_b64 s[26:27], s[34:35], exec
	v_mov_b32_e32 v170, v189
	s_mov_b32 m0, s42
	s_cselect_b32 s27, s23, s62
	s_cselect_b32 s26, s22, s61
	ds_read_b128 v[130:133], v200 offset:16384
	ds_read_b128 v[142:145], v200 offset:17408
	ds_read_b128 v[206:209], v200 offset:18432
	ds_read_b128 v[210:213], v200 offset:19456
	ds_read_b128 v[214:217], v200 offset:20480
	ds_read_b128 v[218:221], v200 offset:21504
	ds_read_b128 v[222:225], v200 offset:22528
	ds_read_b128 v[226:229], v200 offset:23552
	s_add_u32 s34, s26, 0x80000
	global_load_lds_dwordx4 v170, s[26:27]
	v_mov_b32_e32 v170, v191
	s_mov_b32 m0, s43
	s_addc_u32 s35, s27, 0
	global_load_lds_dwordx4 v170, s[26:27]
	v_mov_b32_e32 v170, v189
	s_mov_b32 m0, s44
	s_nop 0
	global_load_lds_dwordx4 v170, s[34:35]
	v_mov_b32_e32 v170, v191
	s_mov_b32 m0, s45
	s_nop 0
	global_load_lds_dwordx4 v170, s[34:35]
	v_mov_b32_e32 v170, v192
	s_mov_b32 m0, s41
	s_nop 0
	global_load_lds_dwordx4 v170, s[30:31]
	v_mov_b32_e32 v170, v193
	s_mov_b32 m0, s46
	s_nop 0
	global_load_lds_dwordx4 v170, s[30:31]
	s_waitcnt vmcnt(8)
	s_waitcnt lgkmcnt(0)
	s_barrier
; #define PG8_STAGE(bufoff, gbase, voff) do { _Pragma("unroll") for (int _i = 0; _i < 2; ++_i) { unsigned vo_ = (voff)[_i]; asm volatile("" : "+v"(vo_));   \
;         __builtin_amdgcn_global_load_lds((const unsigned*)((const char*)(gbase) + vo_), (LAS unsigned*)(lds + (bufoff) + ldsw + _i * 8192), 16, 0, 0); } } while (0)
; #define PG8_LDA(dst, b, h) do { _Pragma("unroll") for (int m = 0; m < 4; ++m) _Pragma("unroll") for (int k = 0; k < 2; ++k) dst[m][k] = *(const LAS bf16x8*)(lds + PG8_SA(b, h) + aoff + m * 2048 + k * 1024); } while (0)
; #define PG8_LDB(dst, b, h) do { _Pragma("unroll") for (int n = 0; n < 2; ++n) _Pragma("unroll") for (int k = 0; k < 2; ++k) dst[n][k] = *(const LAS bf16x8*)(lds + PG8_SB(b, h) + boff + n * 2048 + k * 1024); } while (0)
; #define PG8_WAIT_V(n) asm volatile("s_waitcnt vmcnt(" #n ")" ::: "memory")
; #define PG8_WAIT_L(n) asm volatile("s_waitcnt lgkmcnt(" #n ")" ::: "memory")
; #define PG8_BAR __builtin_amdgcn_s_barrier()
; #define PG8_SCHED __builtin_amdgcn_sched_barrier(0)
;     ...
;             PG8_WAIT_V(8); PG8_WAIT_L(0); PG8_BAR; PG8_MMA(1, 0, At, B0); PG8_MMA(1, 1, At, B1); PG8_BAR; PG8_SCHED;
;             PG8_LDB(B0, 1, 0); PG8_LDB(B1, 1, 1); PG8_SCHED; PG8_LDA(At, 1, 0); PG8_STAGE(PG8_SA(0, 1), a2, va[1]);
;             PG8_WAIT_V(8); PG8_WAIT_L(0); PG8_BAR; PG8_MMA(0, 0, At, B0); PG8_MMA(0, 1, At, B1); PG8_BAR; PG8_SCHED;
	s_setprio 1
	s_waitcnt lgkmcnt(0)
	v_mfma_f32_16x16x32_bf16 v[62:65], v[154:157], v[130:133], v[62:65]
	v_mfma_f32_16x16x32_bf16 v[58:61], v[162:165], v[130:133], v[58:61]
	v_mfma_f32_16x16x32_bf16 v[50:53], v[154:157], v[206:209], v[50:53]
	v_mfma_f32_16x16x32_bf16 v[42:45], v[162:165], v[206:209], v[42:45]
	v_mfma_f32_16x16x32_bf16 v[34:37], v[154:157], v[214:217], v[34:37]
	v_mfma_f32_16x16x32_bf16 v[26:29], v[162:165], v[214:217], v[26:29]
	v_mfma_f32_16x16x32_bf16 v[18:21], v[154:157], v[222:225], v[18:21]
	v_mfma_f32_16x16x32_bf16 v[10:13], v[162:165], v[222:225], v[10:13]
	v_mfma_f32_16x16x32_bf16 v[62:65], v[158:161], v[142:145], v[62:65]
	v_mfma_f32_16x16x32_bf16 v[58:61], v[166:169], v[142:145], v[58:61]
	v_mfma_f32_16x16x32_bf16 v[50:53], v[158:161], v[210:213], v[50:53]
	v_mfma_f32_16x16x32_bf16 v[42:45], v[166:169], v[210:213], v[42:45]
	v_mfma_f32_16x16x32_bf16 v[34:37], v[158:161], v[218:221], v[34:37]
	v_mfma_f32_16x16x32_bf16 v[26:29], v[166:169], v[218:221], v[26:29]
	v_mfma_f32_16x16x32_bf16 v[18:21], v[158:161], v[226:229], v[18:21]
	v_mfma_f32_16x16x32_bf16 v[10:13], v[166:169], v[226:229], v[10:13]
	v_mfma_f32_16x16x32_bf16 v[54:57], v[134:137], v[130:133], v[54:57]
	v_mfma_f32_16x16x32_bf16 v[46:49], v[146:149], v[130:133], v[46:49]
	v_mfma_f32_16x16x32_bf16 v[38:41], v[134:137], v[206:209], v[38:41]
	v_mfma_f32_16x16x32_bf16 v[30:33], v[146:149], v[206:209], v[30:33]
	v_mfma_f32_16x16x32_bf16 v[22:25], v[134:137], v[214:217], v[22:25]
	v_mfma_f32_16x16x32_bf16 v[14:17], v[146:149], v[214:217], v[14:17]
	v_mfma_f32_16x16x32_bf16 v[6:9], v[134:137], v[222:225], v[6:9]
	v_mfma_f32_16x16x32_bf16 v[2:5], v[146:149], v[222:225], v[2:5]
	v_mfma_f32_16x16x32_bf16 v[54:57], v[138:141], v[142:145], v[54:57]
	v_mfma_f32_16x16x32_bf16 v[46:49], v[150:153], v[142:145], v[46:49]
	v_mfma_f32_16x16x32_bf16 v[38:41], v[138:141], v[210:213], v[38:41]
	v_mfma_f32_16x16x32_bf16 v[30:33], v[150:153], v[210:213], v[30:33]
	v_mfma_f32_16x16x32_bf16 v[22:25], v[138:141], v[218:221], v[22:25]
	v_mfma_f32_16x16x32_bf16 v[14:17], v[150:153], v[218:221], v[14:17]
	v_mfma_f32_16x16x32_bf16 v[6:9], v[138:141], v[226:229], v[6:9]
	v_mfma_f32_16x16x32_bf16 v[2:5], v[150:153], v[226:229], v[2:5]
	s_setprio 0
	s_barrier
	s_add_i32 s34, 0, 0x18000
	v_add_u32_e32 v130, s34, v196
	s_add_i32 s35, 0, 0x1c000
	ds_read_b128 v[134:137], v130
	ds_read_b128 v[138:141], v130 offset:1024
	ds_read_b128 v[146:149], v130 offset:2048
	ds_read_b128 v[150:153], v130 offset:3072
	v_add_u32_e32 v130, s35, v196
	ds_read_b128 v[154:157], v130
	ds_read_b128 v[158:161], v130 offset:1024
	ds_read_b128 v[162:165], v130 offset:2048
	ds_read_b128 v[166:169], v130 offset:3072
	v_mov_b32_e32 v130, v194
	s_mov_b32 m0, s47
	ds_read_b128 v[206:209], v200 offset:32768
	ds_read_b128 v[210:213], v200 offset:33792
	ds_read_b128 v[214:217], v200 offset:34816
	ds_read_b128 v[218:221], v200 offset:35840
	ds_read_b128 v[222:225], v200 offset:36864
	ds_read_b128 v[226:229], v200 offset:37888
	ds_read_b128 v[230:233], v200 offset:38912
	ds_read_b128 v[234:237], v200 offset:39936
	s_nop 0
	global_load_lds_dwordx4 v130, s[30:31]
	v_mov_b32_e32 v130, v195
	s_mov_b32 m0, s48
	s_nop 0
	global_load_lds_dwordx4 v130, s[30:31]
	s_waitcnt vmcnt(8)
	s_waitcnt lgkmcnt(0)
	s_barrier
	s_setprio 1
	s_waitcnt lgkmcnt(0)
	v_mfma_f32_16x16x32_bf16 v[122:125], v[134:137], v[206:209], v[122:125]
	v_mfma_f32_16x16x32_bf16 v[142:145], v[138:141], v[210:213], v[122:125]
	v_mfma_f32_16x16x32_bf16 v[122:125], v[146:149], v[206:209], v[126:129]
	v_mfma_f32_16x16x32_bf16 v[114:117], v[134:137], v[214:217], v[114:117]
	v_mfma_f32_16x16x32_bf16 v[106:109], v[146:149], v[214:217], v[106:109]
	v_mfma_f32_16x16x32_bf16 v[98:101], v[134:137], v[222:225], v[98:101]
	v_mfma_f32_16x16x32_bf16 v[90:93], v[146:149], v[222:225], v[90:93]
	v_mfma_f32_16x16x32_bf16 v[82:85], v[134:137], v[230:233], v[82:85]
	v_mfma_f32_16x16x32_bf16 v[74:77], v[146:149], v[230:233], v[74:77]
	v_mfma_f32_16x16x32_bf16 v[130:133], v[150:153], v[210:213], v[122:125]
	v_mfma_f32_16x16x32_bf16 v[114:117], v[138:141], v[218:221], v[114:117]
	v_mfma_f32_16x16x32_bf16 v[106:109], v[150:153], v[218:221], v[106:109]
	v_mfma_f32_16x16x32_bf16 v[98:101], v[138:141], v[226:229], v[98:101]
	v_mfma_f32_16x16x32_bf16 v[90:93], v[150:153], v[226:229], v[90:93]
	v_mfma_f32_16x16x32_bf16 v[82:85], v[138:141], v[234:237], v[82:85]
	v_mfma_f32_16x16x32_bf16 v[74:77], v[150:153], v[234:237], v[74:77]
	v_mfma_f32_16x16x32_bf16 v[118:121], v[154:157], v[206:209], v[118:121]
	v_mfma_f32_16x16x32_bf16 v[110:113], v[162:165], v[206:209], v[110:113]
	v_mfma_f32_16x16x32_bf16 v[102:105], v[154:157], v[214:217], v[102:105]
	v_mfma_f32_16x16x32_bf16 v[94:97], v[162:165], v[214:217], v[94:97]
	v_mfma_f32_16x16x32_bf16 v[86:89], v[154:157], v[222:225], v[86:89]
	v_mfma_f32_16x16x32_bf16 v[78:81], v[162:165], v[222:225], v[78:81]
	v_mfma_f32_16x16x32_bf16 v[70:73], v[154:157], v[230:233], v[70:73]
	v_mfma_f32_16x16x32_bf16 v[66:69], v[162:165], v[230:233], v[66:69]
	v_mfma_f32_16x16x32_bf16 v[118:121], v[158:161], v[210:213], v[118:121]
	v_mfma_f32_16x16x32_bf16 v[110:113], v[166:169], v[210:213], v[110:113]
	v_mfma_f32_16x16x32_bf16 v[102:105], v[158:161], v[218:221], v[102:105]
	v_mfma_f32_16x16x32_bf16 v[94:97], v[166:169], v[218:221], v[94:97]
	v_mfma_f32_16x16x32_bf16 v[86:89], v[158:161], v[226:229], v[86:89]
	v_mfma_f32_16x16x32_bf16 v[78:81], v[166:169], v[226:229], v[78:81]
	v_mfma_f32_16x16x32_bf16 v[70:73], v[158:161], v[234:237], v[70:73]
	v_mfma_f32_16x16x32_bf16 v[66:69], v[166:169], v[234:237], v[66:69]
	s_setprio 0
	s_barrier
; #define PG8_STAGE(bufoff, gbase, voff) do { _Pragma("unroll") for (int _i = 0; _i < 2; ++_i) { unsigned vo_ = (voff)[_i]; asm volatile("" : "+v"(vo_));   \
;         __builtin_amdgcn_global_load_lds((const unsigned*)((const char*)(gbase) + vo_), (LAS unsigned*)(lds + (bufoff) + ldsw + _i * 8192), 16, 0, 0); } } while (0)
; #define PG8_LDA(dst, b, h) do { _Pragma("unroll") for (int m = 0; m < 4; ++m) _Pragma("unroll") for (int k = 0; k < 2; ++k) dst[m][k] = *(const LAS bf16x8*)(lds + PG8_SA(b, h) + aoff + m * 2048 + k * 1024); } while (0)
; #define PG8_WAIT_V(n) asm volatile("s_waitcnt vmcnt(" #n ")" ::: "memory")
; #define PG8_WAIT_L(n) asm volatile("s_waitcnt lgkmcnt(" #n ")" ::: "memory")
; #define PG8_BAR __builtin_amdgcn_s_barrier()
; #define PG8_SCHED __builtin_amdgcn_sched_barrier(0)
;     ...
;             PG8_LDA(At, 1, 1); PG8_STAGE(PG8_SB(1, 0), b3, voffB); PG8_STAGE(PG8_SB(1, 1), b3 + hstepB, voffB); PG8_STAGE(PG8_SA(1, 0), a3, va[0]);
;             PG8_WAIT_V(8); PG8_WAIT_L(0); PG8_BAR; PG8_MMA(1, 0, At, B0); PG8_MMA(1, 1, At, B1); PG8_BAR; PG8_SCHED;
;         }
	v_mov_b32_e32 v170, v189
	ds_read_b128 v[122:125], v200 offset:49152
	ds_read_b128 v[126:129], v200 offset:50176
	ds_read_b128 v[206:209], v200 offset:51200
	ds_read_b128 v[210:213], v200 offset:52224
	ds_read_b128 v[214:217], v200 offset:53248
	ds_read_b128 v[218:221], v200 offset:54272
	ds_read_b128 v[222:225], v200 offset:55296
	ds_read_b128 v[226:229], v200 offset:56320
	s_add_i32 s34, s34, s40
	v_lshl_add_u64 v[230:231], s[26:27], 0, v[170:171]
	v_lshl_add_u64 v[230:231], v[230:231], 0, s[12:13]
	s_mov_b32 m0, s34
	v_mov_b32_e32 v170, v191
	global_load_lds_dwordx4 v[230:231], off
	s_add_i32 m0, s34, 0x2000
	s_nop 0
	v_lshl_add_u64 v[230:231], s[26:27], 0, v[170:171]
	s_add_u32 s26, s26, 0x80080
	v_lshl_add_u64 v[230:231], v[230:231], 0, s[12:13]
	s_addc_u32 s27, s27, 0
	v_mov_b32_e32 v170, v189
	s_add_i32 s34, s35, s40
	global_load_lds_dwordx4 v[230:231], off
	s_mov_b32 m0, s34
	s_nop 0
	global_load_lds_dwordx4 v170, s[26:27]
	v_mov_b32_e32 v170, v191
	s_add_i32 m0, s34, 0x2000
	s_nop 0
	global_load_lds_dwordx4 v170, s[26:27]
	v_mov_b32_e32 v170, v192
	s_mov_b32 m0, s55
	v_lshl_add_u64 v[230:231], s[30:31], 0, v[170:171]
	v_lshl_add_u64 v[230:231], v[230:231], 0, s[12:13]
	v_mov_b32_e32 v170, v193
	global_load_lds_dwordx4 v[230:231], off
	s_mov_b32 m0, s56
	v_lshl_add_u64 v[230:231], s[30:31], 0, v[170:171]
	v_lshl_add_u64 v[230:231], v[230:231], 0, s[12:13]
	global_load_lds_dwordx4 v[230:231], off
	s_waitcnt vmcnt(8)
	s_waitcnt lgkmcnt(0)
	s_barrier
	s_setprio 1
	s_waitcnt lgkmcnt(0)
	v_mfma_f32_16x16x32_bf16 v[62:65], v[134:137], v[122:125], v[62:65]
	v_mfma_f32_16x16x32_bf16 v[58:61], v[146:149], v[122:125], v[58:61]
	v_mfma_f32_16x16x32_bf16 v[50:53], v[134:137], v[206:209], v[50:53]
	v_mfma_f32_16x16x32_bf16 v[42:45], v[146:149], v[206:209], v[42:45]
	v_mfma_f32_16x16x32_bf16 v[34:37], v[134:137], v[214:217], v[34:37]
	v_mfma_f32_16x16x32_bf16 v[26:29], v[146:149], v[214:217], v[26:29]
	v_mfma_f32_16x16x32_bf16 v[18:21], v[134:137], v[222:225], v[18:21]
	v_mfma_f32_16x16x32_bf16 v[10:13], v[146:149], v[222:225], v[10:13]
	v_mfma_f32_16x16x32_bf16 v[62:65], v[138:141], v[126:129], v[62:65]
	v_mfma_f32_16x16x32_bf16 v[58:61], v[150:153], v[126:129], v[58:61]
	v_mfma_f32_16x16x32_bf16 v[50:53], v[138:141], v[210:213], v[50:53]
	v_mfma_f32_16x16x32_bf16 v[42:45], v[150:153], v[210:213], v[42:45]
	v_mfma_f32_16x16x32_bf16 v[34:37], v[138:141], v[218:221], v[34:37]
	v_mfma_f32_16x16x32_bf16 v[26:29], v[150:153], v[218:221], v[26:29]
	v_mfma_f32_16x16x32_bf16 v[18:21], v[138:141], v[226:229], v[18:21]
	v_mfma_f32_16x16x32_bf16 v[10:13], v[150:153], v[226:229], v[10:13]
	v_mfma_f32_16x16x32_bf16 v[54:57], v[154:157], v[122:125], v[54:57]
	v_mfma_f32_16x16x32_bf16 v[46:49], v[162:165], v[122:125], v[46:49]
	v_mfma_f32_16x16x32_bf16 v[38:41], v[154:157], v[206:209], v[38:41]
	v_mfma_f32_16x16x32_bf16 v[30:33], v[162:165], v[206:209], v[30:33]
	v_mfma_f32_16x16x32_bf16 v[22:25], v[154:157], v[214:217], v[22:25]
	v_mfma_f32_16x16x32_bf16 v[14:17], v[162:165], v[214:217], v[14:17]
	v_mfma_f32_16x16x32_bf16 v[6:9], v[154:157], v[222:225], v[6:9]
	v_mfma_f32_16x16x32_bf16 v[2:5], v[162:165], v[222:225], v[2:5]
	v_mfma_f32_16x16x32_bf16 v[54:57], v[158:161], v[126:129], v[54:57]
	v_mfma_f32_16x16x32_bf16 v[46:49], v[166:169], v[126:129], v[46:49]
	v_mfma_f32_16x16x32_bf16 v[38:41], v[158:161], v[210:213], v[38:41]
	v_mfma_f32_16x16x32_bf16 v[30:33], v[166:169], v[210:213], v[30:33]
	v_mfma_f32_16x16x32_bf16 v[22:25], v[158:161], v[218:221], v[22:25]
	v_mfma_f32_16x16x32_bf16 v[14:17], v[166:169], v[218:221], v[14:17]
	v_mfma_f32_16x16x32_bf16 v[6:9], v[158:161], v[226:229], v[6:9]
	v_mfma_f32_16x16x32_bf16 v[2:5], v[166:169], v[226:229], v[2:5]
	s_setprio 0
	s_barrier
	s_add_i32 s25, s25, 2
	s_cmp_gt_u32 s25, 29
	s_cbranch_scc1 .LBB0_2263
	s_mov_b64 s[26:27], s[28:29]
	s_branch .LBB0_2259

; #define PG8_STAGE(bufoff, gbase, voff) do { _Pragma("unroll") for (int _i = 0; _i < 2; ++_i) { unsigned vo_ = (voff)[_i]; asm volatile("" : "+v"(vo_));   \
;         __builtin_amdgcn_global_load_lds((const unsigned*)((const char*)(gbase) + vo_), (LAS unsigned*)(lds + (bufoff) + ldsw + _i * 8192), 16, 0, 0); } } while (0)
; #define PG8_LDA(dst, b, h) do { _Pragma("unroll") for (int m = 0; m < 4; ++m) _Pragma("unroll") for (int k = 0; k < 2; ++k) dst[m][k] = *(const LAS bf16x8*)(lds + PG8_SA(b, h) + aoff + m * 2048 + k * 1024); } while (0)
; #define PG8_LDB(dst, b, h) do { _Pragma("unroll") for (int n = 0; n < 2; ++n) _Pragma("unroll") for (int k = 0; k < 2; ++k) dst[n][k] = *(const LAS bf16x8*)(lds + PG8_SB(b, h) + boff + n * 2048 + k * 1024); } while (0)
; #define PG8_WAIT_V(n) asm volatile("s_waitcnt vmcnt(" #n ")" ::: "memory")
; #define PG8_WAIT_L(n) asm volatile("s_waitcnt lgkmcnt(" #n ")" ::: "memory")
; #define PG8_BAR __builtin_amdgcn_s_barrier()
; #define PG8_SCHED __builtin_amdgcn_sched_barrier(0)
;     ...
;         for (int t = 0; t < nt; t += 2) {
;             const bool last = (t == nt - 2);
;             const char* a1 = Abase + (size_t)(t + 1) * kstep;
;             const char* a2 = Abase + (last ? (size_t)0 : (size_t)(t + 2) * kstep); const char* b2 = last ? nB : cB + (size_t)(t + 2) * kstep;
;             const char* a3 = a2 + kstep; const char* b3 = b2 + kstep;
;             PG8_LDB(B0, 0, 0); PG8_LDB(B1, 0, 1); PG8_SCHED; PG8_LDA(At, 0, 0); PG8_STAGE(PG8_SA(1, 1), a1, va[1]);
;             PG8_WAIT_V(8); PG8_WAIT_L(0); PG8_BAR; PG8_MMA(0, 0, At, B0); PG8_MMA(0, 1, At, B1); PG8_BAR; PG8_SCHED;
;             if (last && has_next) { PG8_AOFFS(va, nxt); }
;             PG8_LDA(At, 0, 1); PG8_STAGE(PG8_SB(0, 0), b2, voffB); PG8_STAGE(PG8_SB(0, 1), b2 + hstepB, voffB); PG8_STAGE(PG8_SA(0, 0), a2, va[0]);
;             PG8_WAIT_V(8); PG8_WAIT_L(0); PG8_BAR; PG8_MMA(1, 0, At, B0); PG8_MMA(1, 1, At, B1); PG8_BAR; PG8_SCHED;
;             PG8_LDB(B0, 1, 0); PG8_LDB(B1, 1, 1); PG8_SCHED; PG8_LDA(At, 1, 0); PG8_STAGE(PG8_SA(0, 1), a2, va[1]);
;             PG8_WAIT_V(8); PG8_WAIT_L(0); PG8_BAR; PG8_MMA(0, 0, At, B0); PG8_MMA(0, 1, At, B1); PG8_BAR; PG8_SCHED;
.LBB0_2547:
	v_add_u32_e32 v130, 0, v179
	v_add_u32_e32 v131, 0x10000, v130
	v_add_u32_e32 v142, 0x14000, v130
	ds_read_b128 v[146:149], v131
	ds_read_b128 v[150:153], v131 offset:1024
	ds_read_b128 v[154:157], v131 offset:2048
	ds_read_b128 v[158:161], v131 offset:3072
	ds_read_b128 v[130:133], v142
	ds_read_b128 v[134:137], v142 offset:1024
	ds_read_b128 v[138:141], v142 offset:2048
	ds_read_b128 v[142:145], v142 offset:3072
	s_cmp_eq_u32 s43, 12
	s_cselect_b64 s[6:7], -1, 0
	s_add_i32 m0, s45, 0xc000
	v_mov_b32_e32 v162, v177
	s_add_u32 s48, s28, s46
	ds_read_b128 v[194:197], v186
	ds_read_b128 v[198:201], v186 offset:1024
	ds_read_b128 v[202:205], v186 offset:2048
	ds_read_b128 v[206:209], v186 offset:3072
	ds_read_b128 v[210:213], v186 offset:4096
	ds_read_b128 v[214:217], v186 offset:5120
	ds_read_b128 v[218:221], v186 offset:6144
	ds_read_b128 v[222:225], v186 offset:7168
	s_addc_u32 s49, s29, s47
	global_load_lds_dwordx4 v162, s[48:49]
	v_mov_b32_e32 v162, v178
	s_add_i32 m0, s45, 0xe000
	s_nop 0
	global_load_lds_dwordx4 v162, s[48:49]
	s_waitcnt vmcnt(8)
	s_waitcnt lgkmcnt(0)
	s_barrier
	s_setprio 1
	s_waitcnt lgkmcnt(0)
	v_mfma_i32_16x16x64_i8 v[126:129], v[146:149], v[194:197], v[126:129]
	v_mfma_i32_16x16x64_i8 v[118:121], v[154:157], v[194:197], v[118:121]
	v_mfma_i32_16x16x64_i8 v[110:113], v[146:149], v[202:205], v[110:113]
	v_mfma_i32_16x16x64_i8 v[106:109], v[154:157], v[202:205], v[106:109]
	v_mfma_i32_16x16x64_i8 v[94:97], v[146:149], v[210:213], v[94:97]
	v_mfma_i32_16x16x64_i8 v[90:93], v[154:157], v[210:213], v[90:93]
	v_mfma_i32_16x16x64_i8 v[78:81], v[146:149], v[218:221], v[78:81]
	v_mfma_i32_16x16x64_i8 v[74:77], v[154:157], v[218:221], v[74:77]
	v_mfma_i32_16x16x64_i8 v[126:129], v[150:153], v[198:201], v[126:129]
	v_mfma_i32_16x16x64_i8 v[118:121], v[158:161], v[198:201], v[118:121]
	v_mfma_i32_16x16x64_i8 v[110:113], v[150:153], v[206:209], v[110:113]
	v_mfma_i32_16x16x64_i8 v[106:109], v[158:161], v[206:209], v[106:109]
	v_mfma_i32_16x16x64_i8 v[94:97], v[150:153], v[214:217], v[94:97]
	v_mfma_i32_16x16x64_i8 v[90:93], v[158:161], v[214:217], v[90:93]
	v_mfma_i32_16x16x64_i8 v[78:81], v[150:153], v[222:225], v[78:81]
	v_mfma_i32_16x16x64_i8 v[74:77], v[158:161], v[222:225], v[74:77]
	v_mfma_i32_16x16x64_i8 v[122:125], v[130:133], v[194:197], v[122:125]
	v_mfma_i32_16x16x64_i8 v[114:117], v[138:141], v[194:197], v[114:117]
	v_mfma_i32_16x16x64_i8 v[102:105], v[130:133], v[202:205], v[102:105]
	v_mfma_i32_16x16x64_i8 v[98:101], v[138:141], v[202:205], v[98:101]
	v_mfma_i32_16x16x64_i8 v[86:89], v[130:133], v[210:213], v[86:89]
	v_mfma_i32_16x16x64_i8 v[82:85], v[138:141], v[210:213], v[82:85]
	v_mfma_i32_16x16x64_i8 v[70:73], v[130:133], v[218:221], v[70:73]
	v_mfma_i32_16x16x64_i8 v[66:69], v[138:141], v[218:221], v[66:69]
	v_mfma_i32_16x16x64_i8 v[122:125], v[134:137], v[198:201], v[122:125]
	v_mfma_i32_16x16x64_i8 v[114:117], v[142:145], v[198:201], v[114:117]
	v_mfma_i32_16x16x64_i8 v[102:105], v[134:137], v[206:209], v[102:105]
	v_mfma_i32_16x16x64_i8 v[98:101], v[142:145], v[206:209], v[98:101]
	v_mfma_i32_16x16x64_i8 v[86:89], v[134:137], v[214:217], v[86:89]
	v_mfma_i32_16x16x64_i8 v[82:85], v[142:145], v[214:217], v[82:85]
	v_mfma_i32_16x16x64_i8 v[70:73], v[134:137], v[222:225], v[70:73]
	v_mfma_i32_16x16x64_i8 v[66:69], v[142:145], v[222:225], v[66:69]
	s_setprio 0
	s_barrier
	s_and_b64 s[48:49], s[4:5], s[6:7]
	s_andn2_b64 vcc, exec, s[48:49]
	s_cbranch_vccnz .LBB0_2549
	v_mov_b32_e32 v178, v193
	v_mov_b32_e32 v177, v192
	v_mov_b32_e32 v176, v191
	v_mov_b32_e32 v175, v169
.LBB0_2549:
	s_add_u32 s48, s46, 0x100
	v_lshl_add_u64 v[194:195], v[170:171], 0, s[46:47]
	s_addc_u32 s49, s47, 0
	v_cndmask_b32_e64 v227, v195, v167, s[6:7]
	v_cndmask_b32_e64 v226, v194, v166, s[6:7]
	v_mov_b32_e32 v162, v172
	s_mov_b32 m0, s53
	s_and_b64 s[50:51], s[6:7], exec
	ds_read_b128 v[194:197], v186 offset:16384
	ds_read_b128 v[198:201], v186 offset:17408
	ds_read_b128 v[202:205], v186 offset:18432
	ds_read_b128 v[206:209], v186 offset:19456
	ds_read_b128 v[210:213], v186 offset:20480
	ds_read_b128 v[214:217], v186 offset:21504
	ds_read_b128 v[218:221], v186 offset:22528
	ds_read_b128 v[222:225], v186 offset:23552
	v_readfirstlane_b32 s6, v226
	v_readfirstlane_b32 s7, v227
	v_lshl_add_u64 v[228:229], v[226:227], 0, s[16:17]
	s_cselect_b32 s50, 0, s48
	s_cselect_b32 s51, 0, s49
	s_add_u32 s50, s14, s50
	s_addc_u32 s51, s15, s51
	global_load_lds_dwordx4 v162, s[6:7]
	v_mov_b32_e32 v162, v174
	s_mov_b32 m0, s54
	s_nop 0
	global_load_lds_dwordx4 v162, s[6:7]
	v_mov_b32_e32 v162, v172
	v_readfirstlane_b32 s6, v228
	v_readfirstlane_b32 s7, v229
	s_mov_b32 m0, s55
	s_nop 3
	global_load_lds_dwordx4 v162, s[6:7]
	v_mov_b32_e32 v162, v174
	s_mov_b32 m0, s56
	s_nop 0
	global_load_lds_dwordx4 v162, s[6:7]
	v_mov_b32_e32 v162, v175
	s_mov_b32 m0, s45
	s_nop 0
	global_load_lds_dwordx4 v162, s[50:51]
	v_mov_b32_e32 v162, v176
	s_mov_b32 m0, s57
	s_nop 0
	global_load_lds_dwordx4 v162, s[50:51]
	s_waitcnt vmcnt(8)
	s_waitcnt lgkmcnt(0)
	s_barrier
; #define PG8_STAGE(bufoff, gbase, voff) do { _Pragma("unroll") for (int _i = 0; _i < 2; ++_i) { unsigned vo_ = (voff)[_i]; asm volatile("" : "+v"(vo_));   \
;         __builtin_amdgcn_global_load_lds((const unsigned*)((const char*)(gbase) + vo_), (LAS unsigned*)(lds + (bufoff) + ldsw + _i * 8192), 16, 0, 0); } } while (0)
; #define PG8_LDA(dst, b, h) do { _Pragma("unroll") for (int m = 0; m < 4; ++m) _Pragma("unroll") for (int k = 0; k < 2; ++k) dst[m][k] = *(const LAS bf16x8*)(lds + PG8_SA(b, h) + aoff + m * 2048 + k * 1024); } while (0)
; #define PG8_LDB(dst, b, h) do { _Pragma("unroll") for (int n = 0; n < 2; ++n) _Pragma("unroll") for (int k = 0; k < 2; ++k) dst[n][k] = *(const LAS bf16x8*)(lds + PG8_SB(b, h) + boff + n * 2048 + k * 1024); } while (0)
; #define PG8_WAIT_V(n) asm volatile("s_waitcnt vmcnt(" #n ")" ::: "memory")
; #define PG8_WAIT_L(n) asm volatile("s_waitcnt lgkmcnt(" #n ")" ::: "memory")
; #define PG8_BAR __builtin_amdgcn_s_barrier()
; #define PG8_SCHED __builtin_amdgcn_sched_barrier(0)
;     ...
;             PG8_WAIT_V(8); PG8_WAIT_L(0); PG8_BAR; PG8_MMA(1, 0, At, B0); PG8_MMA(1, 1, At, B1); PG8_BAR; PG8_SCHED;
;             PG8_LDB(B0, 1, 0); PG8_LDB(B1, 1, 1); PG8_SCHED; PG8_LDA(At, 1, 0); PG8_STAGE(PG8_SA(0, 1), a2, va[1]);
;             PG8_WAIT_V(8); PG8_WAIT_L(0); PG8_BAR; PG8_MMA(0, 0, At, B0); PG8_MMA(0, 1, At, B1); PG8_BAR; PG8_SCHED;
	s_setprio 1
	s_waitcnt lgkmcnt(0)
	v_mfma_i32_16x16x64_i8 v[62:65], v[146:149], v[194:197], v[62:65]
	v_mfma_i32_16x16x64_i8 v[58:61], v[154:157], v[194:197], v[58:61]
	v_mfma_i32_16x16x64_i8 v[46:49], v[146:149], v[202:205], v[46:49]
	v_mfma_i32_16x16x64_i8 v[42:45], v[154:157], v[202:205], v[42:45]
	v_mfma_i32_16x16x64_i8 v[30:33], v[146:149], v[210:213], v[30:33]
	v_mfma_i32_16x16x64_i8 v[26:29], v[154:157], v[210:213], v[26:29]
	v_mfma_i32_16x16x64_i8 v[14:17], v[146:149], v[218:221], v[14:17]
	v_mfma_i32_16x16x64_i8 v[10:13], v[154:157], v[218:221], v[10:13]
	v_mfma_i32_16x16x64_i8 v[62:65], v[150:153], v[198:201], v[62:65]
	v_mfma_i32_16x16x64_i8 v[58:61], v[158:161], v[198:201], v[58:61]
	v_mfma_i32_16x16x64_i8 v[46:49], v[150:153], v[206:209], v[46:49]
	v_mfma_i32_16x16x64_i8 v[42:45], v[158:161], v[206:209], v[42:45]
	v_mfma_i32_16x16x64_i8 v[30:33], v[150:153], v[214:217], v[30:33]
	v_mfma_i32_16x16x64_i8 v[26:29], v[158:161], v[214:217], v[26:29]
	v_mfma_i32_16x16x64_i8 v[14:17], v[150:153], v[222:225], v[14:17]
	v_mfma_i32_16x16x64_i8 v[10:13], v[158:161], v[222:225], v[10:13]
	v_mfma_i32_16x16x64_i8 v[54:57], v[130:133], v[194:197], v[54:57]
	v_mfma_i32_16x16x64_i8 v[50:53], v[138:141], v[194:197], v[50:53]
	v_mfma_i32_16x16x64_i8 v[38:41], v[130:133], v[202:205], v[38:41]
	v_mfma_i32_16x16x64_i8 v[34:37], v[138:141], v[202:205], v[34:37]
	v_mfma_i32_16x16x64_i8 v[22:25], v[130:133], v[210:213], v[22:25]
	v_mfma_i32_16x16x64_i8 v[18:21], v[138:141], v[210:213], v[18:21]
	v_mfma_i32_16x16x64_i8 v[6:9], v[130:133], v[218:221], v[6:9]
	v_mfma_i32_16x16x64_i8 v[2:5], v[138:141], v[218:221], v[2:5]
	v_mfma_i32_16x16x64_i8 v[54:57], v[134:137], v[198:201], v[54:57]
	v_mfma_i32_16x16x64_i8 v[50:53], v[142:145], v[198:201], v[50:53]
	v_mfma_i32_16x16x64_i8 v[38:41], v[134:137], v[206:209], v[38:41]
	v_mfma_i32_16x16x64_i8 v[34:37], v[142:145], v[206:209], v[34:37]
	v_mfma_i32_16x16x64_i8 v[22:25], v[134:137], v[214:217], v[22:25]
	v_mfma_i32_16x16x64_i8 v[18:21], v[142:145], v[214:217], v[18:21]
	v_mfma_i32_16x16x64_i8 v[6:9], v[134:137], v[222:225], v[6:9]
	v_mfma_i32_16x16x64_i8 v[2:5], v[142:145], v[222:225], v[2:5]
	s_setprio 0
	s_barrier
	s_add_i32 s6, 0, 0x18000
	s_add_i32 s7, 0, 0x1c000
	v_add_u32_e32 v142, s6, v179
	v_add_u32_e32 v158, s7, v179
	ds_read_b128 v[130:133], v142
	ds_read_b128 v[134:137], v142 offset:1024
	ds_read_b128 v[138:141], v142 offset:2048
	ds_read_b128 v[142:145], v142 offset:3072
	ds_read_b128 v[146:149], v158
	ds_read_b128 v[150:153], v158 offset:1024
	ds_read_b128 v[154:157], v158 offset:2048
	ds_read_b128 v[158:161], v158 offset:3072
	v_mov_b32_e32 v162, v177
	s_mov_b32 m0, s58
	ds_read_b128 v[194:197], v186 offset:32768
	ds_read_b128 v[198:201], v186 offset:33792
	ds_read_b128 v[202:205], v186 offset:34816
	ds_read_b128 v[206:209], v186 offset:35840
	ds_read_b128 v[210:213], v186 offset:36864
	ds_read_b128 v[214:217], v186 offset:37888
	ds_read_b128 v[218:221], v186 offset:38912
	ds_read_b128 v[222:225], v186 offset:39936
	s_nop 0
	global_load_lds_dwordx4 v162, s[50:51]
	v_mov_b32_e32 v162, v178
	s_mov_b32 m0, s59
	s_nop 0
	global_load_lds_dwordx4 v162, s[50:51]
	s_waitcnt vmcnt(8)
	s_waitcnt lgkmcnt(0)
	s_barrier
	s_setprio 1
	s_waitcnt lgkmcnt(0)
	v_mfma_i32_16x16x64_i8 v[126:129], v[130:133], v[194:197], v[126:129]
	v_mfma_i32_16x16x64_i8 v[118:121], v[138:141], v[194:197], v[118:121]
	v_mfma_i32_16x16x64_i8 v[110:113], v[130:133], v[202:205], v[110:113]
	v_mfma_i32_16x16x64_i8 v[106:109], v[138:141], v[202:205], v[106:109]
	v_mfma_i32_16x16x64_i8 v[94:97], v[130:133], v[210:213], v[94:97]
	v_mfma_i32_16x16x64_i8 v[90:93], v[138:141], v[210:213], v[90:93]
	v_mfma_i32_16x16x64_i8 v[78:81], v[130:133], v[218:221], v[78:81]
	v_mfma_i32_16x16x64_i8 v[74:77], v[138:141], v[218:221], v[74:77]
	v_mfma_i32_16x16x64_i8 v[126:129], v[134:137], v[198:201], v[126:129]
	v_mfma_i32_16x16x64_i8 v[118:121], v[142:145], v[198:201], v[118:121]
	v_mfma_i32_16x16x64_i8 v[110:113], v[134:137], v[206:209], v[110:113]
	v_mfma_i32_16x16x64_i8 v[106:109], v[142:145], v[206:209], v[106:109]
	v_mfma_i32_16x16x64_i8 v[94:97], v[134:137], v[214:217], v[94:97]
	v_mfma_i32_16x16x64_i8 v[90:93], v[142:145], v[214:217], v[90:93]
	v_mfma_i32_16x16x64_i8 v[78:81], v[134:137], v[222:225], v[78:81]
	v_mfma_i32_16x16x64_i8 v[74:77], v[142:145], v[222:225], v[74:77]
	v_mfma_i32_16x16x64_i8 v[122:125], v[146:149], v[194:197], v[122:125]
	v_mfma_i32_16x16x64_i8 v[114:117], v[154:157], v[194:197], v[114:117]
	v_mfma_i32_16x16x64_i8 v[102:105], v[146:149], v[202:205], v[102:105]
	v_mfma_i32_16x16x64_i8 v[98:101], v[154:157], v[202:205], v[98:101]
	v_mfma_i32_16x16x64_i8 v[86:89], v[146:149], v[210:213], v[86:89]
	v_mfma_i32_16x16x64_i8 v[82:85], v[154:157], v[210:213], v[82:85]
	v_mfma_i32_16x16x64_i8 v[70:73], v[146:149], v[218:221], v[70:73]
	v_mfma_i32_16x16x64_i8 v[66:69], v[154:157], v[218:221], v[66:69]
	v_mfma_i32_16x16x64_i8 v[122:125], v[150:153], v[198:201], v[122:125]
	v_mfma_i32_16x16x64_i8 v[114:117], v[158:161], v[198:201], v[114:117]
	v_mfma_i32_16x16x64_i8 v[102:105], v[150:153], v[206:209], v[102:105]
	v_mfma_i32_16x16x64_i8 v[98:101], v[158:161], v[206:209], v[98:101]
	v_mfma_i32_16x16x64_i8 v[86:89], v[150:153], v[214:217], v[86:89]
	v_mfma_i32_16x16x64_i8 v[82:85], v[158:161], v[214:217], v[82:85]
	v_mfma_i32_16x16x64_i8 v[70:73], v[150:153], v[222:225], v[70:73]
	v_mfma_i32_16x16x64_i8 v[66:69], v[158:161], v[222:225], v[66:69]
	s_setprio 0
	s_barrier
; #define PG8_STAGE(bufoff, gbase, voff) do { _Pragma("unroll") for (int _i = 0; _i < 2; ++_i) { unsigned vo_ = (voff)[_i]; asm volatile("" : "+v"(vo_));   \
;         __builtin_amdgcn_global_load_lds((const unsigned*)((const char*)(gbase) + vo_), (LAS unsigned*)(lds + (bufoff) + ldsw + _i * 8192), 16, 0, 0); } } while (0)
; #define PG8_LDA(dst, b, h) do { _Pragma("unroll") for (int m = 0; m < 4; ++m) _Pragma("unroll") for (int k = 0; k < 2; ++k) dst[m][k] = *(const LAS bf16x8*)(lds + PG8_SA(b, h) + aoff + m * 2048 + k * 1024); } while (0)
; #define PG8_WAIT_V(n) asm volatile("s_waitcnt vmcnt(" #n ")" ::: "memory")
; #define PG8_WAIT_L(n) asm volatile("s_waitcnt lgkmcnt(" #n ")" ::: "memory")
; #define PG8_BAR __builtin_amdgcn_s_barrier()
; #define PG8_SCHED __builtin_amdgcn_sched_barrier(0)
;     ...
;             PG8_LDA(At, 1, 1); PG8_STAGE(PG8_SB(1, 0), b3, voffB); PG8_STAGE(PG8_SB(1, 1), b3 + hstepB, voffB); PG8_STAGE(PG8_SA(1, 0), a3, va[0]);
;             PG8_WAIT_V(8); PG8_WAIT_L(0); PG8_BAR; PG8_MMA(1, 0, At, B0); PG8_MMA(1, 1, At, B1); PG8_BAR; PG8_SCHED;
;         }
	v_mov_b32_e32 v162, v172
	ds_read_b128 v[194:197], v186 offset:49152
	ds_read_b128 v[198:201], v186 offset:50176
	ds_read_b128 v[202:205], v186 offset:51200
	ds_read_b128 v[206:209], v186 offset:52224
	ds_read_b128 v[210:213], v186 offset:53248
	ds_read_b128 v[214:217], v186 offset:54272
	ds_read_b128 v[218:221], v186 offset:55296
	ds_read_b128 v[222:225], v186 offset:56320
	s_add_i32 s6, s6, s9
	v_lshl_add_u64 v[228:229], v[226:227], 0, v[162:163]
	v_lshl_add_u64 v[228:229], v[228:229], 0, s[26:27]
	s_mov_b32 m0, s6
	v_mov_b32_e32 v162, v174
	global_load_lds_dwordx4 v[228:229], off
	s_add_i32 m0, s6, 0x2000
	v_lshl_add_u64 v[228:229], v[226:227], 0, v[162:163]
	v_lshl_add_u64 v[228:229], v[228:229], 0, s[26:27]
	v_lshl_add_u64 v[226:227], v[226:227], 0, s[30:31]
	v_mov_b32_e32 v162, v172
	s_add_i32 s46, s7, s9
	global_load_lds_dwordx4 v[228:229], off
	v_readfirstlane_b32 s6, v226
	v_readfirstlane_b32 s7, v227
	s_mov_b32 m0, s46
	s_nop 3
	global_load_lds_dwordx4 v162, s[6:7]
	v_mov_b32_e32 v162, v174
	s_add_i32 m0, s46, 0x2000
	s_nop 0
	global_load_lds_dwordx4 v162, s[6:7]
	v_mov_b32_e32 v162, v175
	s_mov_b32 m0, s61
	v_lshl_add_u64 v[226:227], s[50:51], 0, v[162:163]
	v_lshl_add_u64 v[226:227], v[226:227], 0, s[26:27]
	v_mov_b32_e32 v162, v176
	global_load_lds_dwordx4 v[226:227], off
	s_mov_b32 m0, s62
	v_lshl_add_u64 v[226:227], s[50:51], 0, v[162:163]
	v_lshl_add_u64 v[226:227], v[226:227], 0, s[26:27]
	global_load_lds_dwordx4 v[226:227], off
	s_waitcnt vmcnt(8)
	s_waitcnt lgkmcnt(0)
	s_barrier
	s_setprio 1
	s_waitcnt lgkmcnt(0)
	v_mfma_i32_16x16x64_i8 v[62:65], v[130:133], v[194:197], v[62:65]
	v_mfma_i32_16x16x64_i8 v[58:61], v[138:141], v[194:197], v[58:61]
	v_mfma_i32_16x16x64_i8 v[46:49], v[130:133], v[202:205], v[46:49]
	v_mfma_i32_16x16x64_i8 v[42:45], v[138:141], v[202:205], v[42:45]
	v_mfma_i32_16x16x64_i8 v[30:33], v[130:133], v[210:213], v[30:33]
	v_mfma_i32_16x16x64_i8 v[26:29], v[138:141], v[210:213], v[26:29]
	v_mfma_i32_16x16x64_i8 v[14:17], v[130:133], v[218:221], v[14:17]
	v_mfma_i32_16x16x64_i8 v[10:13], v[138:141], v[218:221], v[10:13]
	v_mfma_i32_16x16x64_i8 v[62:65], v[134:137], v[198:201], v[62:65]
	v_mfma_i32_16x16x64_i8 v[58:61], v[142:145], v[198:201], v[58:61]
	v_mfma_i32_16x16x64_i8 v[46:49], v[134:137], v[206:209], v[46:49]
	v_mfma_i32_16x16x64_i8 v[42:45], v[142:145], v[206:209], v[42:45]
	v_mfma_i32_16x16x64_i8 v[30:33], v[134:137], v[214:217], v[30:33]
	v_mfma_i32_16x16x64_i8 v[26:29], v[142:145], v[214:217], v[26:29]
	v_mfma_i32_16x16x64_i8 v[14:17], v[134:137], v[222:225], v[14:17]
	v_mfma_i32_16x16x64_i8 v[10:13], v[142:145], v[222:225], v[10:13]
	v_mfma_i32_16x16x64_i8 v[54:57], v[146:149], v[194:197], v[54:57]
	v_mfma_i32_16x16x64_i8 v[50:53], v[154:157], v[194:197], v[50:53]
	v_mfma_i32_16x16x64_i8 v[38:41], v[146:149], v[202:205], v[38:41]
	v_mfma_i32_16x16x64_i8 v[34:37], v[154:157], v[202:205], v[34:37]
	v_mfma_i32_16x16x64_i8 v[22:25], v[146:149], v[210:213], v[22:25]
	v_mfma_i32_16x16x64_i8 v[18:21], v[154:157], v[210:213], v[18:21]
	v_mfma_i32_16x16x64_i8 v[6:9], v[146:149], v[218:221], v[6:9]
	v_mfma_i32_16x16x64_i8 v[2:5], v[154:157], v[218:221], v[2:5]
	v_mfma_i32_16x16x64_i8 v[54:57], v[150:153], v[198:201], v[54:57]
	v_mfma_i32_16x16x64_i8 v[50:53], v[158:161], v[198:201], v[50:53]
	v_mfma_i32_16x16x64_i8 v[38:41], v[150:153], v[206:209], v[38:41]
	v_mfma_i32_16x16x64_i8 v[34:37], v[158:161], v[206:209], v[34:37]
	v_mfma_i32_16x16x64_i8 v[22:25], v[150:153], v[214:217], v[22:25]
	v_mfma_i32_16x16x64_i8 v[18:21], v[158:161], v[214:217], v[18:21]
	v_mfma_i32_16x16x64_i8 v[6:9], v[150:153], v[222:225], v[6:9]
	v_mfma_i32_16x16x64_i8 v[2:5], v[158:161], v[222:225], v[2:5]
	s_setprio 0
	s_barrier
	s_add_i32 s43, s43, 2
	s_cmp_gt_u32 s43, 13
	s_cbranch_scc1 .LBB0_2551
	s_mov_b64 s[46:47], s[48:49]
	s_branch .LBB0_2547

; #define PG8_STAGE(bufoff, gbase, voff) do { _Pragma("unroll") for (int _i = 0; _i < 2; ++_i) { unsigned vo_ = (voff)[_i]; asm volatile("" : "+v"(vo_));   \
;         __builtin_amdgcn_global_load_lds((const unsigned*)((const char*)(gbase) + vo_), (LAS unsigned*)(lds + (bufoff) + ldsw + _i * 8192), 16, 0, 0); } } while (0)
; #define PG8_LDA(dst, b, h) do { _Pragma("unroll") for (int m = 0; m < 4; ++m) _Pragma("unroll") for (int k = 0; k < 2; ++k) dst[m][k] = *(const LAS bf16x8*)(lds + PG8_SA(b, h) + aoff + m * 2048 + k * 1024); } while (0)
; #define PG8_LDB(dst, b, h) do { _Pragma("unroll") for (int n = 0; n < 2; ++n) _Pragma("unroll") for (int k = 0; k < 2; ++k) dst[n][k] = *(const LAS bf16x8*)(lds + PG8_SB(b, h) + boff + n * 2048 + k * 1024); } while (0)
; #define PG8_WAIT_V(n) asm volatile("s_waitcnt vmcnt(" #n ")" ::: "memory")
; #define PG8_WAIT_L(n) asm volatile("s_waitcnt lgkmcnt(" #n ")" ::: "memory")
; #define PG8_BAR __builtin_amdgcn_s_barrier()
; #define PG8_SCHED __builtin_amdgcn_sched_barrier(0)
;     ...
;         for (int t = 0; t < nt; t += 2) {
;             const bool last = (t == nt - 2);
;             const char* a1 = Abase + (size_t)(t + 1) * kstep;
;             const char* a2 = Abase + (last ? (size_t)0 : (size_t)(t + 2) * kstep); const char* b2 = last ? nB : cB + (size_t)(t + 2) * kstep;
;             const char* a3 = a2 + kstep; const char* b3 = b2 + kstep;
;             PG8_LDB(B0, 0, 0); PG8_LDB(B1, 0, 1); PG8_SCHED; PG8_LDA(At, 0, 0); PG8_STAGE(PG8_SA(1, 1), a1, va[1]);
;             PG8_WAIT_V(8); PG8_WAIT_L(0); PG8_BAR; PG8_MMA(0, 0, At, B0); PG8_MMA(0, 1, At, B1); PG8_BAR; PG8_SCHED;
;             if (last && has_next) { PG8_AOFFS(va, nxt); }
;             PG8_LDA(At, 0, 1); PG8_STAGE(PG8_SB(0, 0), b2, voffB); PG8_STAGE(PG8_SB(0, 1), b2 + hstepB, voffB); PG8_STAGE(PG8_SA(0, 0), a2, va[0]);
;             PG8_WAIT_V(8); PG8_WAIT_L(0); PG8_BAR; PG8_MMA(1, 0, At, B0); PG8_MMA(1, 1, At, B1); PG8_BAR; PG8_SCHED;
;             PG8_LDB(B0, 1, 0); PG8_LDB(B1, 1, 1); PG8_SCHED; PG8_LDA(At, 1, 0); PG8_STAGE(PG8_SA(0, 1), a2, va[1]);
;             PG8_WAIT_V(8); PG8_WAIT_L(0); PG8_BAR; PG8_MMA(0, 0, At, B0); PG8_MMA(0, 1, At, B1); PG8_BAR; PG8_SCHED;
.LBB0_2638:
	ds_read_b128 v[18:21], v214
	ds_read_b128 v[22:25], v214 offset:1024
	ds_read_b128 v[26:29], v214 offset:2048
	ds_read_b128 v[30:33], v214 offset:3072
	ds_read_b128 v[2:5], v215
	ds_read_b128 v[6:9], v215 offset:1024
	ds_read_b128 v[10:13], v215 offset:2048
	ds_read_b128 v[14:17], v215 offset:3072
	s_cmp_eq_u32 s89, 52
	s_cselect_b64 s[6:7], -1, 0
	v_mov_b32_e32 v194, v208
	s_add_u32 s56, s24, s54
	s_mov_b32 m0, s79
	ds_read_b128 v[58:61], v216
	ds_read_b128 v[62:65], v216 offset:1024
	ds_read_b128 v[50:53], v216 offset:2048
	ds_read_b128 v[54:57], v216 offset:3072
	ds_read_b128 v[42:45], v216 offset:4096
	ds_read_b128 v[46:49], v216 offset:5120
	ds_read_b128 v[34:37], v216 offset:6144
	ds_read_b128 v[38:41], v216 offset:7168
	s_addc_u32 s57, s25, s55
	global_load_lds_dwordx4 v194, s[56:57]
	v_mov_b32_e32 v194, v209
	s_mov_b32 m0, s80
	s_nop 0
	global_load_lds_dwordx4 v194, s[56:57]
	s_waitcnt vmcnt(8)
	s_waitcnt lgkmcnt(0)
	s_barrier
	s_setprio 1
	s_waitcnt lgkmcnt(0)
	v_mfma_scale_f32_16x16x128_f8f6f4 v[242:245], v[2:9], v[58:65], v[166:169], v217, v217 op_sel_hi:[0,0,0]
	v_mfma_scale_f32_16x16x128_f8f6f4 v[190:193], v[18:25], v[58:65], v[190:193], v217, v217 op_sel_hi:[0,0,0]
	v_mfma_scale_f32_16x16x128_f8f6f4 v[186:189], v[26:33], v[58:65], v[186:189], v217, v217 op_sel_hi:[0,0,0]
	v_mfma_scale_f32_16x16x128_f8f6f4 v[246:249], v[10:17], v[58:65], v[162:165], v217, v217 op_sel_hi:[0,0,0]
	v_mfma_scale_f32_16x16x128_f8f6f4 v[182:185], v[18:25], v[50:57], v[182:185], v217, v217 op_sel_hi:[0,0,0]
	v_mfma_scale_f32_16x16x128_f8f6f4 v[178:181], v[26:33], v[50:57], v[178:181], v217, v217 op_sel_hi:[0,0,0]
	v_mfma_scale_f32_16x16x128_f8f6f4 v[150:153], v[2:9], v[50:57], v[150:153], v217, v217 op_sel_hi:[0,0,0]
	v_mfma_scale_f32_16x16x128_f8f6f4 v[146:149], v[10:17], v[50:57], v[146:149], v217, v217 op_sel_hi:[0,0,0]
	v_mfma_scale_f32_16x16x128_f8f6f4 v[174:177], v[18:25], v[42:49], v[174:177], v217, v217 op_sel_hi:[0,0,0]
	v_mfma_scale_f32_16x16x128_f8f6f4 v[170:173], v[26:33], v[42:49], v[170:173], v217, v217 op_sel_hi:[0,0,0]
	v_mfma_scale_f32_16x16x128_f8f6f4 v[142:145], v[2:9], v[42:49], v[142:145], v217, v217 op_sel_hi:[0,0,0]
	v_mfma_scale_f32_16x16x128_f8f6f4 v[138:141], v[10:17], v[42:49], v[138:141], v217, v217 op_sel_hi:[0,0,0]
	v_mfma_scale_f32_16x16x128_f8f6f4 v[158:161], v[18:25], v[34:41], v[158:161], v217, v217 op_sel_hi:[0,0,0]
	v_mfma_scale_f32_16x16x128_f8f6f4 v[154:157], v[26:33], v[34:41], v[154:157], v217, v217 op_sel_hi:[0,0,0]
	v_mfma_scale_f32_16x16x128_f8f6f4 v[126:129], v[2:9], v[34:41], v[126:129], v217, v217 op_sel_hi:[0,0,0]
	v_mfma_scale_f32_16x16x128_f8f6f4 v[122:125], v[10:17], v[34:41], v[122:125], v217, v217 op_sel_hi:[0,0,0]
	s_setprio 0
	s_barrier
	s_and_b64 s[56:57], s[4:5], s[6:7]
	s_andn2_b64 vcc, exec, s[56:57]
	s_cbranch_vccnz .LBB0_2640
	v_mov_b32_e32 v209, v224
	v_mov_b32_e32 v208, v223
	v_mov_b32_e32 v207, v222
	v_mov_b32_e32 v206, v221
.LBB0_2640:
	s_add_u32 s56, s54, 0x100
	s_waitcnt lgkmcnt(0)
	s_addc_u32 s57, s55, 0
	v_mov_b32_e32 v194, v203
	s_mov_b32 m0, s61
	s_and_b64 s[58:59], s[6:7], exec
	s_cselect_b32 s58, 0, s56
	v_lshl_add_u64 v[166:167], v[198:199], 0, s[54:55]
	v_cndmask_b32_e64 v201, v167, v197, s[6:7]
	v_cndmask_b32_e64 v200, v166, v196, s[6:7]
	s_cselect_b32 s59, 0, s57
	s_add_u32 s58, s14, s58
	s_addc_u32 s59, s15, s59
	v_readfirstlane_b32 s6, v200
	v_readfirstlane_b32 s7, v201
	ds_read_b128 v[58:61], v216 offset:16384
	ds_read_b128 v[62:65], v216 offset:17408
	ds_read_b128 v[162:165], v216 offset:18432
	ds_read_b128 v[166:169], v216 offset:19456
	ds_read_b128 v[226:229], v216 offset:20480
	ds_read_b128 v[230:233], v216 offset:21504
	ds_read_b128 v[234:237], v216 offset:22528
	ds_read_b128 v[238:241], v216 offset:23552
	s_nop 0
	global_load_lds_dwordx4 v194, s[6:7]
	v_mov_b32_e32 v194, v205
	s_mov_b32 m0, s62
	s_nop 0
	global_load_lds_dwordx4 v194, s[6:7]
	s_mov_b32 m0, s63
	v_lshl_add_u64 v[50:51], v[200:201], 0, s[16:17]
	v_mov_b32_e32 v52, v203
	v_readfirstlane_b32 s6, v50
	v_readfirstlane_b32 s7, v51
	v_mov_b32_e32 v50, v205
	s_nop 3
	global_load_lds_dwordx4 v52, s[6:7]
	s_mov_b32 m0, s64
	s_nop 0
	global_load_lds_dwordx4 v50, s[6:7]
	s_mov_b32 m0, s60
	v_mov_b32_e32 v42, v206
	s_nop 0
	global_load_lds_dwordx4 v42, s[58:59]
	v_mov_b32_e32 v42, v207
	s_mov_b32 m0, s65
	s_nop 0
	global_load_lds_dwordx4 v42, s[58:59]
	s_waitcnt vmcnt(8)
	s_waitcnt lgkmcnt(0)
	s_barrier
	s_setprio 1
	s_waitcnt lgkmcnt(0)
	v_mfma_scale_f32_16x16x128_f8f6f4 v[134:137], v[18:25], v[58:65], v[134:137], v217, v217 op_sel_hi:[0,0,0]
	v_mfma_scale_f32_16x16x128_f8f6f4 v[130:133], v[26:33], v[58:65], v[130:133], v217, v217 op_sel_hi:[0,0,0]
	v_mfma_scale_f32_16x16x128_f8f6f4 v[114:117], v[18:25], v[162:169], v[114:117], v217, v217 op_sel_hi:[0,0,0]
	v_mfma_scale_f32_16x16x128_f8f6f4 v[106:109], v[26:33], v[162:169], v[106:109], v217, v217 op_sel_hi:[0,0,0]
	v_mfma_scale_f32_16x16x128_f8f6f4 v[98:101], v[18:25], v[226:233], v[98:101], v217, v217 op_sel_hi:[0,0,0]
	v_mfma_scale_f32_16x16x128_f8f6f4 v[90:93], v[26:33], v[226:233], v[90:93], v217, v217 op_sel_hi:[0,0,0]
	v_mfma_scale_f32_16x16x128_f8f6f4 v[82:85], v[18:25], v[234:241], v[82:85], v217, v217 op_sel_hi:[0,0,0]
	v_mfma_scale_f32_16x16x128_f8f6f4 v[74:77], v[26:33], v[234:241], v[74:77], v217, v217 op_sel_hi:[0,0,0]
	v_mfma_scale_f32_16x16x128_f8f6f4 v[118:121], v[2:9], v[58:65], v[118:121], v217, v217 op_sel_hi:[0,0,0]
	v_mfma_scale_f32_16x16x128_f8f6f4 v[110:113], v[10:17], v[58:65], v[110:113], v217, v217 op_sel_hi:[0,0,0]
	v_mfma_scale_f32_16x16x128_f8f6f4 v[102:105], v[2:9], v[162:169], v[102:105], v217, v217 op_sel_hi:[0,0,0]
	v_mfma_scale_f32_16x16x128_f8f6f4 v[94:97], v[10:17], v[162:169], v[94:97], v217, v217 op_sel_hi:[0,0,0]
	v_mfma_scale_f32_16x16x128_f8f6f4 v[86:89], v[2:9], v[226:233], v[86:89], v217, v217 op_sel_hi:[0,0,0]
	v_mfma_scale_f32_16x16x128_f8f6f4 v[78:81], v[10:17], v[226:233], v[78:81], v217, v217 op_sel_hi:[0,0,0]
	v_mfma_scale_f32_16x16x128_f8f6f4 v[70:73], v[2:9], v[234:241], v[70:73], v217, v217 op_sel_hi:[0,0,0]
	v_mfma_scale_f32_16x16x128_f8f6f4 v[66:69], v[10:17], v[234:241], v[66:69], v217, v217 op_sel_hi:[0,0,0]
	s_setprio 0
	s_barrier
; #define PG8_STAGE(bufoff, gbase, voff) do { _Pragma("unroll") for (int _i = 0; _i < 2; ++_i) { unsigned vo_ = (voff)[_i]; asm volatile("" : "+v"(vo_));   \
;         __builtin_amdgcn_global_load_lds((const unsigned*)((const char*)(gbase) + vo_), (LAS unsigned*)(lds + (bufoff) + ldsw + _i * 8192), 16, 0, 0); } } while (0)
; #define PG8_LDA(dst, b, h) do { _Pragma("unroll") for (int m = 0; m < 4; ++m) _Pragma("unroll") for (int k = 0; k < 2; ++k) dst[m][k] = *(const LAS bf16x8*)(lds + PG8_SA(b, h) + aoff + m * 2048 + k * 1024); } while (0)
; #define PG8_LDB(dst, b, h) do { _Pragma("unroll") for (int n = 0; n < 2; ++n) _Pragma("unroll") for (int k = 0; k < 2; ++k) dst[n][k] = *(const LAS bf16x8*)(lds + PG8_SB(b, h) + boff + n * 2048 + k * 1024); } while (0)
; #define PG8_WAIT_V(n) asm volatile("s_waitcnt vmcnt(" #n ")" ::: "memory")
; #define PG8_WAIT_L(n) asm volatile("s_waitcnt lgkmcnt(" #n ")" ::: "memory")
; #define PG8_BAR __builtin_amdgcn_s_barrier()
; #define PG8_SCHED __builtin_amdgcn_sched_barrier(0)
;     ...
;             PG8_LDB(B0, 1, 0); PG8_LDB(B1, 1, 1); PG8_SCHED; PG8_LDA(At, 1, 0); PG8_STAGE(PG8_SA(0, 1), a2, va[1]);
;             PG8_WAIT_V(8); PG8_WAIT_L(0); PG8_BAR; PG8_MMA(0, 0, At, B0); PG8_MMA(0, 1, At, B1); PG8_BAR; PG8_SCHED;
;             PG8_LDA(At, 1, 1); PG8_STAGE(PG8_SB(1, 0), b3, voffB); PG8_STAGE(PG8_SB(1, 1), b3 + hstepB, voffB); PG8_STAGE(PG8_SA(1, 0), a3, va[0]);
;             PG8_WAIT_V(8); PG8_WAIT_L(0); PG8_BAR; PG8_MMA(1, 0, At, B0); PG8_MMA(1, 1, At, B1); PG8_BAR; PG8_SCHED;
;         }
	s_add_i32 s6, 0, 0x18000
	s_add_i32 s7, 0, 0x1c000
	v_add_u32_e32 v14, s6, v211
	v_add_u32_e32 v30, s7, v211
	ds_read_b128 v[2:5], v14
	ds_read_b128 v[6:9], v14 offset:1024
	ds_read_b128 v[10:13], v14 offset:2048
	ds_read_b128 v[14:17], v14 offset:3072
	ds_read_b128 v[18:21], v30
	ds_read_b128 v[22:25], v30 offset:1024
	ds_read_b128 v[26:29], v30 offset:2048
	ds_read_b128 v[30:33], v30 offset:3072
	v_mov_b32_e32 v162, v208
	s_mov_b32 m0, s66
	ds_read_b128 v[34:37], v216 offset:32768
	ds_read_b128 v[38:41], v216 offset:33792
	ds_read_b128 v[42:45], v216 offset:34816
	ds_read_b128 v[46:49], v216 offset:35840
	ds_read_b128 v[50:53], v216 offset:36864
	ds_read_b128 v[54:57], v216 offset:37888
	ds_read_b128 v[58:61], v216 offset:38912
	ds_read_b128 v[62:65], v216 offset:39936
	s_nop 0
	global_load_lds_dwordx4 v162, s[58:59]
	v_mov_b32_e32 v162, v209
	s_mov_b32 m0, s67
	s_nop 0
	global_load_lds_dwordx4 v162, s[58:59]
	s_waitcnt vmcnt(8)
	s_waitcnt lgkmcnt(0)
	s_barrier
	s_setprio 1
	s_waitcnt lgkmcnt(0)
	v_mfma_scale_f32_16x16x128_f8f6f4 v[190:193], v[2:9], v[34:41], v[190:193], v217, v217 op_sel_hi:[0,0,0]
	v_mfma_scale_f32_16x16x128_f8f6f4 v[186:189], v[10:17], v[34:41], v[186:189], v217, v217 op_sel_hi:[0,0,0]
	v_mfma_scale_f32_16x16x128_f8f6f4 v[182:185], v[2:9], v[42:49], v[182:185], v217, v217 op_sel_hi:[0,0,0]
	v_mfma_scale_f32_16x16x128_f8f6f4 v[178:181], v[10:17], v[42:49], v[178:181], v217, v217 op_sel_hi:[0,0,0]
	v_mfma_scale_f32_16x16x128_f8f6f4 v[174:177], v[2:9], v[50:57], v[174:177], v217, v217 op_sel_hi:[0,0,0]
	v_mfma_scale_f32_16x16x128_f8f6f4 v[170:173], v[10:17], v[50:57], v[170:173], v217, v217 op_sel_hi:[0,0,0]
	v_mfma_scale_f32_16x16x128_f8f6f4 v[158:161], v[2:9], v[58:65], v[158:161], v217, v217 op_sel_hi:[0,0,0]
	v_mfma_scale_f32_16x16x128_f8f6f4 v[154:157], v[10:17], v[58:65], v[154:157], v217, v217 op_sel_hi:[0,0,0]
	v_mfma_scale_f32_16x16x128_f8f6f4 v[166:169], v[18:25], v[34:41], v[242:245], v217, v217 op_sel_hi:[0,0,0]
	v_mfma_scale_f32_16x16x128_f8f6f4 v[162:165], v[26:33], v[34:41], v[246:249], v217, v217 op_sel_hi:[0,0,0]
	v_mfma_scale_f32_16x16x128_f8f6f4 v[150:153], v[18:25], v[42:49], v[150:153], v217, v217 op_sel_hi:[0,0,0]
	v_mfma_scale_f32_16x16x128_f8f6f4 v[146:149], v[26:33], v[42:49], v[146:149], v217, v217 op_sel_hi:[0,0,0]
	v_mfma_scale_f32_16x16x128_f8f6f4 v[142:145], v[18:25], v[50:57], v[142:145], v217, v217 op_sel_hi:[0,0,0]
	v_mfma_scale_f32_16x16x128_f8f6f4 v[138:141], v[26:33], v[50:57], v[138:141], v217, v217 op_sel_hi:[0,0,0]
	v_mfma_scale_f32_16x16x128_f8f6f4 v[126:129], v[18:25], v[58:65], v[126:129], v217, v217 op_sel_hi:[0,0,0]
	v_mfma_scale_f32_16x16x128_f8f6f4 v[122:125], v[26:33], v[58:65], v[122:125], v217, v217 op_sel_hi:[0,0,0]
	s_setprio 0
	s_barrier
	v_mov_b32_e32 v194, v203
	ds_read_b128 v[34:37], v216 offset:49152
	ds_read_b128 v[38:41], v216 offset:50176
	ds_read_b128 v[42:45], v216 offset:51200
	ds_read_b128 v[46:49], v216 offset:52224
	ds_read_b128 v[50:53], v216 offset:53248
	ds_read_b128 v[54:57], v216 offset:54272
	ds_read_b128 v[58:61], v216 offset:55296
	ds_read_b128 v[62:65], v216 offset:56320
	s_add_i32 s6, s6, s35
	v_lshl_add_u64 v[226:227], v[200:201], 0, v[194:195]
	v_lshl_add_u64 v[226:227], v[226:227], 0, s[22:23]
	s_mov_b32 m0, s6
	v_mov_b32_e32 v194, v205
	global_load_lds_dwordx4 v[226:227], off
	s_add_i32 m0, s6, 0x2000
	v_lshl_add_u64 v[226:227], v[200:201], 0, v[194:195]
	v_lshl_add_u64 v[226:227], v[226:227], 0, s[22:23]
	v_lshl_add_u64 v[200:201], v[200:201], 0, s[26:27]
	v_mov_b32_e32 v194, v203
	s_add_i32 s54, s7, s35
	global_load_lds_dwordx4 v[226:227], off
	v_readfirstlane_b32 s6, v200
	v_readfirstlane_b32 s7, v201
	s_mov_b32 m0, s54
	s_nop 3
	global_load_lds_dwordx4 v194, s[6:7]
	v_mov_b32_e32 v194, v205
	s_add_i32 m0, s54, 0x2000
	s_nop 0
	global_load_lds_dwordx4 v194, s[6:7]
	v_mov_b32_e32 v194, v206
	s_mov_b32 m0, s70
	v_lshl_add_u64 v[200:201], s[58:59], 0, v[194:195]
	v_lshl_add_u64 v[200:201], v[200:201], 0, s[22:23]
	v_mov_b32_e32 v194, v207
	global_load_lds_dwordx4 v[200:201], off
	s_mov_b32 m0, s71
	v_lshl_add_u64 v[200:201], s[58:59], 0, v[194:195]
	v_lshl_add_u64 v[200:201], v[200:201], 0, s[22:23]
	global_load_lds_dwordx4 v[200:201], off
	s_waitcnt vmcnt(8)
	s_waitcnt lgkmcnt(0)
	s_barrier
	s_setprio 1
	s_waitcnt lgkmcnt(0)
	v_mfma_scale_f32_16x16x128_f8f6f4 v[134:137], v[2:9], v[34:41], v[134:137], v217, v217 op_sel_hi:[0,0,0]
	v_mfma_scale_f32_16x16x128_f8f6f4 v[130:133], v[10:17], v[34:41], v[130:133], v217, v217 op_sel_hi:[0,0,0]
	v_mfma_scale_f32_16x16x128_f8f6f4 v[114:117], v[2:9], v[42:49], v[114:117], v217, v217 op_sel_hi:[0,0,0]
	v_mfma_scale_f32_16x16x128_f8f6f4 v[106:109], v[10:17], v[42:49], v[106:109], v217, v217 op_sel_hi:[0,0,0]
	v_mfma_scale_f32_16x16x128_f8f6f4 v[98:101], v[2:9], v[50:57], v[98:101], v217, v217 op_sel_hi:[0,0,0]
	v_mfma_scale_f32_16x16x128_f8f6f4 v[90:93], v[10:17], v[50:57], v[90:93], v217, v217 op_sel_hi:[0,0,0]
	v_mfma_scale_f32_16x16x128_f8f6f4 v[82:85], v[2:9], v[58:65], v[82:85], v217, v217 op_sel_hi:[0,0,0]
	v_mfma_scale_f32_16x16x128_f8f6f4 v[74:77], v[10:17], v[58:65], v[74:77], v217, v217 op_sel_hi:[0,0,0]
	v_mfma_scale_f32_16x16x128_f8f6f4 v[118:121], v[18:25], v[34:41], v[118:121], v217, v217 op_sel_hi:[0,0,0]
	v_mfma_scale_f32_16x16x128_f8f6f4 v[110:113], v[26:33], v[34:41], v[110:113], v217, v217 op_sel_hi:[0,0,0]
	v_mfma_scale_f32_16x16x128_f8f6f4 v[102:105], v[18:25], v[42:49], v[102:105], v217, v217 op_sel_hi:[0,0,0]
	v_mfma_scale_f32_16x16x128_f8f6f4 v[94:97], v[26:33], v[42:49], v[94:97], v217, v217 op_sel_hi:[0,0,0]
	v_mfma_scale_f32_16x16x128_f8f6f4 v[86:89], v[18:25], v[50:57], v[86:89], v217, v217 op_sel_hi:[0,0,0]
	v_mfma_scale_f32_16x16x128_f8f6f4 v[78:81], v[26:33], v[50:57], v[78:81], v217, v217 op_sel_hi:[0,0,0]
	v_mfma_scale_f32_16x16x128_f8f6f4 v[70:73], v[18:25], v[58:65], v[70:73], v217, v217 op_sel_hi:[0,0,0]
	v_mfma_scale_f32_16x16x128_f8f6f4 v[66:69], v[26:33], v[58:65], v[66:69], v217, v217 op_sel_hi:[0,0,0]
	s_setprio 0
	s_barrier
	s_add_i32 s89, s89, 2
	s_cmp_gt_u32 s89, 53
	s_cbranch_scc1 .LBB0_2642
	s_mov_b64 s[54:55], s[56:57]
	s_branch .LBB0_2638
